# as the previous version but the RWKV workgroups convert 10 (not 8) rows per wave of the layer-0 u table
# speedup vs baseline: 1.0121x; 1.0006x over previous
; __device__ __forceinline__ void peer_row_load(f32x4 (&v)[16], const float* const (&in)[34], int it, int layer, int lane) {
;     const int tbl = it >= NEXP, r = it - tbl * NEXP + layer * NEXP;
;     const f32x4* src = (const f32x4*)((tbl ? in[33] : in[32]) + (size_t)r * D) + lane;
; #pragma unroll
;     for (int j = 0; j < 16; ++j) v[j] = src[64 * j];
;     f32x4 va[16], vb[16];
;     if (it_lo + gw >= it_hi) return;
;     peer_row_load(va, in, it_lo + gw, only_layer, lane);
; #pragma unroll 1
;     for (int it = it_lo + gw; it < it_hi; it += 2 * NGW) {
;         const int it1 = it + NGW, it2 = it + 2 * NGW;
;         peer_row_load(vb, in, it1 < it_hi ? it1 : it, only_layer, lane);
.LBB0_618:
	v_mov_b32_e32 v1, v0
	s_nop 0
	v_readfirstlane_b32 s0, v1
	s_ashr_i32 s16, s0, 6
	s_lshl_b32 s0, s35, 3
	s_add_i32 s4, s16, s0
	v_and_b32_e32 v134, 63, v1
	s_cmpk_gt_i32 s4, 0x17ff
	v_lshlrev_b32_e32 v136, 2, v134
	v_cmp_eq_u32_e64 s[0:1], 0, v134
	s_cbranch_scc1 .LBB0_627
	s_ashr_i32 s5, s4, 31
	s_lshl_b64 s[6:7], s[4:5], 14
	s_add_u32 s6, s84, s6
	s_addc_u32 s7, s85, s7
	v_mov_b32_e32 v131, 0
	v_lshlrev_b32_e32 v130, 4, v134
	v_lshl_add_u64 v[2:3], s[6:7], 0, v[130:131]
	v_add_co_u32_e32 v4, vcc, 0x1000, v2
	global_load_dwordx4 v[86:89], v130, s[6:7]
	global_load_dwordx4 v[62:65], v130, s[6:7] offset:1024
	global_load_dwordx4 v[50:53], v130, s[6:7] offset:2048
	global_load_dwordx4 v[54:57], v130, s[6:7] offset:3072
	v_addc_co_u32_e32 v5, vcc, 0, v3, vcc
	global_load_dwordx4 v[46:49], v[4:5], off
	global_load_dwordx4 v[42:45], v[4:5], off offset:1024
	global_load_dwordx4 v[38:41], v[4:5], off offset:2048
	global_load_dwordx4 v[34:37], v[4:5], off offset:3072
	v_add_co_u32_e32 v4, vcc, 0x2000, v2
	v_mov_b32_e32 v137, v131
	s_nop 0
	v_addc_co_u32_e32 v5, vcc, 0, v3, vcc
	v_add_co_u32_e32 v2, vcc, 0x3000, v2
	global_load_dwordx4 v[30:33], v[4:5], off
	global_load_dwordx4 v[26:29], v[4:5], off offset:1024
	global_load_dwordx4 v[22:25], v[4:5], off offset:2048
	global_load_dwordx4 v[14:17], v[4:5], off offset:3072
	v_addc_co_u32_e32 v3, vcc, 0, v3, vcc
	global_load_dwordx4 v[18:21], v[2:3], off
	global_load_dwordx4 v[10:13], v[2:3], off offset:1024
	global_load_dwordx4 v[6:9], v[2:3], off offset:2048
	s_nop 0
	global_load_dwordx4 v[2:5], v[2:3], off offset:3072
	v_lshl_add_u64 v[58:59], s[90:91], 0, v[136:137]
	s_mov_b64 s[6:7], 0xba00000
	s_add_u32 s17, s90, 0x1ba00000
	v_lshl_add_u64 v[132:133], v[58:59], 0, s[6:7]
	s_addc_u32 s18, s91, 0
	s_lshl_b32 s6, s2, 3
	s_lshl_b32 s29, s34, 4
	s_lshl_b32 s30, s34, 3
	s_movk_i32 s5, 0x1000
	s_movk_i32 s14, 0x2000
	s_movk_i32 s15, 0x3000
	s_add_i32 s19, s16, s6
	s_add_i32 s28, s29, 0xfffff800
	s_addk_i32 s29, 0xf400
	s_addk_i32 s30, 0xf800
	s_mov_b32 s31, 0x43800000
	s_branch .LBB0_622

; __device__ __forceinline__ void peer_row_load(f32x4 (&v)[16], const float* const (&in)[34], int it, int layer, int lane) {
;     const int tbl = it >= NEXP, r = it - tbl * NEXP + layer * NEXP;
;     const f32x4* src = (const f32x4*)((tbl ? in[33] : in[32]) + (size_t)r * D) + lane;
; #pragma unroll
;     for (int j = 0; j < 16; ++j) v[j] = src[64 * j];
; }
; __device__ __forceinline__ void peer_row_store(const f32x4 (&v)[16], unsigned char* ws, int it, int layer, int lane) {
;     const int tbl = it >= NEXP, r = it - tbl * NEXP + layer * NEXP;
;     float am = 0.f;
; #pragma unroll
;     for (int j = 0; j < 16; ++j) am = fmaxf(fmaxf(am, fmaxf(fabsf(v[j][0]), fabsf(v[j][1]))), fmaxf(fabsf(v[j][2]), fabsf(v[j][3])));
;     am = __uint_as_float(max64u(__float_as_uint(am)));
;     ...
;     for (int it = it_lo + gw; it < it_hi; it += 2 * NGW) {
;         const int it1 = it + NGW, it2 = it + 2 * NGW;
;         peer_row_load(vb, in, it1 < it_hi ? it1 : it, only_layer, lane);
.LBB0_621:
	s_add_i32 s19, s19, s28
	s_add_i32 s6, s19, 0xfffffc00
	s_cmpk_lt_i32 s6, 0x1800
	s_cbranch_scc0 .LBB0_627
.LBB0_622:
	s_add_i32 s10, s19, 0xfffffc00
	s_add_i32 s6, s30, s19
	s_cmpk_lt_i32 s6, 0x1800
	s_cselect_b64 s[8:9], -1, 0
	s_and_b64 s[12:13], s[8:9], exec
	s_cselect_b32 s7, s6, s10
	s_cmpk_gt_i32 s7, 0x3fff
	s_cselect_b32 s11, 0xffffc000, 0
	s_cselect_b32 s20, s86, s84
	s_cselect_b32 s21, s87, s85
	s_add_i32 s12, s11, s7
	s_ashr_i32 s13, s12, 31
	s_lshl_b64 s[12:13], s[12:13], 14
	s_add_u32 s12, s20, s12
	s_addc_u32 s13, s21, s13
	v_lshlrev_b32_e32 v130, 4, v134
	s_waitcnt vmcnt(32)
	v_lshl_add_u64 v[58:59], s[12:13], 0, v[130:131]
	v_add_co_u32_e32 v60, vcc, s5, v58
	global_load_dwordx4 v[122:125], v130, s[12:13] offset:1024
	global_load_dwordx4 v[118:121], v130, s[12:13] offset:2048
	v_addc_co_u32_e32 v61, vcc, 0, v59, vcc
	v_add_co_u32_e32 v66, vcc, s14, v58
	s_nop 1
	v_addc_co_u32_e32 v67, vcc, 0, v59, vcc
	global_load_dwordx4 v[114:117], v130, s[12:13] offset:3072
	global_load_dwordx4 v[110:113], v[66:67], off offset:-4096
	global_load_dwordx4 v[106:109], v[60:61], off offset:1024
	global_load_dwordx4 v[102:105], v[60:61], off offset:2048
	global_load_dwordx4 v[94:97], v[66:67], off
	global_load_dwordx4 v[90:93], v[66:67], off offset:1024
	global_load_dwordx4 v[82:85], v[66:67], off offset:2048
	global_load_dwordx4 v[78:81], v[66:67], off offset:3072
	v_add_co_u32_e32 v58, vcc, s15, v58
	s_nop 1
	v_addc_co_u32_e32 v59, vcc, 0, v59, vcc
	global_load_dwordx4 v[98:101], v[60:61], off offset:3072
	global_load_dwordx4 v[74:77], v[58:59], off
	global_load_dwordx4 v[70:73], v[58:59], off offset:1024
	global_load_dwordx4 v[66:69], v[58:59], off offset:2048
	global_load_dwordx4 v[126:129], v130, s[12:13]
	s_nop 0
	global_load_dwordx4 v[58:61], v[58:59], off offset:3072
	s_waitcnt vmcnt(17)
	v_max_f32_e64 v135, |v87|, |v87|
	v_max_f32_e64 v137, |v86|, |v86|
	v_max_f32_e32 v135, v137, v135
	v_max_f32_e64 v137, |v89|, |v89|
	v_max_f32_e64 v138, |v88|, |v88|
	v_max_f32_e32 v137, v138, v137
	v_max3_f32 v135, v135, 0, v137
	s_waitcnt vmcnt(30)
	v_max_f32_e64 v137, |v63|, |v63|
	v_max_f32_e64 v138, |v62|, |v62|
	v_max_f32_e32 v137, v138, v137
	v_max_f32_e64 v138, |v65|, |v65|
	v_max_f32_e64 v139, |v64|, |v64|
	v_max_f32_e32 v138, v139, v138
	v_max3_f32 v135, v135, v137, v138
	s_waitcnt vmcnt(29)
	v_max_f32_e64 v137, |v51|, |v51|
	v_max_f32_e64 v138, |v50|, |v50|
	v_max_f32_e32 v137, v138, v137
	v_max_f32_e64 v138, |v53|, |v53|
	v_max_f32_e64 v139, |v52|, |v52|
	v_max_f32_e32 v138, v139, v138
	v_max3_f32 v135, v135, v137, v138
	s_waitcnt vmcnt(28)
	v_max_f32_e64 v137, |v55|, |v55|
	v_max_f32_e64 v138, |v54|, |v54|
	v_max_f32_e32 v137, v138, v137
	v_max_f32_e64 v138, |v57|, |v57|
	v_max_f32_e64 v139, |v56|, |v56|
	v_max_f32_e32 v138, v139, v138
	v_max3_f32 v135, v135, v137, v138
	s_waitcnt vmcnt(27)
	v_max_f32_e64 v137, |v47|, |v47|
	v_max_f32_e64 v138, |v46|, |v46|
	v_max_f32_e32 v137, v138, v137
	v_max_f32_e64 v138, |v49|, |v49|
	v_max_f32_e64 v139, |v48|, |v48|
	v_max_f32_e32 v138, v139, v138
	v_max3_f32 v135, v135, v137, v138
	s_waitcnt vmcnt(26)
	v_max_f32_e64 v137, |v43|, |v43|
	v_max_f32_e64 v138, |v42|, |v42|
	v_max_f32_e32 v137, v138, v137
	v_max_f32_e64 v138, |v45|, |v45|
	v_max_f32_e64 v139, |v44|, |v44|
	v_max_f32_e32 v138, v139, v138
	v_max3_f32 v135, v135, v137, v138
	s_waitcnt vmcnt(25)
	v_max_f32_e64 v137, |v39|, |v39|
	v_max_f32_e64 v138, |v38|, |v38|
	v_max_f32_e32 v137, v138, v137
	v_max_f32_e64 v138, |v41|, |v41|
	v_max_f32_e64 v139, |v40|, |v40|
	v_max_f32_e32 v138, v139, v138
	v_max3_f32 v135, v135, v137, v138
	s_waitcnt vmcnt(24)
	v_max_f32_e64 v137, |v35|, |v35|
	v_max_f32_e64 v138, |v34|, |v34|
	v_max_f32_e32 v137, v138, v137
	v_max_f32_e64 v138, |v37|, |v37|
	v_max_f32_e64 v139, |v36|, |v36|
	v_max_f32_e32 v138, v139, v138
	v_max3_f32 v135, v135, v137, v138
	s_waitcnt vmcnt(23)
	v_max_f32_e64 v137, |v31|, |v31|
	v_max_f32_e64 v138, |v30|, |v30|
	v_max_f32_e32 v137, v138, v137
	v_max_f32_e64 v138, |v33|, |v33|
	v_max_f32_e64 v139, |v32|, |v32|
	v_max_f32_e32 v138, v139, v138
	v_max3_f32 v135, v135, v137, v138
	s_waitcnt vmcnt(22)
	v_max_f32_e64 v137, |v27|, |v27|
	v_max_f32_e64 v138, |v26|, |v26|
	v_max_f32_e32 v137, v138, v137
	v_max_f32_e64 v138, |v29|, |v29|
	v_max_f32_e64 v139, |v28|, |v28|
	v_max_f32_e32 v138, v139, v138
	v_max3_f32 v135, v135, v137, v138
	s_waitcnt vmcnt(21)
	v_max_f32_e64 v137, |v23|, |v23|
	v_max_f32_e64 v138, |v22|, |v22|
	v_max_f32_e32 v137, v138, v137
	v_max_f32_e64 v138, |v25|, |v25|
	v_max_f32_e64 v139, |v24|, |v24|
	v_max_f32_e32 v138, v139, v138
	v_max3_f32 v135, v135, v137, v138
	s_waitcnt vmcnt(20)
	v_max_f32_e64 v137, |v15|, |v15|
	v_max_f32_e64 v138, |v14|, |v14|
	v_max_f32_e32 v137, v138, v137
	v_max_f32_e64 v138, |v17|, |v17|
	v_max_f32_e64 v139, |v16|, |v16|
	v_max_f32_e32 v138, v139, v138
	v_max3_f32 v135, v135, v137, v138
	s_waitcnt vmcnt(19)
	v_max_f32_e64 v137, |v19|, |v19|
	v_max_f32_e64 v138, |v18|, |v18|
	v_max_f32_e32 v137, v138, v137
	v_max_f32_e64 v138, |v21|, |v21|
	v_max_f32_e64 v139, |v20|, |v20|
	v_max_f32_e32 v138, v139, v138
	v_max3_f32 v135, v135, v137, v138
	s_waitcnt vmcnt(18)
	v_max_f32_e64 v137, |v11|, |v11|
	v_max_f32_e64 v138, |v10|, |v10|
	v_max_f32_e32 v137, v138, v137
	v_max_f32_e64 v138, |v13|, |v13|
	v_max_f32_e64 v139, |v12|, |v12|
	v_max_f32_e32 v138, v139, v138
	v_max3_f32 v135, v135, v137, v138
	s_waitcnt vmcnt(17)
	v_max_f32_e64 v137, |v7|, |v7|
	v_max_f32_e64 v138, |v6|, |v6|
	v_max_f32_e32 v137, v138, v137
	v_max_f32_e64 v138, |v9|, |v9|
	v_max_f32_e64 v139, |v8|, |v8|
	v_max_f32_e32 v138, v139, v138
	v_max3_f32 v135, v135, v137, v138
	s_waitcnt vmcnt(16)
; __device__ __forceinline__ void peer_row_store(const f32x4 (&v)[16], unsigned char* ws, int it, int layer, int lane) {
;     const int tbl = it >= NEXP, r = it - tbl * NEXP + layer * NEXP;
;     float am = 0.f;
; #pragma unroll
;     for (int j = 0; j < 16; ++j) am = fmaxf(fmaxf(am, fmaxf(fabsf(v[j][0]), fabsf(v[j][1]))), fmaxf(fabsf(v[j][2]), fabsf(v[j][3])));
;     am = __uint_as_float(max64u(__float_as_uint(am)));
;     const float q = am > 0.f ? 256.0f / am : 0.f;
;     unsigned* dst = (unsigned*)(ws + (tbl ? WS_PV : WS_PU) + (size_t)r * D) + lane;
;     if (tbl) {
;         const int rl = it - NEXP;
;         unsigned char* pvl = ws + WS_PV + (size_t)layer * NEXP * D + (size_t)rl * 8 + (lane & 1) * 4;
;         unsigned char* pvg = ws + WS_PV + (size_t)layer * NEXP * D + (size_t)NEXP * 2048 + (size_t)rl * 2048 + 4 * lane;
; #pragma unroll
;         for (int j = 0; j < 16; ++j) { int w = __builtin_amdgcn_cvt_pk_bf8_f32(v[j][0] * q, v[j][1] * q, 0, false); w = __builtin_amdgcn_cvt_pk_bf8_f32(v[j][2] * q, v[j][3] * q, w, true);
;             if (j < 8) *(unsigned*)(pvl + (size_t)((lane >> 1) + 32 * j) * (NEXP * 8)) = (unsigned)w;
;             else *(unsigned*)(pvg + 256 * (j - 8)) = (unsigned)w; }
;     } else {
; #pragma unroll
;         for (int j = 0; j < 16; ++j) { int w = __builtin_amdgcn_cvt_pk_fp8_f32(v[j][0] * q, v[j][1] * q, 0, false); w = __builtin_amdgcn_cvt_pk_fp8_f32(v[j][2] * q, v[j][3] * q, w, true); dst[64 * j] = (unsigned)w; }
;     }
;     if (lane == 0) ((float*)(ws + (tbl ? WS_SV : WS_SU)))[r] = am * (1.0f / 256.0f);
	v_max_f32_e64 v137, |v3|, |v3|
	v_max_f32_e64 v138, |v2|, |v2|
	v_max_f32_e32 v137, v138, v137
	v_max_f32_e64 v138, |v5|, |v5|
	v_max_f32_e64 v139, |v4|, |v4|
	v_max_f32_e32 v138, v139, v138
	v_max3_f32 v135, v135, v137, v138
	s_ashr_i32 s11, s10, 31
	s_nop 0
	v_max_u32_dpp v135, v135, v135 quad_perm:[1,0,3,2] row_mask:0xf bank_mask:0xf bound_ctrl:1
	s_nop 1
	v_max_u32_dpp v135, v135, v135 quad_perm:[2,3,0,1] row_mask:0xf bank_mask:0xf bound_ctrl:1
	s_nop 1
	v_max_u32_dpp v135, v135, v135 row_half_mirror row_mask:0xf bank_mask:0xf bound_ctrl:1
	s_nop 1
	v_max_u32_dpp v135, v135, v135 row_mirror row_mask:0xf bank_mask:0xf bound_ctrl:1
	v_mov_b32_e32 v137, v135
	s_nop 1
	v_permlane16_swap_b32_e32 v135, v137
	v_max_u32_e32 v135, v135, v137
	v_mov_b32_e32 v137, v135
	s_nop 1
	v_permlane32_swap_b32_e32 v135, v137
	v_max_u32_e32 v135, v135, v137
	v_div_scale_f32 v137, s[12:13], v135, v135, s31
	v_rcp_f32_e32 v138, v137
	s_lshl_b64 s[12:13], s[10:11], 12
	v_fma_f32 v139, -v137, v138, 1.0
	v_fmac_f32_e32 v138, v139, v138
	v_div_scale_f32 v139, vcc, s31, v135, s31
	v_mul_f32_e32 v140, v139, v138
	v_fma_f32 v141, -v137, v140, v139
	v_fmac_f32_e32 v140, v141, v138
	v_fma_f32 v137, -v137, v140, v139
	v_div_fmas_f32 v137, v137, v138, v140
	v_div_fixup_f32 v137, v137, v135, s31
	v_cmp_lt_f32_e32 vcc, 0, v135
	v_mov_b32_e32 v140, v131
	v_lshl_add_u64 v[138:139], v[132:133], 0, s[12:13]
	v_cndmask_b32_e32 v137, 0, v137, vcc
	v_mul_f32_e32 v86, v86, v137
	v_mul_f32_e32 v87, v87, v137
	v_cvt_pk_fp8_f32 v140, v86, v87
	v_mul_f32_e32 v86, v88, v137
	v_mul_f32_e32 v62, v62, v137
	v_mul_f32_e32 v63, v63, v137
	v_mov_b32_e32 v88, v131
	v_cvt_pk_fp8_f32 v88, v62, v63
	v_mul_f32_e32 v62, v64, v137
	v_mul_f32_e32 v63, v65, v137
	v_mul_f32_e32 v50, v50, v137
	v_cvt_pk_fp8_f32 v88, v62, v63 op_sel:[0,0,1]
	v_mul_f32_e32 v51, v51, v137
	v_mov_b32_e32 v62, v131
	v_cvt_pk_fp8_f32 v62, v50, v51
	v_mul_f32_e32 v50, v52, v137
	v_mul_f32_e32 v51, v53, v137
	v_mul_f32_e32 v52, v54, v137
	v_mul_f32_e32 v53, v55, v137
	v_mov_b32_e32 v54, v131
	v_cvt_pk_fp8_f32 v54, v52, v53
	v_cvt_pk_fp8_f32 v62, v50, v51 op_sel:[0,0,1]
	v_mul_f32_e32 v50, v56, v137
	v_mul_f32_e32 v51, v57, v137
	v_cvt_pk_fp8_f32 v54, v50, v51 op_sel:[0,0,1]
	v_mul_f32_e32 v46, v46, v137
	v_mul_f32_e32 v47, v47, v137
	v_mov_b32_e32 v50, v131
	v_cvt_pk_fp8_f32 v50, v46, v47
	v_mul_f32_e32 v46, v48, v137
	v_mul_f32_e32 v42, v42, v137
	v_mul_f32_e32 v43, v43, v137
	v_mov_b32_e32 v48, v131
	v_cvt_pk_fp8_f32 v48, v42, v43
	v_mul_f32_e32 v42, v44, v137
	v_mul_f32_e32 v43, v45, v137
	v_mul_f32_e32 v38, v38, v137
	v_cvt_pk_fp8_f32 v48, v42, v43 op_sel:[0,0,1]
	v_mul_f32_e32 v39, v39, v137
	v_mov_b32_e32 v42, v131
	v_cvt_pk_fp8_f32 v42, v38, v39
	v_mul_f32_e32 v38, v40, v137
	v_mul_f32_e32 v34, v34, v137
	v_mul_f32_e32 v35, v35, v137
	v_mov_b32_e32 v40, v131
	v_cvt_pk_fp8_f32 v40, v34, v35
	v_mul_f32_e32 v34, v36, v137
	v_mul_f32_e32 v35, v37, v137
	v_mul_f32_e32 v30, v30, v137
	v_cvt_pk_fp8_f32 v40, v34, v35 op_sel:[0,0,1]
	v_mul_f32_e32 v31, v31, v137
	v_mov_b32_e32 v34, v131
	v_cvt_pk_fp8_f32 v34, v30, v31
	v_mul_f32_e32 v30, v32, v137
	v_mul_f32_e32 v26, v26, v137
	v_mul_f32_e32 v27, v27, v137
	v_mov_b32_e32 v32, v131
	v_cvt_pk_fp8_f32 v32, v26, v27
	v_mul_f32_e32 v26, v28, v137
	v_mul_f32_e32 v27, v29, v137
	v_mul_f32_e32 v22, v22, v137
	v_cvt_pk_fp8_f32 v32, v26, v27 op_sel:[0,0,1]
	v_mul_f32_e32 v23, v23, v137
	v_mov_b32_e32 v26, v131
	v_cvt_pk_fp8_f32 v26, v22, v23
	v_mul_f32_e32 v22, v24, v137
	v_mul_f32_e32 v14, v14, v137
	v_mul_f32_e32 v15, v15, v137
	v_mov_b32_e32 v24, v131
	v_cvt_pk_fp8_f32 v24, v14, v15
	v_mul_f32_e32 v15, v17, v137
	v_mul_f32_e32 v10, v10, v137
	v_mul_f32_e32 v11, v11, v137
	v_mov_b32_e32 v17, v131
	v_cvt_pk_fp8_f32 v17, v10, v11
	v_mul_f32_e32 v14, v16, v137
	v_cvt_pk_fp8_f32 v24, v14, v15 op_sel:[0,0,1]
	v_mul_f32_e32 v14, v18, v137
	v_mul_f32_e32 v15, v19, v137
	v_mov_b32_e32 v16, v131
	v_cvt_pk_fp8_f32 v16, v14, v15
	v_mul_f32_e32 v10, v12, v137
	v_mul_f32_e32 v11, v13, v137
	v_cvt_pk_fp8_f32 v17, v10, v11 op_sel:[0,0,1]
	v_mul_f32_e32 v6, v6, v137
	v_mul_f32_e32 v7, v7, v137
	v_mov_b32_e32 v10, v131
	v_cvt_pk_fp8_f32 v10, v6, v7
	v_mul_f32_e32 v6, v8, v137
	v_mul_f32_e32 v2, v2, v137
	v_mul_f32_e32 v3, v3, v137
	v_mov_b32_e32 v8, v131
	v_mul_f32_e32 v87, v89, v137
	v_mul_f32_e32 v47, v49, v137
	v_mul_f32_e32 v31, v33, v137
	v_mul_f32_e32 v14, v20, v137
	v_mul_f32_e32 v15, v21, v137
	v_cvt_pk_fp8_f32 v8, v2, v3
	v_cvt_pk_fp8_f32 v140, v86, v87 op_sel:[0,0,1]
	v_cvt_pk_fp8_f32 v50, v46, v47 op_sel:[0,0,1]
	v_cvt_pk_fp8_f32 v34, v30, v31 op_sel:[0,0,1]
	v_cvt_pk_fp8_f32 v16, v14, v15 op_sel:[0,0,1]
	v_mul_f32_e32 v39, v41, v137
	v_mul_f32_e32 v23, v25, v137
	v_mul_f32_e32 v7, v9, v137
	v_cvt_pk_fp8_f32 v42, v38, v39 op_sel:[0,0,1]
	v_cvt_pk_fp8_f32 v26, v22, v23 op_sel:[0,0,1]
	v_cvt_pk_fp8_f32 v10, v6, v7 op_sel:[0,0,1]
	v_mul_f32_e32 v2, v4, v137
	v_mul_f32_e32 v3, v5, v137
	v_cvt_pk_fp8_f32 v8, v2, v3 op_sel:[0,0,1]
	global_store_dword v[138:139], v140, off
	global_store_dword v[138:139], v88, off offset:256
	global_store_dword v[138:139], v62, off offset:512
	global_store_dword v[138:139], v54, off offset:768
	global_store_dword v[138:139], v50, off offset:1024
	global_store_dword v[138:139], v48, off offset:1280
	global_store_dword v[138:139], v42, off offset:1536
	global_store_dword v[138:139], v40, off offset:1792
	global_store_dword v[138:139], v34, off offset:2048
	global_store_dword v[138:139], v32, off offset:2304
	global_store_dword v[138:139], v26, off offset:2560
	global_store_dword v[138:139], v24, off offset:2816
	global_store_dword v[138:139], v16, off offset:3072
	global_store_dword v[138:139], v17, off offset:3328
	global_store_dword v[138:139], v10, off offset:3584
	global_store_dword v[138:139], v8, off offset:3840
	s_and_saveexec_b64 s[12:13], s[0:1]
	s_cbranch_execz .LBB0_624
	s_lshl_b64 s[20:21], s[10:11], 2
	s_add_u32 s20, s17, s20
	s_addc_u32 s21, s18, s21
	v_mul_f32_e32 v2, 0x3b800000, v135
	global_store_dword v131, v2, s[20:21]
; __device__ __forceinline__ void peer_row_load(f32x4 (&v)[16], const float* const (&in)[34], int it, int layer, int lane) {
;     const int tbl = it >= NEXP, r = it - tbl * NEXP + layer * NEXP;
;     const f32x4* src = (const f32x4*)((tbl ? in[33] : in[32]) + (size_t)r * D) + lane;
; #pragma unroll
;     for (int j = 0; j < 16; ++j) v[j] = src[64 * j];
; }
; __device__ __forceinline__ void peer_row_store(const f32x4 (&v)[16], unsigned char* ws, int it, int layer, int lane) {
;     const int tbl = it >= NEXP, r = it - tbl * NEXP + layer * NEXP;
;     float am = 0.f;
; #pragma unroll
;     for (int j = 0; j < 16; ++j) am = fmaxf(fmaxf(am, fmaxf(fabsf(v[j][0]), fabsf(v[j][1]))), fmaxf(fabsf(v[j][2]), fabsf(v[j][3])));
;     am = __uint_as_float(max64u(__float_as_uint(am)));
;     ...
;     for (int it = it_lo + gw; it < it_hi; it += 2 * NGW) {
;         const int it1 = it + NGW, it2 = it + 2 * NGW;
;         peer_row_load(vb, in, it1 < it_hi ? it1 : it, only_layer, lane);
;         __builtin_amdgcn_sched_barrier(0);
;         peer_row_store(va, ws, it, only_layer, lane);
;         __builtin_amdgcn_sched_barrier(0);
;         peer_row_load(va, in, it2 < it_hi ? it2 : it, only_layer, lane);
;         __builtin_amdgcn_sched_barrier(0);
;         if (it1 < it_hi) peer_row_store(vb, ws, it1, only_layer, lane);
.LBB0_624:
	s_or_b64 exec, exec, s[12:13]
	s_add_i32 s7, s29, s19
	s_cmpk_lt_i32 s7, 0x1800
	s_cselect_b32 s7, s7, s10
	s_cmpk_gt_i32 s7, 0x3fff
	s_cselect_b64 s[10:11], -1, 0
	s_and_b64 s[12:13], s[10:11], exec
	s_cselect_b32 s12, 0xffffc000, 0
	s_add_i32 s12, s12, s7
	s_and_b64 s[10:11], s[10:11], exec
	s_cselect_b32 s7, s87, s85
	s_cselect_b32 s20, s86, s84
	s_ashr_i32 s13, s12, 31
	s_lshl_b64 s[10:11], s[12:13], 14
	s_add_u32 s10, s20, s10
	s_addc_u32 s11, s7, s11
	v_lshl_add_u64 v[2:3], s[10:11], 0, v[130:131]
	v_add_co_u32_e32 v4, vcc, s5, v2
	global_load_dwordx4 v[62:65], v130, s[10:11] offset:1024
	global_load_dwordx4 v[50:53], v130, s[10:11] offset:2048
	v_addc_co_u32_e32 v5, vcc, 0, v3, vcc
	v_add_co_u32_e32 v6, vcc, s14, v2
	s_nop 1
	v_addc_co_u32_e32 v7, vcc, 0, v3, vcc
	global_load_dwordx4 v[54:57], v130, s[10:11] offset:3072
	global_load_dwordx4 v[46:49], v[6:7], off offset:-4096
	global_load_dwordx4 v[42:45], v[4:5], off offset:1024
	global_load_dwordx4 v[38:41], v[4:5], off offset:2048
	global_load_dwordx4 v[30:33], v[6:7], off
	global_load_dwordx4 v[26:29], v[6:7], off offset:1024
	global_load_dwordx4 v[22:25], v[6:7], off offset:2048
	global_load_dwordx4 v[14:17], v[6:7], off offset:3072
	v_add_co_u32_e32 v2, vcc, 0x3000, v2
	s_nop 1
	v_addc_co_u32_e32 v3, vcc, 0, v3, vcc
	global_load_dwordx4 v[34:37], v[4:5], off offset:3072
	global_load_dwordx4 v[18:21], v[2:3], off
	global_load_dwordx4 v[10:13], v[2:3], off offset:1024
	global_load_dwordx4 v[6:9], v[2:3], off offset:2048
	global_load_dwordx4 v[86:89], v130, s[10:11]
	s_nop 0
	global_load_dwordx4 v[2:5], v[2:3], off offset:3072
	s_andn2_b64 vcc, exec, s[8:9]
	s_cbranch_vccnz .LBB0_621
	s_waitcnt vmcnt(33)
	v_max_f32_e64 v130, |v127|, |v127|
	v_max_f32_e64 v135, |v126|, |v126|
	v_max_f32_e32 v130, v135, v130
	v_max_f32_e64 v135, |v129|, |v129|
	v_max_f32_e64 v137, |v128|, |v128|
	v_max_f32_e32 v135, v137, v135
	v_max3_f32 v130, v130, 0, v135
	v_max_f32_e64 v135, |v123|, |v123|
	v_max_f32_e64 v137, |v122|, |v122|
	v_max_f32_e32 v135, v137, v135
	v_max_f32_e64 v137, |v125|, |v125|
	v_max_f32_e64 v138, |v124|, |v124|
	v_max_f32_e32 v137, v138, v137
	v_max3_f32 v130, v130, v135, v137
	v_max_f32_e64 v135, |v119|, |v119|
	v_max_f32_e64 v137, |v118|, |v118|
	v_max_f32_e32 v135, v137, v135
	v_max_f32_e64 v137, |v121|, |v121|
	v_max_f32_e64 v138, |v120|, |v120|
	v_max_f32_e32 v137, v138, v137
	v_max3_f32 v130, v130, v135, v137
	v_max_f32_e64 v135, |v115|, |v115|
	v_max_f32_e64 v137, |v114|, |v114|
	v_max_f32_e32 v135, v137, v135
	v_max_f32_e64 v137, |v117|, |v117|
	v_max_f32_e64 v138, |v116|, |v116|
	v_max_f32_e32 v137, v138, v137
	v_max3_f32 v130, v130, v135, v137
	v_max_f32_e64 v135, |v111|, |v111|
	v_max_f32_e64 v137, |v110|, |v110|
	v_max_f32_e32 v135, v137, v135
	v_max_f32_e64 v137, |v113|, |v113|
	v_max_f32_e64 v138, |v112|, |v112|
	v_max_f32_e32 v137, v138, v137
	v_max3_f32 v130, v130, v135, v137
	v_max_f32_e64 v135, |v107|, |v107|
	v_max_f32_e64 v137, |v106|, |v106|
	v_max_f32_e32 v135, v137, v135
	v_max_f32_e64 v137, |v109|, |v109|
	v_max_f32_e64 v138, |v108|, |v108|
	v_max_f32_e32 v137, v138, v137
	v_max3_f32 v130, v130, v135, v137
	v_max_f32_e64 v135, |v103|, |v103|
	v_max_f32_e64 v137, |v102|, |v102|
	v_max_f32_e32 v135, v137, v135
	v_max_f32_e64 v137, |v105|, |v105|
	v_max_f32_e64 v138, |v104|, |v104|
	v_max_f32_e32 v137, v138, v137
	v_max3_f32 v130, v130, v135, v137
	v_max_f32_e64 v135, |v99|, |v99|
	v_max_f32_e64 v137, |v98|, |v98|
	v_max_f32_e32 v135, v137, v135
	v_max_f32_e64 v137, |v101|, |v101|
	v_max_f32_e64 v138, |v100|, |v100|
	v_max_f32_e32 v137, v138, v137
	v_max3_f32 v130, v130, v135, v137
	v_max_f32_e64 v135, |v95|, |v95|
	v_max_f32_e64 v137, |v94|, |v94|
	v_max_f32_e32 v135, v137, v135
	v_max_f32_e64 v137, |v97|, |v97|
	v_max_f32_e64 v138, |v96|, |v96|
	v_max_f32_e32 v137, v138, v137
	v_max3_f32 v130, v130, v135, v137
	v_max_f32_e64 v135, |v91|, |v91|
	v_max_f32_e64 v137, |v90|, |v90|
	v_max_f32_e32 v135, v137, v135
	v_max_f32_e64 v137, |v93|, |v93|
	v_max_f32_e64 v138, |v92|, |v92|
	v_max_f32_e32 v137, v138, v137
	v_max3_f32 v130, v130, v135, v137
	v_max_f32_e64 v135, |v83|, |v83|
	v_max_f32_e64 v137, |v82|, |v82|
	v_max_f32_e32 v135, v137, v135
	v_max_f32_e64 v137, |v85|, |v85|
	v_max_f32_e64 v138, |v84|, |v84|
	v_max_f32_e32 v137, v138, v137
	v_max3_f32 v130, v130, v135, v137
	v_max_f32_e64 v135, |v79|, |v79|
	v_max_f32_e64 v137, |v78|, |v78|
	v_max_f32_e32 v135, v137, v135
	v_max_f32_e64 v137, |v81|, |v81|
	v_max_f32_e64 v138, |v80|, |v80|
	v_max_f32_e32 v137, v138, v137
	v_max3_f32 v130, v130, v135, v137
	v_max_f32_e64 v135, |v75|, |v75|
	v_max_f32_e64 v137, |v74|, |v74|
	v_max_f32_e32 v135, v137, v135
	v_max_f32_e64 v137, |v77|, |v77|
	v_max_f32_e64 v138, |v76|, |v76|
	v_max_f32_e32 v137, v138, v137
	v_max3_f32 v130, v130, v135, v137
	v_max_f32_e64 v135, |v71|, |v71|
	v_max_f32_e64 v137, |v70|, |v70|
	v_max_f32_e32 v135, v137, v135
	v_max_f32_e64 v137, |v73|, |v73|
	v_max_f32_e64 v138, |v72|, |v72|
	v_max_f32_e32 v137, v138, v137
	v_max3_f32 v130, v130, v135, v137
	v_max_f32_e64 v135, |v67|, |v67|
	v_max_f32_e64 v137, |v66|, |v66|
	v_max_f32_e32 v135, v137, v135
	v_max_f32_e64 v137, |v69|, |v69|
	v_max_f32_e64 v138, |v68|, |v68|
	v_max_f32_e32 v137, v138, v137
	v_max3_f32 v130, v130, v135, v137
	s_waitcnt vmcnt(32)
; __device__ __forceinline__ void peer_row_store(const f32x4 (&v)[16], unsigned char* ws, int it, int layer, int lane) {
;     const int tbl = it >= NEXP, r = it - tbl * NEXP + layer * NEXP;
;     float am = 0.f;
; #pragma unroll
;     for (int j = 0; j < 16; ++j) am = fmaxf(fmaxf(am, fmaxf(fabsf(v[j][0]), fabsf(v[j][1]))), fmaxf(fabsf(v[j][2]), fabsf(v[j][3])));
;     am = __uint_as_float(max64u(__float_as_uint(am)));
;     const float q = am > 0.f ? 256.0f / am : 0.f;
;     unsigned* dst = (unsigned*)(ws + (tbl ? WS_PV : WS_PU) + (size_t)r * D) + lane;
;     if (tbl) {
;         const int rl = it - NEXP;
;         unsigned char* pvl = ws + WS_PV + (size_t)layer * NEXP * D + (size_t)rl * 8 + (lane & 1) * 4;
;         unsigned char* pvg = ws + WS_PV + (size_t)layer * NEXP * D + (size_t)NEXP * 2048 + (size_t)rl * 2048 + 4 * lane;
; #pragma unroll
;         for (int j = 0; j < 16; ++j) { int w = __builtin_amdgcn_cvt_pk_bf8_f32(v[j][0] * q, v[j][1] * q, 0, false); w = __builtin_amdgcn_cvt_pk_bf8_f32(v[j][2] * q, v[j][3] * q, w, true);
;             if (j < 8) *(unsigned*)(pvl + (size_t)((lane >> 1) + 32 * j) * (NEXP * 8)) = (unsigned)w;
;             else *(unsigned*)(pvg + 256 * (j - 8)) = (unsigned)w; }
;     } else {
; #pragma unroll
;         for (int j = 0; j < 16; ++j) { int w = __builtin_amdgcn_cvt_pk_fp8_f32(v[j][0] * q, v[j][1] * q, 0, false); w = __builtin_amdgcn_cvt_pk_fp8_f32(v[j][2] * q, v[j][3] * q, w, true); dst[64 * j] = (unsigned)w; }
;     }
;     if (lane == 0) ((float*)(ws + (tbl ? WS_SV : WS_SU)))[r] = am * (1.0f / 256.0f);
	v_max_f32_e64 v135, |v59|, |v59|
	v_max_f32_e64 v137, |v58|, |v58|
	v_max_f32_e32 v135, v137, v135
	v_max_f32_e64 v137, |v61|, |v61|
	v_max_f32_e64 v138, |v60|, |v60|
	v_max_f32_e32 v137, v138, v137
	v_max3_f32 v130, v130, v135, v137
	s_ashr_i32 s7, s6, 31
	s_nop 0
	v_max_u32_dpp v130, v130, v130 quad_perm:[1,0,3,2] row_mask:0xf bank_mask:0xf bound_ctrl:1
	s_nop 1
	v_max_u32_dpp v130, v130, v130 quad_perm:[2,3,0,1] row_mask:0xf bank_mask:0xf bound_ctrl:1
	s_nop 1
	v_max_u32_dpp v130, v130, v130 row_half_mirror row_mask:0xf bank_mask:0xf bound_ctrl:1
	s_nop 1
	v_max_u32_dpp v130, v130, v130 row_mirror row_mask:0xf bank_mask:0xf bound_ctrl:1
	v_mov_b32_e32 v135, v130
	s_nop 1
	v_permlane16_swap_b32_e32 v130, v135
	v_max_u32_e32 v130, v130, v135
	v_mov_b32_e32 v135, v130
	s_nop 1
	v_permlane32_swap_b32_e32 v130, v135
	v_max_u32_e32 v130, v130, v135
	v_div_scale_f32 v135, s[8:9], v130, v130, s31
	v_rcp_f32_e32 v137, v135
	s_lshl_b64 s[8:9], s[6:7], 12
	v_fma_f32 v138, -v135, v137, 1.0
	v_fmac_f32_e32 v137, v138, v137
	v_div_scale_f32 v138, vcc, s31, v130, s31
	v_mul_f32_e32 v139, v138, v137
	v_fma_f32 v140, -v135, v139, v138
	v_fmac_f32_e32 v139, v140, v137
	v_fma_f32 v135, -v135, v139, v138
	v_div_fmas_f32 v135, v135, v137, v139
	v_div_fixup_f32 v135, v135, v130, s31
	v_cmp_lt_f32_e32 vcc, 0, v130
	v_mov_b32_e32 v137, v131
	v_lshl_add_u64 v[138:139], v[132:133], 0, s[8:9]
	v_cndmask_b32_e32 v135, 0, v135, vcc
	v_mul_f32_e32 v126, v126, v135
	v_mul_f32_e32 v127, v127, v135
	v_cvt_pk_fp8_f32 v137, v126, v127
	v_mul_f32_e32 v126, v128, v135
	v_mul_f32_e32 v122, v122, v135
	v_mul_f32_e32 v123, v123, v135
	v_mov_b32_e32 v128, v131
	v_cvt_pk_fp8_f32 v128, v122, v123
	v_mul_f32_e32 v122, v124, v135
	v_mul_f32_e32 v123, v125, v135
	v_mul_f32_e32 v118, v118, v135
	v_cvt_pk_fp8_f32 v128, v122, v123 op_sel:[0,0,1]
	v_mul_f32_e32 v119, v119, v135
	v_mov_b32_e32 v122, v131
	v_cvt_pk_fp8_f32 v122, v118, v119
	v_mul_f32_e32 v118, v120, v135
	v_mul_f32_e32 v114, v114, v135
	v_mul_f32_e32 v115, v115, v135
	v_mov_b32_e32 v120, v131
	v_cvt_pk_fp8_f32 v120, v114, v115
	v_mul_f32_e32 v114, v116, v135
	v_mul_f32_e32 v115, v117, v135
	v_mul_f32_e32 v110, v110, v135
	v_cvt_pk_fp8_f32 v120, v114, v115 op_sel:[0,0,1]
	v_mul_f32_e32 v111, v111, v135
	v_mov_b32_e32 v114, v131
	v_cvt_pk_fp8_f32 v114, v110, v111
	v_mul_f32_e32 v110, v112, v135
	v_mul_f32_e32 v106, v106, v135
	v_mul_f32_e32 v107, v107, v135
	v_mov_b32_e32 v112, v131
	v_cvt_pk_fp8_f32 v112, v106, v107
	v_mul_f32_e32 v106, v108, v135
	v_mul_f32_e32 v107, v109, v135
	v_mul_f32_e32 v102, v102, v135
	v_cvt_pk_fp8_f32 v112, v106, v107 op_sel:[0,0,1]
	v_mul_f32_e32 v103, v103, v135
	v_mov_b32_e32 v106, v131
	v_cvt_pk_fp8_f32 v106, v102, v103
	v_mul_f32_e32 v102, v104, v135
	v_mul_f32_e32 v98, v98, v135
	v_mul_f32_e32 v99, v99, v135
	v_mov_b32_e32 v104, v131
	v_cvt_pk_fp8_f32 v104, v98, v99
	v_mul_f32_e32 v98, v100, v135
	v_mul_f32_e32 v99, v101, v135
	v_mul_f32_e32 v94, v94, v135
	v_cvt_pk_fp8_f32 v104, v98, v99 op_sel:[0,0,1]
	v_mul_f32_e32 v95, v95, v135
	v_mov_b32_e32 v98, v131
	v_cvt_pk_fp8_f32 v98, v94, v95
	v_mul_f32_e32 v94, v96, v135
	v_mul_f32_e32 v90, v90, v135
	v_mul_f32_e32 v91, v91, v135
	v_mov_b32_e32 v96, v131
	v_cvt_pk_fp8_f32 v96, v90, v91
	v_mul_f32_e32 v90, v92, v135
	v_mul_f32_e32 v91, v93, v135
	v_mul_f32_e32 v82, v82, v135
	v_cvt_pk_fp8_f32 v96, v90, v91 op_sel:[0,0,1]
	v_mul_f32_e32 v83, v83, v135
	v_mov_b32_e32 v90, v131
	v_cvt_pk_fp8_f32 v90, v82, v83
	v_mul_f32_e32 v82, v84, v135
	v_mul_f32_e32 v78, v78, v135
	v_mul_f32_e32 v79, v79, v135
	v_mov_b32_e32 v84, v131
	v_cvt_pk_fp8_f32 v84, v78, v79
	v_mul_f32_e32 v78, v80, v135
	v_mul_f32_e32 v79, v81, v135
	v_mul_f32_e32 v74, v74, v135
	v_cvt_pk_fp8_f32 v84, v78, v79 op_sel:[0,0,1]
	v_mul_f32_e32 v75, v75, v135
	v_mov_b32_e32 v78, v131
	v_cvt_pk_fp8_f32 v78, v74, v75
	v_mul_f32_e32 v74, v76, v135
	v_mul_f32_e32 v70, v70, v135
	v_mul_f32_e32 v71, v71, v135
	v_mov_b32_e32 v76, v131
	v_cvt_pk_fp8_f32 v76, v70, v71
	v_mul_f32_e32 v70, v72, v135
	v_mul_f32_e32 v71, v73, v135
	v_mul_f32_e32 v66, v66, v135
	v_cvt_pk_fp8_f32 v76, v70, v71 op_sel:[0,0,1]
	v_mul_f32_e32 v67, v67, v135
	v_mov_b32_e32 v70, v131
	v_cvt_pk_fp8_f32 v70, v66, v67
	v_mul_f32_e32 v66, v68, v135
	v_mul_f32_e32 v58, v58, v135
	v_mul_f32_e32 v59, v59, v135
	v_mov_b32_e32 v68, v131
	v_mul_f32_e32 v127, v129, v135
	v_mul_f32_e32 v111, v113, v135
	v_mul_f32_e32 v95, v97, v135
	v_mul_f32_e32 v75, v77, v135
	v_cvt_pk_fp8_f32 v68, v58, v59
	v_cvt_pk_fp8_f32 v137, v126, v127 op_sel:[0,0,1]
	v_cvt_pk_fp8_f32 v114, v110, v111 op_sel:[0,0,1]
	v_cvt_pk_fp8_f32 v98, v94, v95 op_sel:[0,0,1]
	v_cvt_pk_fp8_f32 v78, v74, v75 op_sel:[0,0,1]
	v_mul_f32_e32 v119, v121, v135
	v_mul_f32_e32 v103, v105, v135
	v_mul_f32_e32 v83, v85, v135
	v_mul_f32_e32 v67, v69, v135
	v_cvt_pk_fp8_f32 v122, v118, v119 op_sel:[0,0,1]
	v_cvt_pk_fp8_f32 v106, v102, v103 op_sel:[0,0,1]
	v_cvt_pk_fp8_f32 v90, v82, v83 op_sel:[0,0,1]
	v_cvt_pk_fp8_f32 v70, v66, v67 op_sel:[0,0,1]
	v_mul_f32_e32 v58, v60, v135
	v_mul_f32_e32 v59, v61, v135
	v_cvt_pk_fp8_f32 v68, v58, v59 op_sel:[0,0,1]
	global_store_dword v[138:139], v137, off
	global_store_dword v[138:139], v128, off offset:256
	global_store_dword v[138:139], v122, off offset:512
	global_store_dword v[138:139], v120, off offset:768
	global_store_dword v[138:139], v114, off offset:1024
	global_store_dword v[138:139], v112, off offset:1280
	global_store_dword v[138:139], v106, off offset:1536
	global_store_dword v[138:139], v104, off offset:1792
	global_store_dword v[138:139], v98, off offset:2048
	global_store_dword v[138:139], v96, off offset:2304
	global_store_dword v[138:139], v90, off offset:2560
	global_store_dword v[138:139], v84, off offset:2816
	global_store_dword v[138:139], v78, off offset:3072
	global_store_dword v[138:139], v76, off offset:3328
	global_store_dword v[138:139], v70, off offset:3584
	global_store_dword v[138:139], v68, off offset:3840
	s_and_saveexec_b64 s[8:9], s[0:1]
	s_cbranch_execz .LBB0_620
	s_lshl_b64 s[6:7], s[6:7], 2
	s_add_u32 s6, s17, s6
	s_addc_u32 s7, s18, s7
	v_mul_f32_e32 v58, 0x3b800000, v130
	global_store_dword v131, v58, s[6:7]
	s_branch .LBB0_620

; __device__ __forceinline__ void peer_row_load(f32x4 (&v)[16], const float* const (&in)[34], int it, int layer, int lane) {
;     const int tbl = it >= NEXP, r = it - tbl * NEXP + layer * NEXP;
;     const f32x4* src = (const f32x4*)((tbl ? in[33] : in[32]) + (size_t)r * D) + lane;
; #pragma unroll
;     for (int j = 0; j < 16; ++j) v[j] = src[64 * j];
; }
; __device__ __forceinline__ void peer_row_store(const f32x4 (&v)[16], unsigned char* ws, int it, int layer, int lane) {
;     const int tbl = it >= NEXP, r = it - tbl * NEXP + layer * NEXP;
;     float am = 0.f;
; #pragma unroll
;     for (int j = 0; j < 16; ++j) am = fmaxf(fmaxf(am, fmaxf(fabsf(v[j][0]), fabsf(v[j][1]))), fmaxf(fabsf(v[j][2]), fabsf(v[j][3])));
;     am = __uint_as_float(max64u(__float_as_uint(am)));
;     const float q = am > 0.f ? 256.0f / am : 0.f;
;     unsigned* dst = (unsigned*)(ws + (tbl ? WS_PV : WS_PU) + (size_t)r * D) + lane;
;     if (tbl) {
;         const int rl = it - NEXP;
;         unsigned char* pvl = ws + WS_PV + (size_t)layer * NEXP * D + (size_t)rl * 8 + (lane & 1) * 4;
;         unsigned char* pvg = ws + WS_PV + (size_t)layer * NEXP * D + (size_t)NEXP * 2048 + (size_t)rl * 2048 + 4 * lane;
; #pragma unroll
;         for (int j = 0; j < 16; ++j) { int w = __builtin_amdgcn_cvt_pk_bf8_f32(v[j][0] * q, v[j][1] * q, 0, false); w = __builtin_amdgcn_cvt_pk_bf8_f32(v[j][2] * q, v[j][3] * q, w, true);
;             if (j < 8) *(unsigned*)(pvl + (size_t)((lane >> 1) + 32 * j) * (NEXP * 8)) = (unsigned)w;
;             else *(unsigned*)(pvg + 256 * (j - 8)) = (unsigned)w; }
;     } else {
; #pragma unroll
;         for (int j = 0; j < 16; ++j) { int w = __builtin_amdgcn_cvt_pk_fp8_f32(v[j][0] * q, v[j][1] * q, 0, false); w = __builtin_amdgcn_cvt_pk_fp8_f32(v[j][2] * q, v[j][3] * q, w, true); dst[64 * j] = (unsigned)w; }
;     }
;     if (lane == 0) ((float*)(ws + (tbl ? WS_SV : WS_SU)))[r] = am * (1.0f / 256.0f);
.Lp4r_conv:
	s_waitcnt vmcnt(0) lgkmcnt(0)
	v_and_b32_e32 v11, 63, v0
	v_lshrrev_b32_e32 v7, 6, v0
	v_lshlrev_b32_e32 v1, 4, v11
	v_readfirstlane_b32 s0, v7
	v_lshlrev_b32_e32 v2, 2, v11
	v_add_u32_e32 v3, 0x1000, v1
	v_add_u32_e32 v4, 0x2000, v1
	v_add_u32_e32 v5, 0x3000, v1
	v_mov_b32_e32 v10, 0
	v_cmp_eq_u32_e64 s[12:13], 0, v11
	s_lshl_b32 s1, s2, 3
	s_add_i32 s4, s1, s0
	s_addk_i32 s4, 0x1800
	s_mov_b32 s14, 0x43800000
	s_lshl_b32 s1, s4, 14
	s_add_u32 s6, s84, s1
	s_addc_u32 s7, s85, 0
	global_load_dwordx4 v[40:43], v1, s[6:7]
	global_load_dwordx4 v[44:47], v1, s[6:7] offset:1024
	global_load_dwordx4 v[48:51], v1, s[6:7] offset:2048
	global_load_dwordx4 v[52:55], v1, s[6:7] offset:3072
	global_load_dwordx4 v[56:59], v3, s[6:7]
	global_load_dwordx4 v[60:63], v3, s[6:7] offset:1024
	global_load_dwordx4 v[64:67], v3, s[6:7] offset:2048
	global_load_dwordx4 v[68:71], v3, s[6:7] offset:3072
	global_load_dwordx4 v[72:75], v4, s[6:7]
	global_load_dwordx4 v[76:79], v4, s[6:7] offset:1024
	global_load_dwordx4 v[80:83], v4, s[6:7] offset:2048
	global_load_dwordx4 v[84:87], v4, s[6:7] offset:3072
	global_load_dwordx4 v[88:91], v5, s[6:7]
	global_load_dwordx4 v[92:95], v5, s[6:7] offset:1024
	global_load_dwordx4 v[96:99], v5, s[6:7] offset:2048
	global_load_dwordx4 v[100:103], v5, s[6:7] offset:3072
	s_add_i32 s5, s4, 1024
	s_lshl_b32 s1, s5, 14
	s_add_u32 s6, s84, s1
	s_addc_u32 s7, s85, 0
	global_load_dwordx4 v[104:107], v1, s[6:7]
	global_load_dwordx4 v[108:111], v1, s[6:7] offset:1024
	global_load_dwordx4 v[112:115], v1, s[6:7] offset:2048
	global_load_dwordx4 v[116:119], v1, s[6:7] offset:3072
	global_load_dwordx4 v[120:123], v3, s[6:7]
	global_load_dwordx4 v[124:127], v3, s[6:7] offset:1024
	global_load_dwordx4 v[128:131], v3, s[6:7] offset:2048
	global_load_dwordx4 v[132:135], v3, s[6:7] offset:3072
	global_load_dwordx4 v[136:139], v4, s[6:7]
	global_load_dwordx4 v[140:143], v4, s[6:7] offset:1024
	global_load_dwordx4 v[144:147], v4, s[6:7] offset:2048
	global_load_dwordx4 v[148:151], v4, s[6:7] offset:3072
	global_load_dwordx4 v[152:155], v5, s[6:7]
	global_load_dwordx4 v[156:159], v5, s[6:7] offset:1024
	global_load_dwordx4 v[160:163], v5, s[6:7] offset:2048
	global_load_dwordx4 v[164:167], v5, s[6:7] offset:3072
	s_waitcnt vmcnt(31)
	v_max3_f32 v6, |v40|, |v41|, 0
	v_max3_f32 v6, |v42|, |v43|, v6
	s_waitcnt vmcnt(30)
	v_max3_f32 v6, |v44|, |v45|, v6
	v_max3_f32 v6, |v46|, |v47|, v6
	s_waitcnt vmcnt(29)
	v_max3_f32 v6, |v48|, |v49|, v6
	v_max3_f32 v6, |v50|, |v51|, v6
	s_waitcnt vmcnt(28)
	v_max3_f32 v6, |v52|, |v53|, v6
	v_max3_f32 v6, |v54|, |v55|, v6
	s_waitcnt vmcnt(27)
	v_max3_f32 v6, |v56|, |v57|, v6
	v_max3_f32 v6, |v58|, |v59|, v6
	s_waitcnt vmcnt(26)
	v_max3_f32 v6, |v60|, |v61|, v6
	v_max3_f32 v6, |v62|, |v63|, v6
	s_waitcnt vmcnt(25)
	v_max3_f32 v6, |v64|, |v65|, v6
	v_max3_f32 v6, |v66|, |v67|, v6
	s_waitcnt vmcnt(24)
	v_max3_f32 v6, |v68|, |v69|, v6
	v_max3_f32 v6, |v70|, |v71|, v6
	s_waitcnt vmcnt(23)
	v_max3_f32 v6, |v72|, |v73|, v6
	v_max3_f32 v6, |v74|, |v75|, v6
	s_waitcnt vmcnt(22)
	v_max3_f32 v6, |v76|, |v77|, v6
	v_max3_f32 v6, |v78|, |v79|, v6
	s_waitcnt vmcnt(21)
	v_max3_f32 v6, |v80|, |v81|, v6
	v_max3_f32 v6, |v82|, |v83|, v6
	s_waitcnt vmcnt(20)
	v_max3_f32 v6, |v84|, |v85|, v6
	v_max3_f32 v6, |v86|, |v87|, v6
	s_waitcnt vmcnt(19)
	v_max3_f32 v6, |v88|, |v89|, v6
	v_max3_f32 v6, |v90|, |v91|, v6
	s_waitcnt vmcnt(18)
	v_max3_f32 v6, |v92|, |v93|, v6
	v_max3_f32 v6, |v94|, |v95|, v6
	s_waitcnt vmcnt(17)
	v_max3_f32 v6, |v96|, |v97|, v6
	v_max3_f32 v6, |v98|, |v99|, v6
	s_waitcnt vmcnt(16)
	v_max3_f32 v6, |v100|, |v101|, v6
	v_max3_f32 v6, |v102|, |v103|, v6
	s_nop 1
	v_max_u32_dpp v6, v6, v6 quad_perm:[1,0,3,2] row_mask:0xf bank_mask:0xf bound_ctrl:1
	s_nop 1
	v_max_u32_dpp v6, v6, v6 quad_perm:[2,3,0,1] row_mask:0xf bank_mask:0xf bound_ctrl:1
	s_nop 1
	v_max_u32_dpp v6, v6, v6 row_half_mirror row_mask:0xf bank_mask:0xf bound_ctrl:1
	s_nop 1
	v_max_u32_dpp v6, v6, v6 row_mirror row_mask:0xf bank_mask:0xf bound_ctrl:1
	s_nop 1
	v_mov_b32_e32 v7, v6
	s_nop 1
	v_permlane16_swap_b32_e32 v6, v7
	v_max_u32_e32 v6, v6, v7
	v_mov_b32_e32 v7, v6
	s_nop 1
	v_permlane32_swap_b32_e32 v6, v7
	v_max_u32_e32 v6, v6, v7
	v_div_scale_f32 v12, s[16:17], v6, v6, s14
	v_rcp_f32_e32 v13, v12
	s_nop 0
	v_fma_f32 v14, -v12, v13, 1.0
	v_fmac_f32_e32 v13, v14, v13
	v_div_scale_f32 v14, vcc, s14, v6, s14
	v_mul_f32_e32 v15, v14, v13
	v_fma_f32 v16, -v12, v15, v14
	v_fmac_f32_e32 v15, v16, v13
	v_fma_f32 v12, -v12, v15, v14
	v_div_fmas_f32 v12, v12, v13, v15
	v_div_fixup_f32 v9, v12, v6, s14
	v_cmp_lt_f32_e32 vcc, 0, v6
	s_nop 1
	v_cndmask_b32_e32 v9, 0, v9, vcc
	s_lshl_b32 s1, s4, 12
	s_add_u32 s8, s90, 0xba00000
	s_addc_u32 s9, s91, 0
	s_add_u32 s8, s8, s1
	s_addc_u32 s9, s9, 0
	s_lshl_b32 s1, s4, 2
	s_add_u32 s10, s90, 0x1ba00000
	s_addc_u32 s11, s91, 0
	s_add_u32 s10, s10, s1
	s_addc_u32 s11, s11, 0
	v_mul_f32_e32 v40, v40, v9
	v_mul_f32_e32 v41, v41, v9
	v_mul_f32_e32 v42, v42, v9
	v_mul_f32_e32 v43, v43, v9
	v_mov_b32_e32 v20, v10
	v_cvt_pk_fp8_f32 v20, v40, v41
	v_mul_f32_e32 v44, v44, v9
	v_mul_f32_e32 v45, v45, v9
	v_mul_f32_e32 v46, v46, v9
	v_mul_f32_e32 v47, v47, v9
	v_mov_b32_e32 v21, v10
	v_cvt_pk_fp8_f32 v21, v44, v45
	v_cvt_pk_fp8_f32 v20, v42, v43 op_sel:[0,0,1]
	v_mul_f32_e32 v48, v48, v9
	v_mul_f32_e32 v49, v49, v9
	v_mul_f32_e32 v50, v50, v9
	v_mul_f32_e32 v51, v51, v9
	v_mov_b32_e32 v22, v10
	v_cvt_pk_fp8_f32 v22, v48, v49
	v_cvt_pk_fp8_f32 v21, v46, v47 op_sel:[0,0,1]
	v_mul_f32_e32 v52, v52, v9
	v_mul_f32_e32 v53, v53, v9
	v_mul_f32_e32 v54, v54, v9
	v_mul_f32_e32 v55, v55, v9
	v_mov_b32_e32 v23, v10
; __device__ __forceinline__ void peer_row_load(f32x4 (&v)[16], const float* const (&in)[34], int it, int layer, int lane) {
;     const int tbl = it >= NEXP, r = it - tbl * NEXP + layer * NEXP;
;     const f32x4* src = (const f32x4*)((tbl ? in[33] : in[32]) + (size_t)r * D) + lane;
; #pragma unroll
;     for (int j = 0; j < 16; ++j) v[j] = src[64 * j];
; }
; __device__ __forceinline__ void peer_row_store(const f32x4 (&v)[16], unsigned char* ws, int it, int layer, int lane) {
;     const int tbl = it >= NEXP, r = it - tbl * NEXP + layer * NEXP;
;     float am = 0.f;
; #pragma unroll
;     for (int j = 0; j < 16; ++j) am = fmaxf(fmaxf(am, fmaxf(fabsf(v[j][0]), fabsf(v[j][1]))), fmaxf(fabsf(v[j][2]), fabsf(v[j][3])));
;     am = __uint_as_float(max64u(__float_as_uint(am)));
;     const float q = am > 0.f ? 256.0f / am : 0.f;
;     unsigned* dst = (unsigned*)(ws + (tbl ? WS_PV : WS_PU) + (size_t)r * D) + lane;
;     if (tbl) {
;         const int rl = it - NEXP;
;         unsigned char* pvl = ws + WS_PV + (size_t)layer * NEXP * D + (size_t)rl * 8 + (lane & 1) * 4;
;         unsigned char* pvg = ws + WS_PV + (size_t)layer * NEXP * D + (size_t)NEXP * 2048 + (size_t)rl * 2048 + 4 * lane;
; #pragma unroll
;         for (int j = 0; j < 16; ++j) { int w = __builtin_amdgcn_cvt_pk_bf8_f32(v[j][0] * q, v[j][1] * q, 0, false); w = __builtin_amdgcn_cvt_pk_bf8_f32(v[j][2] * q, v[j][3] * q, w, true);
;             if (j < 8) *(unsigned*)(pvl + (size_t)((lane >> 1) + 32 * j) * (NEXP * 8)) = (unsigned)w;
;             else *(unsigned*)(pvg + 256 * (j - 8)) = (unsigned)w; }
;     } else {
; #pragma unroll
;         for (int j = 0; j < 16; ++j) { int w = __builtin_amdgcn_cvt_pk_fp8_f32(v[j][0] * q, v[j][1] * q, 0, false); w = __builtin_amdgcn_cvt_pk_fp8_f32(v[j][2] * q, v[j][3] * q, w, true); dst[64 * j] = (unsigned)w; }
;     }
;     if (lane == 0) ((float*)(ws + (tbl ? WS_SV : WS_SU)))[r] = am * (1.0f / 256.0f);
	v_cvt_pk_fp8_f32 v23, v52, v53
	v_cvt_pk_fp8_f32 v22, v50, v51 op_sel:[0,0,1]
	v_mul_f32_e32 v56, v56, v9
	v_mul_f32_e32 v57, v57, v9
	v_mul_f32_e32 v58, v58, v9
	v_mul_f32_e32 v59, v59, v9
	v_mov_b32_e32 v24, v10
	v_cvt_pk_fp8_f32 v24, v56, v57
	v_cvt_pk_fp8_f32 v23, v54, v55 op_sel:[0,0,1]
	v_mul_f32_e32 v60, v60, v9
	v_mul_f32_e32 v61, v61, v9
	v_mul_f32_e32 v62, v62, v9
	v_mul_f32_e32 v63, v63, v9
	v_mov_b32_e32 v25, v10
	v_cvt_pk_fp8_f32 v25, v60, v61
	v_cvt_pk_fp8_f32 v24, v58, v59 op_sel:[0,0,1]
	v_mul_f32_e32 v64, v64, v9
	v_mul_f32_e32 v65, v65, v9
	v_mul_f32_e32 v66, v66, v9
	v_mul_f32_e32 v67, v67, v9
	v_mov_b32_e32 v26, v10
	v_cvt_pk_fp8_f32 v26, v64, v65
	v_cvt_pk_fp8_f32 v25, v62, v63 op_sel:[0,0,1]
	v_mul_f32_e32 v68, v68, v9
	v_mul_f32_e32 v69, v69, v9
	v_mul_f32_e32 v70, v70, v9
	v_mul_f32_e32 v71, v71, v9
	v_mov_b32_e32 v27, v10
	v_cvt_pk_fp8_f32 v27, v68, v69
	v_cvt_pk_fp8_f32 v26, v66, v67 op_sel:[0,0,1]
	v_mul_f32_e32 v72, v72, v9
	v_mul_f32_e32 v73, v73, v9
	v_mul_f32_e32 v74, v74, v9
	v_mul_f32_e32 v75, v75, v9
	v_mov_b32_e32 v28, v10
	v_cvt_pk_fp8_f32 v28, v72, v73
	v_cvt_pk_fp8_f32 v27, v70, v71 op_sel:[0,0,1]
	v_mul_f32_e32 v76, v76, v9
	v_mul_f32_e32 v77, v77, v9
	v_mul_f32_e32 v78, v78, v9
	v_mul_f32_e32 v79, v79, v9
	v_mov_b32_e32 v29, v10
	v_cvt_pk_fp8_f32 v29, v76, v77
	v_cvt_pk_fp8_f32 v28, v74, v75 op_sel:[0,0,1]
	v_mul_f32_e32 v80, v80, v9
	v_mul_f32_e32 v81, v81, v9
	v_mul_f32_e32 v82, v82, v9
	v_mul_f32_e32 v83, v83, v9
	v_mov_b32_e32 v30, v10
	v_cvt_pk_fp8_f32 v30, v80, v81
	v_cvt_pk_fp8_f32 v29, v78, v79 op_sel:[0,0,1]
	v_mul_f32_e32 v84, v84, v9
	v_mul_f32_e32 v85, v85, v9
	v_mul_f32_e32 v86, v86, v9
	v_mul_f32_e32 v87, v87, v9
	v_mov_b32_e32 v31, v10
	v_cvt_pk_fp8_f32 v31, v84, v85
	v_cvt_pk_fp8_f32 v30, v82, v83 op_sel:[0,0,1]
	v_mul_f32_e32 v88, v88, v9
	v_mul_f32_e32 v89, v89, v9
	v_mul_f32_e32 v90, v90, v9
	v_mul_f32_e32 v91, v91, v9
	v_mov_b32_e32 v32, v10
	v_cvt_pk_fp8_f32 v32, v88, v89
	v_cvt_pk_fp8_f32 v31, v86, v87 op_sel:[0,0,1]
	v_mul_f32_e32 v92, v92, v9
	v_mul_f32_e32 v93, v93, v9
	v_mul_f32_e32 v94, v94, v9
	v_mul_f32_e32 v95, v95, v9
	v_mov_b32_e32 v33, v10
	v_cvt_pk_fp8_f32 v33, v92, v93
	v_cvt_pk_fp8_f32 v32, v90, v91 op_sel:[0,0,1]
	v_mul_f32_e32 v96, v96, v9
	v_mul_f32_e32 v97, v97, v9
	v_mul_f32_e32 v98, v98, v9
	v_mul_f32_e32 v99, v99, v9
	v_mov_b32_e32 v34, v10
	v_cvt_pk_fp8_f32 v34, v96, v97
	v_cvt_pk_fp8_f32 v33, v94, v95 op_sel:[0,0,1]
	v_mul_f32_e32 v100, v100, v9
	v_mul_f32_e32 v101, v101, v9
	v_mul_f32_e32 v102, v102, v9
	v_mul_f32_e32 v103, v103, v9
	v_mov_b32_e32 v35, v10
	v_cvt_pk_fp8_f32 v35, v100, v101
	v_cvt_pk_fp8_f32 v34, v98, v99 op_sel:[0,0,1]
	v_cvt_pk_fp8_f32 v35, v102, v103 op_sel:[0,0,1]
	s_nop 0
	v_mul_f32_e32 v8, 0x3b800000, v6
	global_store_dword v2, v20, s[8:9]
	global_store_dword v2, v21, s[8:9] offset:256
	global_store_dword v2, v22, s[8:9] offset:512
	global_store_dword v2, v23, s[8:9] offset:768
	global_store_dword v2, v24, s[8:9] offset:1024
	global_store_dword v2, v25, s[8:9] offset:1280
	global_store_dword v2, v26, s[8:9] offset:1536
	global_store_dword v2, v27, s[8:9] offset:1792
	global_store_dword v2, v28, s[8:9] offset:2048
	global_store_dword v2, v29, s[8:9] offset:2304
	global_store_dword v2, v30, s[8:9] offset:2560
	global_store_dword v2, v31, s[8:9] offset:2816
	global_store_dword v2, v32, s[8:9] offset:3072
	global_store_dword v2, v33, s[8:9] offset:3328
	global_store_dword v2, v34, s[8:9] offset:3584
	global_store_dword v2, v35, s[8:9] offset:3840
	s_mov_b64 s[18:19], exec
	s_mov_b64 exec, s[12:13]
	global_store_dword v10, v8, s[10:11]
	s_mov_b64 exec, s[18:19]
	s_mov_b32 s4, s5
	s_add_i32 s5, s4, 1024
	s_lshl_b32 s1, s5, 14
	s_add_u32 s6, s84, s1
	s_addc_u32 s7, s85, 0
	global_load_dwordx4 v[40:43], v1, s[6:7]
	global_load_dwordx4 v[44:47], v1, s[6:7] offset:1024
	global_load_dwordx4 v[48:51], v1, s[6:7] offset:2048
	global_load_dwordx4 v[52:55], v1, s[6:7] offset:3072
	global_load_dwordx4 v[56:59], v3, s[6:7]
	global_load_dwordx4 v[60:63], v3, s[6:7] offset:1024
	global_load_dwordx4 v[64:67], v3, s[6:7] offset:2048
	global_load_dwordx4 v[68:71], v3, s[6:7] offset:3072
	global_load_dwordx4 v[72:75], v4, s[6:7]
	global_load_dwordx4 v[76:79], v4, s[6:7] offset:1024
	global_load_dwordx4 v[80:83], v4, s[6:7] offset:2048
	global_load_dwordx4 v[84:87], v4, s[6:7] offset:3072
	global_load_dwordx4 v[88:91], v5, s[6:7]
	global_load_dwordx4 v[92:95], v5, s[6:7] offset:1024
	global_load_dwordx4 v[96:99], v5, s[6:7] offset:2048
	global_load_dwordx4 v[100:103], v5, s[6:7] offset:3072
	s_waitcnt vmcnt(48)
	v_max3_f32 v6, |v104|, |v105|, 0
	v_max3_f32 v6, |v106|, |v107|, v6
	s_waitcnt vmcnt(47)
	v_max3_f32 v6, |v108|, |v109|, v6
	v_max3_f32 v6, |v110|, |v111|, v6
	s_waitcnt vmcnt(46)
	v_max3_f32 v6, |v112|, |v113|, v6
	v_max3_f32 v6, |v114|, |v115|, v6
	s_waitcnt vmcnt(45)
	v_max3_f32 v6, |v116|, |v117|, v6
	v_max3_f32 v6, |v118|, |v119|, v6
	s_waitcnt vmcnt(44)
	v_max3_f32 v6, |v120|, |v121|, v6
	v_max3_f32 v6, |v122|, |v123|, v6
	s_waitcnt vmcnt(43)
	v_max3_f32 v6, |v124|, |v125|, v6
	v_max3_f32 v6, |v126|, |v127|, v6
	s_waitcnt vmcnt(42)
	v_max3_f32 v6, |v128|, |v129|, v6
	v_max3_f32 v6, |v130|, |v131|, v6
	s_waitcnt vmcnt(41)
	v_max3_f32 v6, |v132|, |v133|, v6
	v_max3_f32 v6, |v134|, |v135|, v6
	s_waitcnt vmcnt(40)
	v_max3_f32 v6, |v136|, |v137|, v6
	v_max3_f32 v6, |v138|, |v139|, v6
	s_waitcnt vmcnt(39)
	v_max3_f32 v6, |v140|, |v141|, v6
	v_max3_f32 v6, |v142|, |v143|, v6
	s_waitcnt vmcnt(38)
	v_max3_f32 v6, |v144|, |v145|, v6
	v_max3_f32 v6, |v146|, |v147|, v6
	s_waitcnt vmcnt(37)
	v_max3_f32 v6, |v148|, |v149|, v6
	v_max3_f32 v6, |v150|, |v151|, v6
	s_waitcnt vmcnt(36)
; __device__ __forceinline__ void peer_row_load(f32x4 (&v)[16], const float* const (&in)[34], int it, int layer, int lane) {
;     const int tbl = it >= NEXP, r = it - tbl * NEXP + layer * NEXP;
;     const f32x4* src = (const f32x4*)((tbl ? in[33] : in[32]) + (size_t)r * D) + lane;
; #pragma unroll
;     for (int j = 0; j < 16; ++j) v[j] = src[64 * j];
; }
; __device__ __forceinline__ void peer_row_store(const f32x4 (&v)[16], unsigned char* ws, int it, int layer, int lane) {
;     const int tbl = it >= NEXP, r = it - tbl * NEXP + layer * NEXP;
;     float am = 0.f;
; #pragma unroll
;     for (int j = 0; j < 16; ++j) am = fmaxf(fmaxf(am, fmaxf(fabsf(v[j][0]), fabsf(v[j][1]))), fmaxf(fabsf(v[j][2]), fabsf(v[j][3])));
;     am = __uint_as_float(max64u(__float_as_uint(am)));
;     const float q = am > 0.f ? 256.0f / am : 0.f;
;     unsigned* dst = (unsigned*)(ws + (tbl ? WS_PV : WS_PU) + (size_t)r * D) + lane;
;     if (tbl) {
;         const int rl = it - NEXP;
;         unsigned char* pvl = ws + WS_PV + (size_t)layer * NEXP * D + (size_t)rl * 8 + (lane & 1) * 4;
;         unsigned char* pvg = ws + WS_PV + (size_t)layer * NEXP * D + (size_t)NEXP * 2048 + (size_t)rl * 2048 + 4 * lane;
; #pragma unroll
;         for (int j = 0; j < 16; ++j) { int w = __builtin_amdgcn_cvt_pk_bf8_f32(v[j][0] * q, v[j][1] * q, 0, false); w = __builtin_amdgcn_cvt_pk_bf8_f32(v[j][2] * q, v[j][3] * q, w, true);
;             if (j < 8) *(unsigned*)(pvl + (size_t)((lane >> 1) + 32 * j) * (NEXP * 8)) = (unsigned)w;
;             else *(unsigned*)(pvg + 256 * (j - 8)) = (unsigned)w; }
;     } else {
; #pragma unroll
;         for (int j = 0; j < 16; ++j) { int w = __builtin_amdgcn_cvt_pk_fp8_f32(v[j][0] * q, v[j][1] * q, 0, false); w = __builtin_amdgcn_cvt_pk_fp8_f32(v[j][2] * q, v[j][3] * q, w, true); dst[64 * j] = (unsigned)w; }
;     }
;     if (lane == 0) ((float*)(ws + (tbl ? WS_SV : WS_SU)))[r] = am * (1.0f / 256.0f);
	v_max3_f32 v6, |v152|, |v153|, v6
	v_max3_f32 v6, |v154|, |v155|, v6
	s_waitcnt vmcnt(35)
	v_max3_f32 v6, |v156|, |v157|, v6
	v_max3_f32 v6, |v158|, |v159|, v6
	s_waitcnt vmcnt(34)
	v_max3_f32 v6, |v160|, |v161|, v6
	v_max3_f32 v6, |v162|, |v163|, v6
	s_waitcnt vmcnt(33)
	v_max3_f32 v6, |v164|, |v165|, v6
	v_max3_f32 v6, |v166|, |v167|, v6
	s_nop 1
	v_max_u32_dpp v6, v6, v6 quad_perm:[1,0,3,2] row_mask:0xf bank_mask:0xf bound_ctrl:1
	s_nop 1
	v_max_u32_dpp v6, v6, v6 quad_perm:[2,3,0,1] row_mask:0xf bank_mask:0xf bound_ctrl:1
	s_nop 1
	v_max_u32_dpp v6, v6, v6 row_half_mirror row_mask:0xf bank_mask:0xf bound_ctrl:1
	s_nop 1
	v_max_u32_dpp v6, v6, v6 row_mirror row_mask:0xf bank_mask:0xf bound_ctrl:1
	s_nop 1
	v_mov_b32_e32 v7, v6
	s_nop 1
	v_permlane16_swap_b32_e32 v6, v7
	v_max_u32_e32 v6, v6, v7
	v_mov_b32_e32 v7, v6
	s_nop 1
	v_permlane32_swap_b32_e32 v6, v7
	v_max_u32_e32 v6, v6, v7
	v_div_scale_f32 v12, s[16:17], v6, v6, s14
	v_rcp_f32_e32 v13, v12
	s_nop 0
	v_fma_f32 v14, -v12, v13, 1.0
	v_fmac_f32_e32 v13, v14, v13
	v_div_scale_f32 v14, vcc, s14, v6, s14
	v_mul_f32_e32 v15, v14, v13
	v_fma_f32 v16, -v12, v15, v14
	v_fmac_f32_e32 v15, v16, v13
	v_fma_f32 v12, -v12, v15, v14
	v_div_fmas_f32 v12, v12, v13, v15
	v_div_fixup_f32 v9, v12, v6, s14
	v_cmp_lt_f32_e32 vcc, 0, v6
	s_nop 1
	v_cndmask_b32_e32 v9, 0, v9, vcc
	s_lshl_b32 s1, s4, 12
	s_add_u32 s8, s90, 0xba00000
	s_addc_u32 s9, s91, 0
	s_add_u32 s8, s8, s1
	s_addc_u32 s9, s9, 0
	s_lshl_b32 s1, s4, 2
	s_add_u32 s10, s90, 0x1ba00000
	s_addc_u32 s11, s91, 0
	s_add_u32 s10, s10, s1
	s_addc_u32 s11, s11, 0
	v_mul_f32_e32 v104, v104, v9
	v_mul_f32_e32 v105, v105, v9
	v_mul_f32_e32 v106, v106, v9
	v_mul_f32_e32 v107, v107, v9
	v_mov_b32_e32 v20, v10
	v_cvt_pk_fp8_f32 v20, v104, v105
	v_mul_f32_e32 v108, v108, v9
	v_mul_f32_e32 v109, v109, v9
	v_mul_f32_e32 v110, v110, v9
	v_mul_f32_e32 v111, v111, v9
	v_mov_b32_e32 v21, v10
	v_cvt_pk_fp8_f32 v21, v108, v109
	v_cvt_pk_fp8_f32 v20, v106, v107 op_sel:[0,0,1]
	v_mul_f32_e32 v112, v112, v9
	v_mul_f32_e32 v113, v113, v9
	v_mul_f32_e32 v114, v114, v9
	v_mul_f32_e32 v115, v115, v9
	v_mov_b32_e32 v22, v10
	v_cvt_pk_fp8_f32 v22, v112, v113
	v_cvt_pk_fp8_f32 v21, v110, v111 op_sel:[0,0,1]
	v_mul_f32_e32 v116, v116, v9
	v_mul_f32_e32 v117, v117, v9
	v_mul_f32_e32 v118, v118, v9
	v_mul_f32_e32 v119, v119, v9
	v_mov_b32_e32 v23, v10
	v_cvt_pk_fp8_f32 v23, v116, v117
	v_cvt_pk_fp8_f32 v22, v114, v115 op_sel:[0,0,1]
	v_mul_f32_e32 v120, v120, v9
	v_mul_f32_e32 v121, v121, v9
	v_mul_f32_e32 v122, v122, v9
	v_mul_f32_e32 v123, v123, v9
	v_mov_b32_e32 v24, v10
	v_cvt_pk_fp8_f32 v24, v120, v121
	v_cvt_pk_fp8_f32 v23, v118, v119 op_sel:[0,0,1]
	v_mul_f32_e32 v124, v124, v9
	v_mul_f32_e32 v125, v125, v9
	v_mul_f32_e32 v126, v126, v9
	v_mul_f32_e32 v127, v127, v9
	v_mov_b32_e32 v25, v10
	v_cvt_pk_fp8_f32 v25, v124, v125
	v_cvt_pk_fp8_f32 v24, v122, v123 op_sel:[0,0,1]
	v_mul_f32_e32 v128, v128, v9
	v_mul_f32_e32 v129, v129, v9
	v_mul_f32_e32 v130, v130, v9
	v_mul_f32_e32 v131, v131, v9
	v_mov_b32_e32 v26, v10
	v_cvt_pk_fp8_f32 v26, v128, v129
	v_cvt_pk_fp8_f32 v25, v126, v127 op_sel:[0,0,1]
	v_mul_f32_e32 v132, v132, v9
	v_mul_f32_e32 v133, v133, v9
	v_mul_f32_e32 v134, v134, v9
	v_mul_f32_e32 v135, v135, v9
	v_mov_b32_e32 v27, v10
	v_cvt_pk_fp8_f32 v27, v132, v133
	v_cvt_pk_fp8_f32 v26, v130, v131 op_sel:[0,0,1]
	v_mul_f32_e32 v136, v136, v9
	v_mul_f32_e32 v137, v137, v9
	v_mul_f32_e32 v138, v138, v9
	v_mul_f32_e32 v139, v139, v9
	v_mov_b32_e32 v28, v10
	v_cvt_pk_fp8_f32 v28, v136, v137
	v_cvt_pk_fp8_f32 v27, v134, v135 op_sel:[0,0,1]
	v_mul_f32_e32 v140, v140, v9
	v_mul_f32_e32 v141, v141, v9
	v_mul_f32_e32 v142, v142, v9
	v_mul_f32_e32 v143, v143, v9
	v_mov_b32_e32 v29, v10
	v_cvt_pk_fp8_f32 v29, v140, v141
	v_cvt_pk_fp8_f32 v28, v138, v139 op_sel:[0,0,1]
	v_mul_f32_e32 v144, v144, v9
	v_mul_f32_e32 v145, v145, v9
	v_mul_f32_e32 v146, v146, v9
	v_mul_f32_e32 v147, v147, v9
	v_mov_b32_e32 v30, v10
	v_cvt_pk_fp8_f32 v30, v144, v145
	v_cvt_pk_fp8_f32 v29, v142, v143 op_sel:[0,0,1]
	v_mul_f32_e32 v148, v148, v9
	v_mul_f32_e32 v149, v149, v9
	v_mul_f32_e32 v150, v150, v9
	v_mul_f32_e32 v151, v151, v9
	v_mov_b32_e32 v31, v10
	v_cvt_pk_fp8_f32 v31, v148, v149
	v_cvt_pk_fp8_f32 v30, v146, v147 op_sel:[0,0,1]
	v_mul_f32_e32 v152, v152, v9
	v_mul_f32_e32 v153, v153, v9
	v_mul_f32_e32 v154, v154, v9
	v_mul_f32_e32 v155, v155, v9
	v_mov_b32_e32 v32, v10
	v_cvt_pk_fp8_f32 v32, v152, v153
	v_cvt_pk_fp8_f32 v31, v150, v151 op_sel:[0,0,1]
	v_mul_f32_e32 v156, v156, v9
	v_mul_f32_e32 v157, v157, v9
	v_mul_f32_e32 v158, v158, v9
	v_mul_f32_e32 v159, v159, v9
	v_mov_b32_e32 v33, v10
	v_cvt_pk_fp8_f32 v33, v156, v157
	v_cvt_pk_fp8_f32 v32, v154, v155 op_sel:[0,0,1]
	v_mul_f32_e32 v160, v160, v9
	v_mul_f32_e32 v161, v161, v9
	v_mul_f32_e32 v162, v162, v9
	v_mul_f32_e32 v163, v163, v9
	v_mov_b32_e32 v34, v10
	v_cvt_pk_fp8_f32 v34, v160, v161
	v_cvt_pk_fp8_f32 v33, v158, v159 op_sel:[0,0,1]
	v_mul_f32_e32 v164, v164, v9
	v_mul_f32_e32 v165, v165, v9
	v_mul_f32_e32 v166, v166, v9
	v_mul_f32_e32 v167, v167, v9
	v_mov_b32_e32 v35, v10
	v_cvt_pk_fp8_f32 v35, v164, v165
	v_cvt_pk_fp8_f32 v34, v162, v163 op_sel:[0,0,1]
	v_cvt_pk_fp8_f32 v35, v166, v167 op_sel:[0,0,1]
	s_nop 0
	v_mul_f32_e32 v8, 0x3b800000, v6
	global_store_dword v2, v20, s[8:9]
	global_store_dword v2, v21, s[8:9] offset:256
	global_store_dword v2, v22, s[8:9] offset:512
	global_store_dword v2, v23, s[8:9] offset:768
	global_store_dword v2, v24, s[8:9] offset:1024
	global_store_dword v2, v25, s[8:9] offset:1280
	global_store_dword v2, v26, s[8:9] offset:1536
	global_store_dword v2, v27, s[8:9] offset:1792
; __device__ __forceinline__ void peer_row_load(f32x4 (&v)[16], const float* const (&in)[34], int it, int layer, int lane) {
;     const int tbl = it >= NEXP, r = it - tbl * NEXP + layer * NEXP;
;     const f32x4* src = (const f32x4*)((tbl ? in[33] : in[32]) + (size_t)r * D) + lane;
; #pragma unroll
;     for (int j = 0; j < 16; ++j) v[j] = src[64 * j];
; }
; __device__ __forceinline__ void peer_row_store(const f32x4 (&v)[16], unsigned char* ws, int it, int layer, int lane) {
;     const int tbl = it >= NEXP, r = it - tbl * NEXP + layer * NEXP;
;     float am = 0.f;
; #pragma unroll
;     for (int j = 0; j < 16; ++j) am = fmaxf(fmaxf(am, fmaxf(fabsf(v[j][0]), fabsf(v[j][1]))), fmaxf(fabsf(v[j][2]), fabsf(v[j][3])));
;     am = __uint_as_float(max64u(__float_as_uint(am)));
;     const float q = am > 0.f ? 256.0f / am : 0.f;
;     unsigned* dst = (unsigned*)(ws + (tbl ? WS_PV : WS_PU) + (size_t)r * D) + lane;
;     if (tbl) {
;         const int rl = it - NEXP;
;         unsigned char* pvl = ws + WS_PV + (size_t)layer * NEXP * D + (size_t)rl * 8 + (lane & 1) * 4;
;         unsigned char* pvg = ws + WS_PV + (size_t)layer * NEXP * D + (size_t)NEXP * 2048 + (size_t)rl * 2048 + 4 * lane;
; #pragma unroll
;         for (int j = 0; j < 16; ++j) { int w = __builtin_amdgcn_cvt_pk_bf8_f32(v[j][0] * q, v[j][1] * q, 0, false); w = __builtin_amdgcn_cvt_pk_bf8_f32(v[j][2] * q, v[j][3] * q, w, true);
;             if (j < 8) *(unsigned*)(pvl + (size_t)((lane >> 1) + 32 * j) * (NEXP * 8)) = (unsigned)w;
;             else *(unsigned*)(pvg + 256 * (j - 8)) = (unsigned)w; }
;     } else {
; #pragma unroll
;         for (int j = 0; j < 16; ++j) { int w = __builtin_amdgcn_cvt_pk_fp8_f32(v[j][0] * q, v[j][1] * q, 0, false); w = __builtin_amdgcn_cvt_pk_fp8_f32(v[j][2] * q, v[j][3] * q, w, true); dst[64 * j] = (unsigned)w; }
;     }
;     if (lane == 0) ((float*)(ws + (tbl ? WS_SV : WS_SU)))[r] = am * (1.0f / 256.0f);
	global_store_dword v2, v28, s[8:9] offset:2048
	global_store_dword v2, v29, s[8:9] offset:2304
	global_store_dword v2, v30, s[8:9] offset:2560
	global_store_dword v2, v31, s[8:9] offset:2816
	global_store_dword v2, v32, s[8:9] offset:3072
	global_store_dword v2, v33, s[8:9] offset:3328
	global_store_dword v2, v34, s[8:9] offset:3584
	global_store_dword v2, v35, s[8:9] offset:3840
	s_mov_b64 s[18:19], exec
	s_mov_b64 exec, s[12:13]
	global_store_dword v10, v8, s[10:11]
	s_mov_b64 exec, s[18:19]
	s_mov_b32 s4, s5
	s_add_i32 s5, s4, 1024
	s_lshl_b32 s1, s5, 14
	s_add_u32 s6, s84, s1
	s_addc_u32 s7, s85, 0
	global_load_dwordx4 v[104:107], v1, s[6:7]
	global_load_dwordx4 v[108:111], v1, s[6:7] offset:1024
	global_load_dwordx4 v[112:115], v1, s[6:7] offset:2048
	global_load_dwordx4 v[116:119], v1, s[6:7] offset:3072
	global_load_dwordx4 v[120:123], v3, s[6:7]
	global_load_dwordx4 v[124:127], v3, s[6:7] offset:1024
	global_load_dwordx4 v[128:131], v3, s[6:7] offset:2048
	global_load_dwordx4 v[132:135], v3, s[6:7] offset:3072
	global_load_dwordx4 v[136:139], v4, s[6:7]
	global_load_dwordx4 v[140:143], v4, s[6:7] offset:1024
	global_load_dwordx4 v[144:147], v4, s[6:7] offset:2048
	global_load_dwordx4 v[148:151], v4, s[6:7] offset:3072
	global_load_dwordx4 v[152:155], v5, s[6:7]
	global_load_dwordx4 v[156:159], v5, s[6:7] offset:1024
	global_load_dwordx4 v[160:163], v5, s[6:7] offset:2048
	global_load_dwordx4 v[164:167], v5, s[6:7] offset:3072
	s_waitcnt vmcnt(48)
	v_max3_f32 v6, |v40|, |v41|, 0
	v_max3_f32 v6, |v42|, |v43|, v6
	s_waitcnt vmcnt(47)
	v_max3_f32 v6, |v44|, |v45|, v6
	v_max3_f32 v6, |v46|, |v47|, v6
	s_waitcnt vmcnt(46)
	v_max3_f32 v6, |v48|, |v49|, v6
	v_max3_f32 v6, |v50|, |v51|, v6
	s_waitcnt vmcnt(45)
	v_max3_f32 v6, |v52|, |v53|, v6
	v_max3_f32 v6, |v54|, |v55|, v6
	s_waitcnt vmcnt(44)
	v_max3_f32 v6, |v56|, |v57|, v6
	v_max3_f32 v6, |v58|, |v59|, v6
	s_waitcnt vmcnt(43)
	v_max3_f32 v6, |v60|, |v61|, v6
	v_max3_f32 v6, |v62|, |v63|, v6
	s_waitcnt vmcnt(42)
	v_max3_f32 v6, |v64|, |v65|, v6
	v_max3_f32 v6, |v66|, |v67|, v6
	s_waitcnt vmcnt(41)
	v_max3_f32 v6, |v68|, |v69|, v6
	v_max3_f32 v6, |v70|, |v71|, v6
	s_waitcnt vmcnt(40)
	v_max3_f32 v6, |v72|, |v73|, v6
	v_max3_f32 v6, |v74|, |v75|, v6
	s_waitcnt vmcnt(39)
	v_max3_f32 v6, |v76|, |v77|, v6
	v_max3_f32 v6, |v78|, |v79|, v6
	s_waitcnt vmcnt(38)
	v_max3_f32 v6, |v80|, |v81|, v6
	v_max3_f32 v6, |v82|, |v83|, v6
	s_waitcnt vmcnt(37)
	v_max3_f32 v6, |v84|, |v85|, v6
	v_max3_f32 v6, |v86|, |v87|, v6
	s_waitcnt vmcnt(36)
	v_max3_f32 v6, |v88|, |v89|, v6
	v_max3_f32 v6, |v90|, |v91|, v6
	s_waitcnt vmcnt(35)
	v_max3_f32 v6, |v92|, |v93|, v6
	v_max3_f32 v6, |v94|, |v95|, v6
	s_waitcnt vmcnt(34)
	v_max3_f32 v6, |v96|, |v97|, v6
	v_max3_f32 v6, |v98|, |v99|, v6
	s_waitcnt vmcnt(33)
	v_max3_f32 v6, |v100|, |v101|, v6
	v_max3_f32 v6, |v102|, |v103|, v6
	s_nop 1
	v_max_u32_dpp v6, v6, v6 quad_perm:[1,0,3,2] row_mask:0xf bank_mask:0xf bound_ctrl:1
	s_nop 1
	v_max_u32_dpp v6, v6, v6 quad_perm:[2,3,0,1] row_mask:0xf bank_mask:0xf bound_ctrl:1
	s_nop 1
	v_max_u32_dpp v6, v6, v6 row_half_mirror row_mask:0xf bank_mask:0xf bound_ctrl:1
	s_nop 1
	v_max_u32_dpp v6, v6, v6 row_mirror row_mask:0xf bank_mask:0xf bound_ctrl:1
	s_nop 1
	v_mov_b32_e32 v7, v6
	s_nop 1
	v_permlane16_swap_b32_e32 v6, v7
	v_max_u32_e32 v6, v6, v7
	v_mov_b32_e32 v7, v6
	s_nop 1
	v_permlane32_swap_b32_e32 v6, v7
	v_max_u32_e32 v6, v6, v7
	v_div_scale_f32 v12, s[16:17], v6, v6, s14
	v_rcp_f32_e32 v13, v12
	s_nop 0
	v_fma_f32 v14, -v12, v13, 1.0
	v_fmac_f32_e32 v13, v14, v13
	v_div_scale_f32 v14, vcc, s14, v6, s14
	v_mul_f32_e32 v15, v14, v13
	v_fma_f32 v16, -v12, v15, v14
	v_fmac_f32_e32 v15, v16, v13
	v_fma_f32 v12, -v12, v15, v14
	v_div_fmas_f32 v12, v12, v13, v15
	v_div_fixup_f32 v9, v12, v6, s14
	v_cmp_lt_f32_e32 vcc, 0, v6
	s_nop 1
	v_cndmask_b32_e32 v9, 0, v9, vcc
	s_lshl_b32 s1, s4, 12
	s_add_u32 s8, s90, 0xba00000
	s_addc_u32 s9, s91, 0
	s_add_u32 s8, s8, s1
	s_addc_u32 s9, s9, 0
	s_lshl_b32 s1, s4, 2
	s_add_u32 s10, s90, 0x1ba00000
	s_addc_u32 s11, s91, 0
	s_add_u32 s10, s10, s1
	s_addc_u32 s11, s11, 0
	v_mul_f32_e32 v40, v40, v9
	v_mul_f32_e32 v41, v41, v9
	v_mul_f32_e32 v42, v42, v9
	v_mul_f32_e32 v43, v43, v9
	v_mov_b32_e32 v20, v10
	v_cvt_pk_fp8_f32 v20, v40, v41
	v_mul_f32_e32 v44, v44, v9
	v_mul_f32_e32 v45, v45, v9
	v_mul_f32_e32 v46, v46, v9
	v_mul_f32_e32 v47, v47, v9
	v_mov_b32_e32 v21, v10
	v_cvt_pk_fp8_f32 v21, v44, v45
	v_cvt_pk_fp8_f32 v20, v42, v43 op_sel:[0,0,1]
	v_mul_f32_e32 v48, v48, v9
	v_mul_f32_e32 v49, v49, v9
	v_mul_f32_e32 v50, v50, v9
	v_mul_f32_e32 v51, v51, v9
	v_mov_b32_e32 v22, v10
	v_cvt_pk_fp8_f32 v22, v48, v49
	v_cvt_pk_fp8_f32 v21, v46, v47 op_sel:[0,0,1]
	v_mul_f32_e32 v52, v52, v9
	v_mul_f32_e32 v53, v53, v9
	v_mul_f32_e32 v54, v54, v9
	v_mul_f32_e32 v55, v55, v9
	v_mov_b32_e32 v23, v10
	v_cvt_pk_fp8_f32 v23, v52, v53
	v_cvt_pk_fp8_f32 v22, v50, v51 op_sel:[0,0,1]
	v_mul_f32_e32 v56, v56, v9
	v_mul_f32_e32 v57, v57, v9
	v_mul_f32_e32 v58, v58, v9
	v_mul_f32_e32 v59, v59, v9
	v_mov_b32_e32 v24, v10
	v_cvt_pk_fp8_f32 v24, v56, v57
	v_cvt_pk_fp8_f32 v23, v54, v55 op_sel:[0,0,1]
	v_mul_f32_e32 v60, v60, v9
	v_mul_f32_e32 v61, v61, v9
	v_mul_f32_e32 v62, v62, v9
	v_mul_f32_e32 v63, v63, v9
	v_mov_b32_e32 v25, v10
	v_cvt_pk_fp8_f32 v25, v60, v61
	v_cvt_pk_fp8_f32 v24, v58, v59 op_sel:[0,0,1]
	v_mul_f32_e32 v64, v64, v9
	v_mul_f32_e32 v65, v65, v9
	v_mul_f32_e32 v66, v66, v9
	v_mul_f32_e32 v67, v67, v9
	v_mov_b32_e32 v26, v10
	v_cvt_pk_fp8_f32 v26, v64, v65
	v_cvt_pk_fp8_f32 v25, v62, v63 op_sel:[0,0,1]
	v_mul_f32_e32 v68, v68, v9
	v_mul_f32_e32 v69, v69, v9
	v_mul_f32_e32 v70, v70, v9
; __device__ __forceinline__ void peer_row_load(f32x4 (&v)[16], const float* const (&in)[34], int it, int layer, int lane) {
;     const int tbl = it >= NEXP, r = it - tbl * NEXP + layer * NEXP;
;     const f32x4* src = (const f32x4*)((tbl ? in[33] : in[32]) + (size_t)r * D) + lane;
; #pragma unroll
;     for (int j = 0; j < 16; ++j) v[j] = src[64 * j];
; }
; __device__ __forceinline__ void peer_row_store(const f32x4 (&v)[16], unsigned char* ws, int it, int layer, int lane) {
;     const int tbl = it >= NEXP, r = it - tbl * NEXP + layer * NEXP;
;     float am = 0.f;
; #pragma unroll
;     for (int j = 0; j < 16; ++j) am = fmaxf(fmaxf(am, fmaxf(fabsf(v[j][0]), fabsf(v[j][1]))), fmaxf(fabsf(v[j][2]), fabsf(v[j][3])));
;     am = __uint_as_float(max64u(__float_as_uint(am)));
;     const float q = am > 0.f ? 256.0f / am : 0.f;
;     unsigned* dst = (unsigned*)(ws + (tbl ? WS_PV : WS_PU) + (size_t)r * D) + lane;
;     if (tbl) {
;         const int rl = it - NEXP;
;         unsigned char* pvl = ws + WS_PV + (size_t)layer * NEXP * D + (size_t)rl * 8 + (lane & 1) * 4;
;         unsigned char* pvg = ws + WS_PV + (size_t)layer * NEXP * D + (size_t)NEXP * 2048 + (size_t)rl * 2048 + 4 * lane;
; #pragma unroll
;         for (int j = 0; j < 16; ++j) { int w = __builtin_amdgcn_cvt_pk_bf8_f32(v[j][0] * q, v[j][1] * q, 0, false); w = __builtin_amdgcn_cvt_pk_bf8_f32(v[j][2] * q, v[j][3] * q, w, true);
;             if (j < 8) *(unsigned*)(pvl + (size_t)((lane >> 1) + 32 * j) * (NEXP * 8)) = (unsigned)w;
;             else *(unsigned*)(pvg + 256 * (j - 8)) = (unsigned)w; }
;     } else {
; #pragma unroll
;         for (int j = 0; j < 16; ++j) { int w = __builtin_amdgcn_cvt_pk_fp8_f32(v[j][0] * q, v[j][1] * q, 0, false); w = __builtin_amdgcn_cvt_pk_fp8_f32(v[j][2] * q, v[j][3] * q, w, true); dst[64 * j] = (unsigned)w; }
;     }
;     if (lane == 0) ((float*)(ws + (tbl ? WS_SV : WS_SU)))[r] = am * (1.0f / 256.0f);
	v_mul_f32_e32 v71, v71, v9
	v_mov_b32_e32 v27, v10
	v_cvt_pk_fp8_f32 v27, v68, v69
	v_cvt_pk_fp8_f32 v26, v66, v67 op_sel:[0,0,1]
	v_mul_f32_e32 v72, v72, v9
	v_mul_f32_e32 v73, v73, v9
	v_mul_f32_e32 v74, v74, v9
	v_mul_f32_e32 v75, v75, v9
	v_mov_b32_e32 v28, v10
	v_cvt_pk_fp8_f32 v28, v72, v73
	v_cvt_pk_fp8_f32 v27, v70, v71 op_sel:[0,0,1]
	v_mul_f32_e32 v76, v76, v9
	v_mul_f32_e32 v77, v77, v9
	v_mul_f32_e32 v78, v78, v9
	v_mul_f32_e32 v79, v79, v9
	v_mov_b32_e32 v29, v10
	v_cvt_pk_fp8_f32 v29, v76, v77
	v_cvt_pk_fp8_f32 v28, v74, v75 op_sel:[0,0,1]
	v_mul_f32_e32 v80, v80, v9
	v_mul_f32_e32 v81, v81, v9
	v_mul_f32_e32 v82, v82, v9
	v_mul_f32_e32 v83, v83, v9
	v_mov_b32_e32 v30, v10
	v_cvt_pk_fp8_f32 v30, v80, v81
	v_cvt_pk_fp8_f32 v29, v78, v79 op_sel:[0,0,1]
	v_mul_f32_e32 v84, v84, v9
	v_mul_f32_e32 v85, v85, v9
	v_mul_f32_e32 v86, v86, v9
	v_mul_f32_e32 v87, v87, v9
	v_mov_b32_e32 v31, v10
	v_cvt_pk_fp8_f32 v31, v84, v85
	v_cvt_pk_fp8_f32 v30, v82, v83 op_sel:[0,0,1]
	v_mul_f32_e32 v88, v88, v9
	v_mul_f32_e32 v89, v89, v9
	v_mul_f32_e32 v90, v90, v9
	v_mul_f32_e32 v91, v91, v9
	v_mov_b32_e32 v32, v10
	v_cvt_pk_fp8_f32 v32, v88, v89
	v_cvt_pk_fp8_f32 v31, v86, v87 op_sel:[0,0,1]
	v_mul_f32_e32 v92, v92, v9
	v_mul_f32_e32 v93, v93, v9
	v_mul_f32_e32 v94, v94, v9
	v_mul_f32_e32 v95, v95, v9
	v_mov_b32_e32 v33, v10
	v_cvt_pk_fp8_f32 v33, v92, v93
	v_cvt_pk_fp8_f32 v32, v90, v91 op_sel:[0,0,1]
	v_mul_f32_e32 v96, v96, v9
	v_mul_f32_e32 v97, v97, v9
	v_mul_f32_e32 v98, v98, v9
	v_mul_f32_e32 v99, v99, v9
	v_mov_b32_e32 v34, v10
	v_cvt_pk_fp8_f32 v34, v96, v97
	v_cvt_pk_fp8_f32 v33, v94, v95 op_sel:[0,0,1]
	v_mul_f32_e32 v100, v100, v9
	v_mul_f32_e32 v101, v101, v9
	v_mul_f32_e32 v102, v102, v9
	v_mul_f32_e32 v103, v103, v9
	v_mov_b32_e32 v35, v10
	v_cvt_pk_fp8_f32 v35, v100, v101
	v_cvt_pk_fp8_f32 v34, v98, v99 op_sel:[0,0,1]
	v_cvt_pk_fp8_f32 v35, v102, v103 op_sel:[0,0,1]
	s_nop 0
	v_mul_f32_e32 v8, 0x3b800000, v6
	global_store_dword v2, v20, s[8:9]
	global_store_dword v2, v21, s[8:9] offset:256
	global_store_dword v2, v22, s[8:9] offset:512
	global_store_dword v2, v23, s[8:9] offset:768
	global_store_dword v2, v24, s[8:9] offset:1024
	global_store_dword v2, v25, s[8:9] offset:1280
	global_store_dword v2, v26, s[8:9] offset:1536
	global_store_dword v2, v27, s[8:9] offset:1792
	global_store_dword v2, v28, s[8:9] offset:2048
	global_store_dword v2, v29, s[8:9] offset:2304
	global_store_dword v2, v30, s[8:9] offset:2560
	global_store_dword v2, v31, s[8:9] offset:2816
	global_store_dword v2, v32, s[8:9] offset:3072
	global_store_dword v2, v33, s[8:9] offset:3328
	global_store_dword v2, v34, s[8:9] offset:3584
	global_store_dword v2, v35, s[8:9] offset:3840
	s_mov_b64 s[18:19], exec
	s_mov_b64 exec, s[12:13]
	global_store_dword v10, v8, s[10:11]
	s_mov_b64 exec, s[18:19]
	s_mov_b32 s4, s5
	s_add_i32 s5, s4, 1024
	s_lshl_b32 s1, s5, 14
	s_add_u32 s6, s84, s1
	s_addc_u32 s7, s85, 0
	global_load_dwordx4 v[40:43], v1, s[6:7]
	global_load_dwordx4 v[44:47], v1, s[6:7] offset:1024
	global_load_dwordx4 v[48:51], v1, s[6:7] offset:2048
	global_load_dwordx4 v[52:55], v1, s[6:7] offset:3072
	global_load_dwordx4 v[56:59], v3, s[6:7]
	global_load_dwordx4 v[60:63], v3, s[6:7] offset:1024
	global_load_dwordx4 v[64:67], v3, s[6:7] offset:2048
	global_load_dwordx4 v[68:71], v3, s[6:7] offset:3072
	global_load_dwordx4 v[72:75], v4, s[6:7]
	global_load_dwordx4 v[76:79], v4, s[6:7] offset:1024
	global_load_dwordx4 v[80:83], v4, s[6:7] offset:2048
	global_load_dwordx4 v[84:87], v4, s[6:7] offset:3072
	global_load_dwordx4 v[88:91], v5, s[6:7]
	global_load_dwordx4 v[92:95], v5, s[6:7] offset:1024
	global_load_dwordx4 v[96:99], v5, s[6:7] offset:2048
	global_load_dwordx4 v[100:103], v5, s[6:7] offset:3072
	s_waitcnt vmcnt(48)
	v_max3_f32 v6, |v104|, |v105|, 0
	v_max3_f32 v6, |v106|, |v107|, v6
	s_waitcnt vmcnt(47)
	v_max3_f32 v6, |v108|, |v109|, v6
	v_max3_f32 v6, |v110|, |v111|, v6
	s_waitcnt vmcnt(46)
	v_max3_f32 v6, |v112|, |v113|, v6
	v_max3_f32 v6, |v114|, |v115|, v6
	s_waitcnt vmcnt(45)
	v_max3_f32 v6, |v116|, |v117|, v6
	v_max3_f32 v6, |v118|, |v119|, v6
	s_waitcnt vmcnt(44)
	v_max3_f32 v6, |v120|, |v121|, v6
	v_max3_f32 v6, |v122|, |v123|, v6
	s_waitcnt vmcnt(43)
	v_max3_f32 v6, |v124|, |v125|, v6
	v_max3_f32 v6, |v126|, |v127|, v6
	s_waitcnt vmcnt(42)
	v_max3_f32 v6, |v128|, |v129|, v6
	v_max3_f32 v6, |v130|, |v131|, v6
	s_waitcnt vmcnt(41)
	v_max3_f32 v6, |v132|, |v133|, v6
	v_max3_f32 v6, |v134|, |v135|, v6
	s_waitcnt vmcnt(40)
	v_max3_f32 v6, |v136|, |v137|, v6
	v_max3_f32 v6, |v138|, |v139|, v6
	s_waitcnt vmcnt(39)
	v_max3_f32 v6, |v140|, |v141|, v6
	v_max3_f32 v6, |v142|, |v143|, v6
	s_waitcnt vmcnt(38)
	v_max3_f32 v6, |v144|, |v145|, v6
	v_max3_f32 v6, |v146|, |v147|, v6
	s_waitcnt vmcnt(37)
	v_max3_f32 v6, |v148|, |v149|, v6
	v_max3_f32 v6, |v150|, |v151|, v6
	s_waitcnt vmcnt(36)
	v_max3_f32 v6, |v152|, |v153|, v6
	v_max3_f32 v6, |v154|, |v155|, v6
	s_waitcnt vmcnt(35)
	v_max3_f32 v6, |v156|, |v157|, v6
	v_max3_f32 v6, |v158|, |v159|, v6
	s_waitcnt vmcnt(34)
	v_max3_f32 v6, |v160|, |v161|, v6
	v_max3_f32 v6, |v162|, |v163|, v6
	s_waitcnt vmcnt(33)
; __device__ __forceinline__ void peer_row_store(const f32x4 (&v)[16], unsigned char* ws, int it, int layer, int lane) {
;     ...
;     for (int j = 0; j < 16; ++j) am = fmaxf(fmaxf(am, fmaxf(fabsf(v[j][0]), fabsf(v[j][1]))), fmaxf(fabsf(v[j][2]), fabsf(v[j][3])));
;     am = __uint_as_float(max64u(__float_as_uint(am)));
;     const float q = am > 0.f ? 256.0f / am : 0.f;
;     unsigned* dst = (unsigned*)(ws + (tbl ? WS_PV : WS_PU) + (size_t)r * D) + lane;
;     if (tbl) {
;         const int rl = it - NEXP;
;         unsigned char* pvl = ws + WS_PV + (size_t)layer * NEXP * D + (size_t)rl * 8 + (lane & 1) * 4;
;         unsigned char* pvg = ws + WS_PV + (size_t)layer * NEXP * D + (size_t)NEXP * 2048 + (size_t)rl * 2048 + 4 * lane;
; #pragma unroll
;         for (int j = 0; j < 16; ++j) { int w = __builtin_amdgcn_cvt_pk_bf8_f32(v[j][0] * q, v[j][1] * q, 0, false); w = __builtin_amdgcn_cvt_pk_bf8_f32(v[j][2] * q, v[j][3] * q, w, true);
;             if (j < 8) *(unsigned*)(pvl + (size_t)((lane >> 1) + 32 * j) * (NEXP * 8)) = (unsigned)w;
;             else *(unsigned*)(pvg + 256 * (j - 8)) = (unsigned)w; }
;     } else {
; #pragma unroll
;         for (int j = 0; j < 16; ++j) { int w = __builtin_amdgcn_cvt_pk_fp8_f32(v[j][0] * q, v[j][1] * q, 0, false); w = __builtin_amdgcn_cvt_pk_fp8_f32(v[j][2] * q, v[j][3] * q, w, true); dst[64 * j] = (unsigned)w; }
;     }
;     if (lane == 0) ((float*)(ws + (tbl ? WS_SV : WS_SU)))[r] = am * (1.0f / 256.0f);
;     f32x4 va[16], vb[16];
;     if (it_lo + gw >= it_hi) return;
;     peer_row_load(va, in, it_lo + gw, only_layer, lane);
; #pragma unroll 1
;     for (int it = it_lo + gw; it < it_hi; it += 2 * NGW) {
;         const int it1 = it + NGW, it2 = it + 2 * NGW;
;         peer_row_load(vb, in, it1 < it_hi ? it1 : it, only_layer, lane);
;         __builtin_amdgcn_sched_barrier(0);
;         peer_row_store(va, ws, it, only_layer, lane);
;         __builtin_amdgcn_sched_barrier(0);
;         peer_row_load(va, in, it2 < it_hi ? it2 : it, only_layer, lane);
;         __builtin_amdgcn_sched_barrier(0);
;         if (it1 < it_hi) peer_row_store(vb, ws, it1, only_layer, lane);
;         __builtin_amdgcn_sched_barrier(0);
;     }
	v_max3_f32 v6, |v164|, |v165|, v6
	v_max3_f32 v6, |v166|, |v167|, v6
	s_nop 1
	v_max_u32_dpp v6, v6, v6 quad_perm:[1,0,3,2] row_mask:0xf bank_mask:0xf bound_ctrl:1
	s_nop 1
	v_max_u32_dpp v6, v6, v6 quad_perm:[2,3,0,1] row_mask:0xf bank_mask:0xf bound_ctrl:1
	s_nop 1
	v_max_u32_dpp v6, v6, v6 row_half_mirror row_mask:0xf bank_mask:0xf bound_ctrl:1
	s_nop 1
	v_max_u32_dpp v6, v6, v6 row_mirror row_mask:0xf bank_mask:0xf bound_ctrl:1
	s_nop 1
	v_mov_b32_e32 v7, v6
	s_nop 1
	v_permlane16_swap_b32_e32 v6, v7
	v_max_u32_e32 v6, v6, v7
	v_mov_b32_e32 v7, v6
	s_nop 1
	v_permlane32_swap_b32_e32 v6, v7
	v_max_u32_e32 v6, v6, v7
	v_div_scale_f32 v12, s[16:17], v6, v6, s14
	v_rcp_f32_e32 v13, v12
	s_nop 0
	v_fma_f32 v14, -v12, v13, 1.0
	v_fmac_f32_e32 v13, v14, v13
	v_div_scale_f32 v14, vcc, s14, v6, s14
	v_mul_f32_e32 v15, v14, v13
	v_fma_f32 v16, -v12, v15, v14
	v_fmac_f32_e32 v15, v16, v13
	v_fma_f32 v12, -v12, v15, v14
	v_div_fmas_f32 v12, v12, v13, v15
	v_div_fixup_f32 v9, v12, v6, s14
	v_cmp_lt_f32_e32 vcc, 0, v6
	s_nop 1
	v_cndmask_b32_e32 v9, 0, v9, vcc
	s_lshl_b32 s1, s4, 12
	s_add_u32 s8, s90, 0xba00000
	s_addc_u32 s9, s91, 0
	s_add_u32 s8, s8, s1
	s_addc_u32 s9, s9, 0
	s_lshl_b32 s1, s4, 2
	s_add_u32 s10, s90, 0x1ba00000
	s_addc_u32 s11, s91, 0
	s_add_u32 s10, s10, s1
	s_addc_u32 s11, s11, 0
	v_mul_f32_e32 v104, v104, v9
	v_mul_f32_e32 v105, v105, v9
	v_mul_f32_e32 v106, v106, v9
	v_mul_f32_e32 v107, v107, v9
	v_mov_b32_e32 v20, v10
	v_cvt_pk_fp8_f32 v20, v104, v105
	v_mul_f32_e32 v108, v108, v9
	v_mul_f32_e32 v109, v109, v9
	v_mul_f32_e32 v110, v110, v9
	v_mul_f32_e32 v111, v111, v9
	v_mov_b32_e32 v21, v10
	v_cvt_pk_fp8_f32 v21, v108, v109
	v_cvt_pk_fp8_f32 v20, v106, v107 op_sel:[0,0,1]
	v_mul_f32_e32 v112, v112, v9
	v_mul_f32_e32 v113, v113, v9
	v_mul_f32_e32 v114, v114, v9
	v_mul_f32_e32 v115, v115, v9
	v_mov_b32_e32 v22, v10
	v_cvt_pk_fp8_f32 v22, v112, v113
	v_cvt_pk_fp8_f32 v21, v110, v111 op_sel:[0,0,1]
	v_mul_f32_e32 v116, v116, v9
	v_mul_f32_e32 v117, v117, v9
	v_mul_f32_e32 v118, v118, v9
	v_mul_f32_e32 v119, v119, v9
	v_mov_b32_e32 v23, v10
	v_cvt_pk_fp8_f32 v23, v116, v117
	v_cvt_pk_fp8_f32 v22, v114, v115 op_sel:[0,0,1]
	v_mul_f32_e32 v120, v120, v9
	v_mul_f32_e32 v121, v121, v9
	v_mul_f32_e32 v122, v122, v9
	v_mul_f32_e32 v123, v123, v9
	v_mov_b32_e32 v24, v10
	v_cvt_pk_fp8_f32 v24, v120, v121
	v_cvt_pk_fp8_f32 v23, v118, v119 op_sel:[0,0,1]
	v_mul_f32_e32 v124, v124, v9
	v_mul_f32_e32 v125, v125, v9
	v_mul_f32_e32 v126, v126, v9
	v_mul_f32_e32 v127, v127, v9
	v_mov_b32_e32 v25, v10
	v_cvt_pk_fp8_f32 v25, v124, v125
	v_cvt_pk_fp8_f32 v24, v122, v123 op_sel:[0,0,1]
	v_mul_f32_e32 v128, v128, v9
	v_mul_f32_e32 v129, v129, v9
	v_mul_f32_e32 v130, v130, v9
	v_mul_f32_e32 v131, v131, v9
	v_mov_b32_e32 v26, v10
	v_cvt_pk_fp8_f32 v26, v128, v129
	v_cvt_pk_fp8_f32 v25, v126, v127 op_sel:[0,0,1]
	v_mul_f32_e32 v132, v132, v9
	v_mul_f32_e32 v133, v133, v9
	v_mul_f32_e32 v134, v134, v9
	v_mul_f32_e32 v135, v135, v9
	v_mov_b32_e32 v27, v10
	v_cvt_pk_fp8_f32 v27, v132, v133
	v_cvt_pk_fp8_f32 v26, v130, v131 op_sel:[0,0,1]
	v_mul_f32_e32 v136, v136, v9
	v_mul_f32_e32 v137, v137, v9
	v_mul_f32_e32 v138, v138, v9
	v_mul_f32_e32 v139, v139, v9
	v_mov_b32_e32 v28, v10
	v_cvt_pk_fp8_f32 v28, v136, v137
	v_cvt_pk_fp8_f32 v27, v134, v135 op_sel:[0,0,1]
	v_mul_f32_e32 v140, v140, v9
	v_mul_f32_e32 v141, v141, v9
	v_mul_f32_e32 v142, v142, v9
	v_mul_f32_e32 v143, v143, v9
	v_mov_b32_e32 v29, v10
	v_cvt_pk_fp8_f32 v29, v140, v141
	v_cvt_pk_fp8_f32 v28, v138, v139 op_sel:[0,0,1]
	v_mul_f32_e32 v144, v144, v9
	v_mul_f32_e32 v145, v145, v9
	v_mul_f32_e32 v146, v146, v9
	v_mul_f32_e32 v147, v147, v9
	v_mov_b32_e32 v30, v10
	v_cvt_pk_fp8_f32 v30, v144, v145
	v_cvt_pk_fp8_f32 v29, v142, v143 op_sel:[0,0,1]
	v_mul_f32_e32 v148, v148, v9
	v_mul_f32_e32 v149, v149, v9
	v_mul_f32_e32 v150, v150, v9
	v_mul_f32_e32 v151, v151, v9
	v_mov_b32_e32 v31, v10
	v_cvt_pk_fp8_f32 v31, v148, v149
	v_cvt_pk_fp8_f32 v30, v146, v147 op_sel:[0,0,1]
	v_mul_f32_e32 v152, v152, v9
	v_mul_f32_e32 v153, v153, v9
	v_mul_f32_e32 v154, v154, v9
	v_mul_f32_e32 v155, v155, v9
	v_mov_b32_e32 v32, v10
	v_cvt_pk_fp8_f32 v32, v152, v153
	v_cvt_pk_fp8_f32 v31, v150, v151 op_sel:[0,0,1]
	v_mul_f32_e32 v156, v156, v9
	v_mul_f32_e32 v157, v157, v9
	v_mul_f32_e32 v158, v158, v9
	v_mul_f32_e32 v159, v159, v9
	v_mov_b32_e32 v33, v10
	v_cvt_pk_fp8_f32 v33, v156, v157
	v_cvt_pk_fp8_f32 v32, v154, v155 op_sel:[0,0,1]
	v_mul_f32_e32 v160, v160, v9
	v_mul_f32_e32 v161, v161, v9
	v_mul_f32_e32 v162, v162, v9
	v_mul_f32_e32 v163, v163, v9
	v_mov_b32_e32 v34, v10
	v_cvt_pk_fp8_f32 v34, v160, v161
	v_cvt_pk_fp8_f32 v33, v158, v159 op_sel:[0,0,1]
	v_mul_f32_e32 v164, v164, v9
	v_mul_f32_e32 v165, v165, v9
	v_mul_f32_e32 v166, v166, v9
	v_mul_f32_e32 v167, v167, v9
	v_mov_b32_e32 v35, v10
	v_cvt_pk_fp8_f32 v35, v164, v165
	v_cvt_pk_fp8_f32 v34, v162, v163 op_sel:[0,0,1]
	v_cvt_pk_fp8_f32 v35, v166, v167 op_sel:[0,0,1]
	s_nop 0
	v_mul_f32_e32 v8, 0x3b800000, v6
	global_store_dword v2, v20, s[8:9]
	global_store_dword v2, v21, s[8:9] offset:256
	global_store_dword v2, v22, s[8:9] offset:512
	global_store_dword v2, v23, s[8:9] offset:768
	global_store_dword v2, v24, s[8:9] offset:1024
	global_store_dword v2, v25, s[8:9] offset:1280
	global_store_dword v2, v26, s[8:9] offset:1536
	global_store_dword v2, v27, s[8:9] offset:1792
	global_store_dword v2, v28, s[8:9] offset:2048
	global_store_dword v2, v29, s[8:9] offset:2304
	global_store_dword v2, v30, s[8:9] offset:2560
	global_store_dword v2, v31, s[8:9] offset:2816
	global_store_dword v2, v32, s[8:9] offset:3072
	global_store_dword v2, v33, s[8:9] offset:3328
	global_store_dword v2, v34, s[8:9] offset:3584
	global_store_dword v2, v35, s[8:9] offset:3840
	s_mov_b64 s[18:19], exec
	s_mov_b64 exec, s[12:13]
	global_store_dword v10, v8, s[10:11]
	s_mov_b64 exec, s[18:19]
	s_mov_b32 s4, s5
	s_add_i32 s5, s4, 1024
	s_lshl_b32 s1, s5, 14
	s_add_u32 s6, s84, s1
	s_addc_u32 s7, s85, 0
	global_load_dwordx4 v[104:107], v1, s[6:7]
	global_load_dwordx4 v[108:111], v1, s[6:7] offset:1024
	global_load_dwordx4 v[112:115], v1, s[6:7] offset:2048
	global_load_dwordx4 v[116:119], v1, s[6:7] offset:3072
	global_load_dwordx4 v[120:123], v3, s[6:7]
	global_load_dwordx4 v[124:127], v3, s[6:7] offset:1024
	global_load_dwordx4 v[128:131], v3, s[6:7] offset:2048
	global_load_dwordx4 v[132:135], v3, s[6:7] offset:3072
	global_load_dwordx4 v[136:139], v4, s[6:7]
	global_load_dwordx4 v[140:143], v4, s[6:7] offset:1024
	global_load_dwordx4 v[144:147], v4, s[6:7] offset:2048
	global_load_dwordx4 v[148:151], v4, s[6:7] offset:3072
	global_load_dwordx4 v[152:155], v5, s[6:7]
	global_load_dwordx4 v[156:159], v5, s[6:7] offset:1024
	global_load_dwordx4 v[160:163], v5, s[6:7] offset:2048
	global_load_dwordx4 v[164:167], v5, s[6:7] offset:3072
	s_waitcnt vmcnt(48)
; __device__ __forceinline__ void peer_row_store(const f32x4 (&v)[16], unsigned char* ws, int it, int layer, int lane) {
;     ...
;     for (int j = 0; j < 16; ++j) am = fmaxf(fmaxf(am, fmaxf(fabsf(v[j][0]), fabsf(v[j][1]))), fmaxf(fabsf(v[j][2]), fabsf(v[j][3])));
;     am = __uint_as_float(max64u(__float_as_uint(am)));
;     const float q = am > 0.f ? 256.0f / am : 0.f;
;     unsigned* dst = (unsigned*)(ws + (tbl ? WS_PV : WS_PU) + (size_t)r * D) + lane;
;     if (tbl) {
;         const int rl = it - NEXP;
;         unsigned char* pvl = ws + WS_PV + (size_t)layer * NEXP * D + (size_t)rl * 8 + (lane & 1) * 4;
;         unsigned char* pvg = ws + WS_PV + (size_t)layer * NEXP * D + (size_t)NEXP * 2048 + (size_t)rl * 2048 + 4 * lane;
; #pragma unroll
;         for (int j = 0; j < 16; ++j) { int w = __builtin_amdgcn_cvt_pk_bf8_f32(v[j][0] * q, v[j][1] * q, 0, false); w = __builtin_amdgcn_cvt_pk_bf8_f32(v[j][2] * q, v[j][3] * q, w, true);
;             if (j < 8) *(unsigned*)(pvl + (size_t)((lane >> 1) + 32 * j) * (NEXP * 8)) = (unsigned)w;
;             else *(unsigned*)(pvg + 256 * (j - 8)) = (unsigned)w; }
;     } else {
; #pragma unroll
;         for (int j = 0; j < 16; ++j) { int w = __builtin_amdgcn_cvt_pk_fp8_f32(v[j][0] * q, v[j][1] * q, 0, false); w = __builtin_amdgcn_cvt_pk_fp8_f32(v[j][2] * q, v[j][3] * q, w, true); dst[64 * j] = (unsigned)w; }
;     }
;     if (lane == 0) ((float*)(ws + (tbl ? WS_SV : WS_SU)))[r] = am * (1.0f / 256.0f);
	v_max3_f32 v6, |v40|, |v41|, 0
	v_max3_f32 v6, |v42|, |v43|, v6
	s_waitcnt vmcnt(47)
	v_max3_f32 v6, |v44|, |v45|, v6
	v_max3_f32 v6, |v46|, |v47|, v6
	s_waitcnt vmcnt(46)
	v_max3_f32 v6, |v48|, |v49|, v6
	v_max3_f32 v6, |v50|, |v51|, v6
	s_waitcnt vmcnt(45)
	v_max3_f32 v6, |v52|, |v53|, v6
	v_max3_f32 v6, |v54|, |v55|, v6
	s_waitcnt vmcnt(44)
	v_max3_f32 v6, |v56|, |v57|, v6
	v_max3_f32 v6, |v58|, |v59|, v6
	s_waitcnt vmcnt(43)
	v_max3_f32 v6, |v60|, |v61|, v6
	v_max3_f32 v6, |v62|, |v63|, v6
	s_waitcnt vmcnt(42)
	v_max3_f32 v6, |v64|, |v65|, v6
	v_max3_f32 v6, |v66|, |v67|, v6
	s_waitcnt vmcnt(41)
	v_max3_f32 v6, |v68|, |v69|, v6
	v_max3_f32 v6, |v70|, |v71|, v6
	s_waitcnt vmcnt(40)
	v_max3_f32 v6, |v72|, |v73|, v6
	v_max3_f32 v6, |v74|, |v75|, v6
	s_waitcnt vmcnt(39)
	v_max3_f32 v6, |v76|, |v77|, v6
	v_max3_f32 v6, |v78|, |v79|, v6
	s_waitcnt vmcnt(38)
	v_max3_f32 v6, |v80|, |v81|, v6
	v_max3_f32 v6, |v82|, |v83|, v6
	s_waitcnt vmcnt(37)
	v_max3_f32 v6, |v84|, |v85|, v6
	v_max3_f32 v6, |v86|, |v87|, v6
	s_waitcnt vmcnt(36)
	v_max3_f32 v6, |v88|, |v89|, v6
	v_max3_f32 v6, |v90|, |v91|, v6
	s_waitcnt vmcnt(35)
	v_max3_f32 v6, |v92|, |v93|, v6
	v_max3_f32 v6, |v94|, |v95|, v6
	s_waitcnt vmcnt(34)
	v_max3_f32 v6, |v96|, |v97|, v6
	v_max3_f32 v6, |v98|, |v99|, v6
	s_waitcnt vmcnt(33)
	v_max3_f32 v6, |v100|, |v101|, v6
	v_max3_f32 v6, |v102|, |v103|, v6
	s_nop 1
	v_max_u32_dpp v6, v6, v6 quad_perm:[1,0,3,2] row_mask:0xf bank_mask:0xf bound_ctrl:1
	s_nop 1
	v_max_u32_dpp v6, v6, v6 quad_perm:[2,3,0,1] row_mask:0xf bank_mask:0xf bound_ctrl:1
	s_nop 1
	v_max_u32_dpp v6, v6, v6 row_half_mirror row_mask:0xf bank_mask:0xf bound_ctrl:1
	s_nop 1
	v_max_u32_dpp v6, v6, v6 row_mirror row_mask:0xf bank_mask:0xf bound_ctrl:1
	s_nop 1
	v_mov_b32_e32 v7, v6
	s_nop 1
	v_permlane16_swap_b32_e32 v6, v7
	v_max_u32_e32 v6, v6, v7
	v_mov_b32_e32 v7, v6
	s_nop 1
	v_permlane32_swap_b32_e32 v6, v7
	v_max_u32_e32 v6, v6, v7
	v_div_scale_f32 v12, s[16:17], v6, v6, s14
	v_rcp_f32_e32 v13, v12
	s_nop 0
	v_fma_f32 v14, -v12, v13, 1.0
	v_fmac_f32_e32 v13, v14, v13
	v_div_scale_f32 v14, vcc, s14, v6, s14
	v_mul_f32_e32 v15, v14, v13
	v_fma_f32 v16, -v12, v15, v14
	v_fmac_f32_e32 v15, v16, v13
	v_fma_f32 v12, -v12, v15, v14
	v_div_fmas_f32 v12, v12, v13, v15
	v_div_fixup_f32 v9, v12, v6, s14
	v_cmp_lt_f32_e32 vcc, 0, v6
	s_nop 1
	v_cndmask_b32_e32 v9, 0, v9, vcc
	s_lshl_b32 s1, s4, 12
	s_add_u32 s8, s90, 0xba00000
	s_addc_u32 s9, s91, 0
	s_add_u32 s8, s8, s1
	s_addc_u32 s9, s9, 0
	s_lshl_b32 s1, s4, 2
	s_add_u32 s10, s90, 0x1ba00000
	s_addc_u32 s11, s91, 0
	s_add_u32 s10, s10, s1
	s_addc_u32 s11, s11, 0
	v_mul_f32_e32 v40, v40, v9
	v_mul_f32_e32 v41, v41, v9
	v_mul_f32_e32 v42, v42, v9
	v_mul_f32_e32 v43, v43, v9
	v_mov_b32_e32 v20, v10
	v_cvt_pk_fp8_f32 v20, v40, v41
	v_mul_f32_e32 v44, v44, v9
	v_mul_f32_e32 v45, v45, v9
	v_mul_f32_e32 v46, v46, v9
	v_mul_f32_e32 v47, v47, v9
	v_mov_b32_e32 v21, v10
	v_cvt_pk_fp8_f32 v21, v44, v45
	v_cvt_pk_fp8_f32 v20, v42, v43 op_sel:[0,0,1]
	v_mul_f32_e32 v48, v48, v9
	v_mul_f32_e32 v49, v49, v9
	v_mul_f32_e32 v50, v50, v9
	v_mul_f32_e32 v51, v51, v9
	v_mov_b32_e32 v22, v10
	v_cvt_pk_fp8_f32 v22, v48, v49
	v_cvt_pk_fp8_f32 v21, v46, v47 op_sel:[0,0,1]
	v_mul_f32_e32 v52, v52, v9
	v_mul_f32_e32 v53, v53, v9
	v_mul_f32_e32 v54, v54, v9
	v_mul_f32_e32 v55, v55, v9
	v_mov_b32_e32 v23, v10
	v_cvt_pk_fp8_f32 v23, v52, v53
	v_cvt_pk_fp8_f32 v22, v50, v51 op_sel:[0,0,1]
	v_mul_f32_e32 v56, v56, v9
	v_mul_f32_e32 v57, v57, v9
	v_mul_f32_e32 v58, v58, v9
	v_mul_f32_e32 v59, v59, v9
	v_mov_b32_e32 v24, v10
	v_cvt_pk_fp8_f32 v24, v56, v57
	v_cvt_pk_fp8_f32 v23, v54, v55 op_sel:[0,0,1]
	v_mul_f32_e32 v60, v60, v9
	v_mul_f32_e32 v61, v61, v9
	v_mul_f32_e32 v62, v62, v9
	v_mul_f32_e32 v63, v63, v9
	v_mov_b32_e32 v25, v10
	v_cvt_pk_fp8_f32 v25, v60, v61
	v_cvt_pk_fp8_f32 v24, v58, v59 op_sel:[0,0,1]
	v_mul_f32_e32 v64, v64, v9
	v_mul_f32_e32 v65, v65, v9
	v_mul_f32_e32 v66, v66, v9
	v_mul_f32_e32 v67, v67, v9
	v_mov_b32_e32 v26, v10
	v_cvt_pk_fp8_f32 v26, v64, v65
	v_cvt_pk_fp8_f32 v25, v62, v63 op_sel:[0,0,1]
	v_mul_f32_e32 v68, v68, v9
	v_mul_f32_e32 v69, v69, v9
	v_mul_f32_e32 v70, v70, v9
	v_mul_f32_e32 v71, v71, v9
	v_mov_b32_e32 v27, v10
	v_cvt_pk_fp8_f32 v27, v68, v69
	v_cvt_pk_fp8_f32 v26, v66, v67 op_sel:[0,0,1]
	v_mul_f32_e32 v72, v72, v9
	v_mul_f32_e32 v73, v73, v9
	v_mul_f32_e32 v74, v74, v9
	v_mul_f32_e32 v75, v75, v9
	v_mov_b32_e32 v28, v10
	v_cvt_pk_fp8_f32 v28, v72, v73
	v_cvt_pk_fp8_f32 v27, v70, v71 op_sel:[0,0,1]
	v_mul_f32_e32 v76, v76, v9
	v_mul_f32_e32 v77, v77, v9
	v_mul_f32_e32 v78, v78, v9
	v_mul_f32_e32 v79, v79, v9
	v_mov_b32_e32 v29, v10
	v_cvt_pk_fp8_f32 v29, v76, v77
	v_cvt_pk_fp8_f32 v28, v74, v75 op_sel:[0,0,1]
	v_mul_f32_e32 v80, v80, v9
	v_mul_f32_e32 v81, v81, v9
	v_mul_f32_e32 v82, v82, v9
	v_mul_f32_e32 v83, v83, v9
	v_mov_b32_e32 v30, v10
	v_cvt_pk_fp8_f32 v30, v80, v81
	v_cvt_pk_fp8_f32 v29, v78, v79 op_sel:[0,0,1]
	v_mul_f32_e32 v84, v84, v9
	v_mul_f32_e32 v85, v85, v9
	v_mul_f32_e32 v86, v86, v9
	v_mul_f32_e32 v87, v87, v9
	v_mov_b32_e32 v31, v10
	v_cvt_pk_fp8_f32 v31, v84, v85
	v_cvt_pk_fp8_f32 v30, v82, v83 op_sel:[0,0,1]
	v_mul_f32_e32 v88, v88, v9
	v_mul_f32_e32 v89, v89, v9
	v_mul_f32_e32 v90, v90, v9
	v_mul_f32_e32 v91, v91, v9
	v_mov_b32_e32 v32, v10
	v_cvt_pk_fp8_f32 v32, v88, v89
	v_cvt_pk_fp8_f32 v31, v86, v87 op_sel:[0,0,1]
	v_mul_f32_e32 v92, v92, v9
	v_mul_f32_e32 v93, v93, v9
	v_mul_f32_e32 v94, v94, v9
	v_mul_f32_e32 v95, v95, v9
	v_mov_b32_e32 v33, v10
	v_cvt_pk_fp8_f32 v33, v92, v93
	v_cvt_pk_fp8_f32 v32, v90, v91 op_sel:[0,0,1]
	v_mul_f32_e32 v96, v96, v9
	v_mul_f32_e32 v97, v97, v9
; __device__ __forceinline__ void peer_row_load(f32x4 (&v)[16], const float* const (&in)[34], int it, int layer, int lane) {
;     const int tbl = it >= NEXP, r = it - tbl * NEXP + layer * NEXP;
;     const f32x4* src = (const f32x4*)((tbl ? in[33] : in[32]) + (size_t)r * D) + lane;
; #pragma unroll
;     for (int j = 0; j < 16; ++j) v[j] = src[64 * j];
; __device__ __forceinline__ void peer_row_store(const f32x4 (&v)[16], unsigned char* ws, int it, int layer, int lane) {
;     ...
;     unsigned* dst = (unsigned*)(ws + (tbl ? WS_PV : WS_PU) + (size_t)r * D) + lane;
;     if (tbl) {
;         const int rl = it - NEXP;
;         unsigned char* pvl = ws + WS_PV + (size_t)layer * NEXP * D + (size_t)rl * 8 + (lane & 1) * 4;
;         unsigned char* pvg = ws + WS_PV + (size_t)layer * NEXP * D + (size_t)NEXP * 2048 + (size_t)rl * 2048 + 4 * lane;
; #pragma unroll
;         for (int j = 0; j < 16; ++j) { int w = __builtin_amdgcn_cvt_pk_bf8_f32(v[j][0] * q, v[j][1] * q, 0, false); w = __builtin_amdgcn_cvt_pk_bf8_f32(v[j][2] * q, v[j][3] * q, w, true);
;             if (j < 8) *(unsigned*)(pvl + (size_t)((lane >> 1) + 32 * j) * (NEXP * 8)) = (unsigned)w;
;             else *(unsigned*)(pvg + 256 * (j - 8)) = (unsigned)w; }
;     } else {
; #pragma unroll
;         for (int j = 0; j < 16; ++j) { int w = __builtin_amdgcn_cvt_pk_fp8_f32(v[j][0] * q, v[j][1] * q, 0, false); w = __builtin_amdgcn_cvt_pk_fp8_f32(v[j][2] * q, v[j][3] * q, w, true); dst[64 * j] = (unsigned)w; }
;     }
;     if (lane == 0) ((float*)(ws + (tbl ? WS_SV : WS_SU)))[r] = am * (1.0f / 256.0f);
	v_mul_f32_e32 v98, v98, v9
	v_mul_f32_e32 v99, v99, v9
	v_mov_b32_e32 v34, v10
	v_cvt_pk_fp8_f32 v34, v96, v97
	v_cvt_pk_fp8_f32 v33, v94, v95 op_sel:[0,0,1]
	v_mul_f32_e32 v100, v100, v9
	v_mul_f32_e32 v101, v101, v9
	v_mul_f32_e32 v102, v102, v9
	v_mul_f32_e32 v103, v103, v9
	v_mov_b32_e32 v35, v10
	v_cvt_pk_fp8_f32 v35, v100, v101
	v_cvt_pk_fp8_f32 v34, v98, v99 op_sel:[0,0,1]
	v_cvt_pk_fp8_f32 v35, v102, v103 op_sel:[0,0,1]
	s_nop 0
	v_mul_f32_e32 v8, 0x3b800000, v6
	global_store_dword v2, v20, s[8:9]
	global_store_dword v2, v21, s[8:9] offset:256
	global_store_dword v2, v22, s[8:9] offset:512
	global_store_dword v2, v23, s[8:9] offset:768
	global_store_dword v2, v24, s[8:9] offset:1024
	global_store_dword v2, v25, s[8:9] offset:1280
	global_store_dword v2, v26, s[8:9] offset:1536
	global_store_dword v2, v27, s[8:9] offset:1792
	global_store_dword v2, v28, s[8:9] offset:2048
	global_store_dword v2, v29, s[8:9] offset:2304
	global_store_dword v2, v30, s[8:9] offset:2560
	global_store_dword v2, v31, s[8:9] offset:2816
	global_store_dword v2, v32, s[8:9] offset:3072
	global_store_dword v2, v33, s[8:9] offset:3328
	global_store_dword v2, v34, s[8:9] offset:3584
	global_store_dword v2, v35, s[8:9] offset:3840
	s_mov_b64 s[18:19], exec
	s_mov_b64 exec, s[12:13]
	global_store_dword v10, v8, s[10:11]
	s_mov_b64 exec, s[18:19]
	s_mov_b32 s4, s5
	s_add_i32 s5, s4, 1024
	s_lshl_b32 s1, s5, 14
	s_add_u32 s6, s84, s1
	s_addc_u32 s7, s85, 0
	global_load_dwordx4 v[40:43], v1, s[6:7]
	global_load_dwordx4 v[44:47], v1, s[6:7] offset:1024
	global_load_dwordx4 v[48:51], v1, s[6:7] offset:2048
	global_load_dwordx4 v[52:55], v1, s[6:7] offset:3072
	global_load_dwordx4 v[56:59], v3, s[6:7]
	global_load_dwordx4 v[60:63], v3, s[6:7] offset:1024
	global_load_dwordx4 v[64:67], v3, s[6:7] offset:2048
	global_load_dwordx4 v[68:71], v3, s[6:7] offset:3072
	global_load_dwordx4 v[72:75], v4, s[6:7]
	global_load_dwordx4 v[76:79], v4, s[6:7] offset:1024
	global_load_dwordx4 v[80:83], v4, s[6:7] offset:2048
	global_load_dwordx4 v[84:87], v4, s[6:7] offset:3072
	global_load_dwordx4 v[88:91], v5, s[6:7]
	global_load_dwordx4 v[92:95], v5, s[6:7] offset:1024
	global_load_dwordx4 v[96:99], v5, s[6:7] offset:2048
	global_load_dwordx4 v[100:103], v5, s[6:7] offset:3072
	s_waitcnt vmcnt(48)
	v_max3_f32 v6, |v104|, |v105|, 0
	v_max3_f32 v6, |v106|, |v107|, v6
	s_waitcnt vmcnt(47)
	v_max3_f32 v6, |v108|, |v109|, v6
	v_max3_f32 v6, |v110|, |v111|, v6
	s_waitcnt vmcnt(46)
	v_max3_f32 v6, |v112|, |v113|, v6
	v_max3_f32 v6, |v114|, |v115|, v6
	s_waitcnt vmcnt(45)
	v_max3_f32 v6, |v116|, |v117|, v6
	v_max3_f32 v6, |v118|, |v119|, v6
	s_waitcnt vmcnt(44)
	v_max3_f32 v6, |v120|, |v121|, v6
	v_max3_f32 v6, |v122|, |v123|, v6
	s_waitcnt vmcnt(43)
	v_max3_f32 v6, |v124|, |v125|, v6
	v_max3_f32 v6, |v126|, |v127|, v6
	s_waitcnt vmcnt(42)
	v_max3_f32 v6, |v128|, |v129|, v6
	v_max3_f32 v6, |v130|, |v131|, v6
	s_waitcnt vmcnt(41)
	v_max3_f32 v6, |v132|, |v133|, v6
	v_max3_f32 v6, |v134|, |v135|, v6
	s_waitcnt vmcnt(40)
	v_max3_f32 v6, |v136|, |v137|, v6
	v_max3_f32 v6, |v138|, |v139|, v6
	s_waitcnt vmcnt(39)
	v_max3_f32 v6, |v140|, |v141|, v6
	v_max3_f32 v6, |v142|, |v143|, v6
	s_waitcnt vmcnt(38)
	v_max3_f32 v6, |v144|, |v145|, v6
	v_max3_f32 v6, |v146|, |v147|, v6
	s_waitcnt vmcnt(37)
	v_max3_f32 v6, |v148|, |v149|, v6
	v_max3_f32 v6, |v150|, |v151|, v6
	s_waitcnt vmcnt(36)
	v_max3_f32 v6, |v152|, |v153|, v6
	v_max3_f32 v6, |v154|, |v155|, v6
	s_waitcnt vmcnt(35)
	v_max3_f32 v6, |v156|, |v157|, v6
	v_max3_f32 v6, |v158|, |v159|, v6
	s_waitcnt vmcnt(34)
	v_max3_f32 v6, |v160|, |v161|, v6
	v_max3_f32 v6, |v162|, |v163|, v6
	s_waitcnt vmcnt(33)
	v_max3_f32 v6, |v164|, |v165|, v6
	v_max3_f32 v6, |v166|, |v167|, v6
	s_nop 1
	v_max_u32_dpp v6, v6, v6 quad_perm:[1,0,3,2] row_mask:0xf bank_mask:0xf bound_ctrl:1
	s_nop 1
	v_max_u32_dpp v6, v6, v6 quad_perm:[2,3,0,1] row_mask:0xf bank_mask:0xf bound_ctrl:1
	s_nop 1
	v_max_u32_dpp v6, v6, v6 row_half_mirror row_mask:0xf bank_mask:0xf bound_ctrl:1
	s_nop 1
	v_max_u32_dpp v6, v6, v6 row_mirror row_mask:0xf bank_mask:0xf bound_ctrl:1
	s_nop 1
	v_mov_b32_e32 v7, v6
	s_nop 1
	v_permlane16_swap_b32_e32 v6, v7
	v_max_u32_e32 v6, v6, v7
	v_mov_b32_e32 v7, v6
	s_nop 1
	v_permlane32_swap_b32_e32 v6, v7
	v_max_u32_e32 v6, v6, v7
	v_div_scale_f32 v12, s[16:17], v6, v6, s14
	v_rcp_f32_e32 v13, v12
	s_nop 0
	v_fma_f32 v14, -v12, v13, 1.0
	v_fmac_f32_e32 v13, v14, v13
	v_div_scale_f32 v14, vcc, s14, v6, s14
	v_mul_f32_e32 v15, v14, v13
	v_fma_f32 v16, -v12, v15, v14
	v_fmac_f32_e32 v15, v16, v13
	v_fma_f32 v12, -v12, v15, v14
	v_div_fmas_f32 v12, v12, v13, v15
	v_div_fixup_f32 v9, v12, v6, s14
	v_cmp_lt_f32_e32 vcc, 0, v6
	s_nop 1
	v_cndmask_b32_e32 v9, 0, v9, vcc
	s_lshl_b32 s1, s4, 12
	s_add_u32 s8, s90, 0xba00000
	s_addc_u32 s9, s91, 0
	s_add_u32 s8, s8, s1
	s_addc_u32 s9, s9, 0
	s_lshl_b32 s1, s4, 2
	s_add_u32 s10, s90, 0x1ba00000
	s_addc_u32 s11, s91, 0
	s_add_u32 s10, s10, s1
	s_addc_u32 s11, s11, 0
	v_mul_f32_e32 v104, v104, v9
	v_mul_f32_e32 v105, v105, v9
	v_mul_f32_e32 v106, v106, v9
	v_mul_f32_e32 v107, v107, v9
	v_mov_b32_e32 v20, v10
	v_cvt_pk_fp8_f32 v20, v104, v105
	v_mul_f32_e32 v108, v108, v9
	v_mul_f32_e32 v109, v109, v9
	v_mul_f32_e32 v110, v110, v9
	v_mul_f32_e32 v111, v111, v9
	v_mov_b32_e32 v21, v10
	v_cvt_pk_fp8_f32 v21, v108, v109
	v_cvt_pk_fp8_f32 v20, v106, v107 op_sel:[0,0,1]
	v_mul_f32_e32 v112, v112, v9
	v_mul_f32_e32 v113, v113, v9
	v_mul_f32_e32 v114, v114, v9
	v_mul_f32_e32 v115, v115, v9
	v_mov_b32_e32 v22, v10
	v_cvt_pk_fp8_f32 v22, v112, v113
	v_cvt_pk_fp8_f32 v21, v110, v111 op_sel:[0,0,1]
	v_mul_f32_e32 v116, v116, v9
; __device__ __forceinline__ void peer_row_load(f32x4 (&v)[16], const float* const (&in)[34], int it, int layer, int lane) {
;     const int tbl = it >= NEXP, r = it - tbl * NEXP + layer * NEXP;
;     const f32x4* src = (const f32x4*)((tbl ? in[33] : in[32]) + (size_t)r * D) + lane;
; #pragma unroll
;     for (int j = 0; j < 16; ++j) v[j] = src[64 * j];
; __device__ __forceinline__ void peer_row_store(const f32x4 (&v)[16], unsigned char* ws, int it, int layer, int lane) {
;     ...
;     unsigned* dst = (unsigned*)(ws + (tbl ? WS_PV : WS_PU) + (size_t)r * D) + lane;
;     if (tbl) {
;         const int rl = it - NEXP;
;         unsigned char* pvl = ws + WS_PV + (size_t)layer * NEXP * D + (size_t)rl * 8 + (lane & 1) * 4;
;         unsigned char* pvg = ws + WS_PV + (size_t)layer * NEXP * D + (size_t)NEXP * 2048 + (size_t)rl * 2048 + 4 * lane;
; #pragma unroll
;         for (int j = 0; j < 16; ++j) { int w = __builtin_amdgcn_cvt_pk_bf8_f32(v[j][0] * q, v[j][1] * q, 0, false); w = __builtin_amdgcn_cvt_pk_bf8_f32(v[j][2] * q, v[j][3] * q, w, true);
;             if (j < 8) *(unsigned*)(pvl + (size_t)((lane >> 1) + 32 * j) * (NEXP * 8)) = (unsigned)w;
;             else *(unsigned*)(pvg + 256 * (j - 8)) = (unsigned)w; }
;     } else {
; #pragma unroll
;         for (int j = 0; j < 16; ++j) { int w = __builtin_amdgcn_cvt_pk_fp8_f32(v[j][0] * q, v[j][1] * q, 0, false); w = __builtin_amdgcn_cvt_pk_fp8_f32(v[j][2] * q, v[j][3] * q, w, true); dst[64 * j] = (unsigned)w; }
;     }
;     if (lane == 0) ((float*)(ws + (tbl ? WS_SV : WS_SU)))[r] = am * (1.0f / 256.0f);
	v_mul_f32_e32 v117, v117, v9
	v_mul_f32_e32 v118, v118, v9
	v_mul_f32_e32 v119, v119, v9
	v_mov_b32_e32 v23, v10
	v_cvt_pk_fp8_f32 v23, v116, v117
	v_cvt_pk_fp8_f32 v22, v114, v115 op_sel:[0,0,1]
	v_mul_f32_e32 v120, v120, v9
	v_mul_f32_e32 v121, v121, v9
	v_mul_f32_e32 v122, v122, v9
	v_mul_f32_e32 v123, v123, v9
	v_mov_b32_e32 v24, v10
	v_cvt_pk_fp8_f32 v24, v120, v121
	v_cvt_pk_fp8_f32 v23, v118, v119 op_sel:[0,0,1]
	v_mul_f32_e32 v124, v124, v9
	v_mul_f32_e32 v125, v125, v9
	v_mul_f32_e32 v126, v126, v9
	v_mul_f32_e32 v127, v127, v9
	v_mov_b32_e32 v25, v10
	v_cvt_pk_fp8_f32 v25, v124, v125
	v_cvt_pk_fp8_f32 v24, v122, v123 op_sel:[0,0,1]
	v_mul_f32_e32 v128, v128, v9
	v_mul_f32_e32 v129, v129, v9
	v_mul_f32_e32 v130, v130, v9
	v_mul_f32_e32 v131, v131, v9
	v_mov_b32_e32 v26, v10
	v_cvt_pk_fp8_f32 v26, v128, v129
	v_cvt_pk_fp8_f32 v25, v126, v127 op_sel:[0,0,1]
	v_mul_f32_e32 v132, v132, v9
	v_mul_f32_e32 v133, v133, v9
	v_mul_f32_e32 v134, v134, v9
	v_mul_f32_e32 v135, v135, v9
	v_mov_b32_e32 v27, v10
	v_cvt_pk_fp8_f32 v27, v132, v133
	v_cvt_pk_fp8_f32 v26, v130, v131 op_sel:[0,0,1]
	v_mul_f32_e32 v136, v136, v9
	v_mul_f32_e32 v137, v137, v9
	v_mul_f32_e32 v138, v138, v9
	v_mul_f32_e32 v139, v139, v9
	v_mov_b32_e32 v28, v10
	v_cvt_pk_fp8_f32 v28, v136, v137
	v_cvt_pk_fp8_f32 v27, v134, v135 op_sel:[0,0,1]
	v_mul_f32_e32 v140, v140, v9
	v_mul_f32_e32 v141, v141, v9
	v_mul_f32_e32 v142, v142, v9
	v_mul_f32_e32 v143, v143, v9
	v_mov_b32_e32 v29, v10
	v_cvt_pk_fp8_f32 v29, v140, v141
	v_cvt_pk_fp8_f32 v28, v138, v139 op_sel:[0,0,1]
	v_mul_f32_e32 v144, v144, v9
	v_mul_f32_e32 v145, v145, v9
	v_mul_f32_e32 v146, v146, v9
	v_mul_f32_e32 v147, v147, v9
	v_mov_b32_e32 v30, v10
	v_cvt_pk_fp8_f32 v30, v144, v145
	v_cvt_pk_fp8_f32 v29, v142, v143 op_sel:[0,0,1]
	v_mul_f32_e32 v148, v148, v9
	v_mul_f32_e32 v149, v149, v9
	v_mul_f32_e32 v150, v150, v9
	v_mul_f32_e32 v151, v151, v9
	v_mov_b32_e32 v31, v10
	v_cvt_pk_fp8_f32 v31, v148, v149
	v_cvt_pk_fp8_f32 v30, v146, v147 op_sel:[0,0,1]
	v_mul_f32_e32 v152, v152, v9
	v_mul_f32_e32 v153, v153, v9
	v_mul_f32_e32 v154, v154, v9
	v_mul_f32_e32 v155, v155, v9
	v_mov_b32_e32 v32, v10
	v_cvt_pk_fp8_f32 v32, v152, v153
	v_cvt_pk_fp8_f32 v31, v150, v151 op_sel:[0,0,1]
	v_mul_f32_e32 v156, v156, v9
	v_mul_f32_e32 v157, v157, v9
	v_mul_f32_e32 v158, v158, v9
	v_mul_f32_e32 v159, v159, v9
	v_mov_b32_e32 v33, v10
	v_cvt_pk_fp8_f32 v33, v156, v157
	v_cvt_pk_fp8_f32 v32, v154, v155 op_sel:[0,0,1]
	v_mul_f32_e32 v160, v160, v9
	v_mul_f32_e32 v161, v161, v9
	v_mul_f32_e32 v162, v162, v9
	v_mul_f32_e32 v163, v163, v9
	v_mov_b32_e32 v34, v10
	v_cvt_pk_fp8_f32 v34, v160, v161
	v_cvt_pk_fp8_f32 v33, v158, v159 op_sel:[0,0,1]
	v_mul_f32_e32 v164, v164, v9
	v_mul_f32_e32 v165, v165, v9
	v_mul_f32_e32 v166, v166, v9
	v_mul_f32_e32 v167, v167, v9
	v_mov_b32_e32 v35, v10
	v_cvt_pk_fp8_f32 v35, v164, v165
	v_cvt_pk_fp8_f32 v34, v162, v163 op_sel:[0,0,1]
	v_cvt_pk_fp8_f32 v35, v166, v167 op_sel:[0,0,1]
	s_nop 0
	v_mul_f32_e32 v8, 0x3b800000, v6
	global_store_dword v2, v20, s[8:9]
	global_store_dword v2, v21, s[8:9] offset:256
	global_store_dword v2, v22, s[8:9] offset:512
	global_store_dword v2, v23, s[8:9] offset:768
	global_store_dword v2, v24, s[8:9] offset:1024
	global_store_dword v2, v25, s[8:9] offset:1280
	global_store_dword v2, v26, s[8:9] offset:1536
	global_store_dword v2, v27, s[8:9] offset:1792
	global_store_dword v2, v28, s[8:9] offset:2048
	global_store_dword v2, v29, s[8:9] offset:2304
	global_store_dword v2, v30, s[8:9] offset:2560
	global_store_dword v2, v31, s[8:9] offset:2816
	global_store_dword v2, v32, s[8:9] offset:3072
	global_store_dword v2, v33, s[8:9] offset:3328
	global_store_dword v2, v34, s[8:9] offset:3584
	global_store_dword v2, v35, s[8:9] offset:3840
	s_mov_b64 s[18:19], exec
	s_mov_b64 exec, s[12:13]
	global_store_dword v10, v8, s[10:11]
	s_mov_b64 exec, s[18:19]
	s_mov_b32 s4, s5
	s_add_i32 s5, s4, 1024
	s_lshl_b32 s1, s5, 14
	s_add_u32 s6, s84, s1
	s_addc_u32 s7, s85, 0
	global_load_dwordx4 v[104:107], v1, s[6:7]
	global_load_dwordx4 v[108:111], v1, s[6:7] offset:1024
	global_load_dwordx4 v[112:115], v1, s[6:7] offset:2048
	global_load_dwordx4 v[116:119], v1, s[6:7] offset:3072
	global_load_dwordx4 v[120:123], v3, s[6:7]
	global_load_dwordx4 v[124:127], v3, s[6:7] offset:1024
	global_load_dwordx4 v[128:131], v3, s[6:7] offset:2048
	global_load_dwordx4 v[132:135], v3, s[6:7] offset:3072
	global_load_dwordx4 v[136:139], v4, s[6:7]
	global_load_dwordx4 v[140:143], v4, s[6:7] offset:1024
	global_load_dwordx4 v[144:147], v4, s[6:7] offset:2048
	global_load_dwordx4 v[148:151], v4, s[6:7] offset:3072
	global_load_dwordx4 v[152:155], v5, s[6:7]
	global_load_dwordx4 v[156:159], v5, s[6:7] offset:1024
	global_load_dwordx4 v[160:163], v5, s[6:7] offset:2048
	global_load_dwordx4 v[164:167], v5, s[6:7] offset:3072
	s_waitcnt vmcnt(48)
	v_max3_f32 v6, |v40|, |v41|, 0
	v_max3_f32 v6, |v42|, |v43|, v6
	s_waitcnt vmcnt(47)
	v_max3_f32 v6, |v44|, |v45|, v6
	v_max3_f32 v6, |v46|, |v47|, v6
	s_waitcnt vmcnt(46)
	v_max3_f32 v6, |v48|, |v49|, v6
	v_max3_f32 v6, |v50|, |v51|, v6
	s_waitcnt vmcnt(45)
	v_max3_f32 v6, |v52|, |v53|, v6
	v_max3_f32 v6, |v54|, |v55|, v6
	s_waitcnt vmcnt(44)
	v_max3_f32 v6, |v56|, |v57|, v6
	v_max3_f32 v6, |v58|, |v59|, v6
	s_waitcnt vmcnt(43)
	v_max3_f32 v6, |v60|, |v61|, v6
	v_max3_f32 v6, |v62|, |v63|, v6
	s_waitcnt vmcnt(42)
	v_max3_f32 v6, |v64|, |v65|, v6
	v_max3_f32 v6, |v66|, |v67|, v6
	s_waitcnt vmcnt(41)
	v_max3_f32 v6, |v68|, |v69|, v6
	v_max3_f32 v6, |v70|, |v71|, v6
	s_waitcnt vmcnt(40)
	v_max3_f32 v6, |v72|, |v73|, v6
	v_max3_f32 v6, |v74|, |v75|, v6
	s_waitcnt vmcnt(39)
; __device__ __forceinline__ void peer_row_store(const f32x4 (&v)[16], unsigned char* ws, int it, int layer, int lane) {
;     ...
;     for (int j = 0; j < 16; ++j) am = fmaxf(fmaxf(am, fmaxf(fabsf(v[j][0]), fabsf(v[j][1]))), fmaxf(fabsf(v[j][2]), fabsf(v[j][3])));
;     am = __uint_as_float(max64u(__float_as_uint(am)));
;     const float q = am > 0.f ? 256.0f / am : 0.f;
;     unsigned* dst = (unsigned*)(ws + (tbl ? WS_PV : WS_PU) + (size_t)r * D) + lane;
;     if (tbl) {
;         const int rl = it - NEXP;
;         unsigned char* pvl = ws + WS_PV + (size_t)layer * NEXP * D + (size_t)rl * 8 + (lane & 1) * 4;
;         unsigned char* pvg = ws + WS_PV + (size_t)layer * NEXP * D + (size_t)NEXP * 2048 + (size_t)rl * 2048 + 4 * lane;
; #pragma unroll
;         for (int j = 0; j < 16; ++j) { int w = __builtin_amdgcn_cvt_pk_bf8_f32(v[j][0] * q, v[j][1] * q, 0, false); w = __builtin_amdgcn_cvt_pk_bf8_f32(v[j][2] * q, v[j][3] * q, w, true);
;             if (j < 8) *(unsigned*)(pvl + (size_t)((lane >> 1) + 32 * j) * (NEXP * 8)) = (unsigned)w;
;             else *(unsigned*)(pvg + 256 * (j - 8)) = (unsigned)w; }
;     } else {
; #pragma unroll
;         for (int j = 0; j < 16; ++j) { int w = __builtin_amdgcn_cvt_pk_fp8_f32(v[j][0] * q, v[j][1] * q, 0, false); w = __builtin_amdgcn_cvt_pk_fp8_f32(v[j][2] * q, v[j][3] * q, w, true); dst[64 * j] = (unsigned)w; }
;     }
;     if (lane == 0) ((float*)(ws + (tbl ? WS_SV : WS_SU)))[r] = am * (1.0f / 256.0f);
	v_max3_f32 v6, |v76|, |v77|, v6
	v_max3_f32 v6, |v78|, |v79|, v6
	s_waitcnt vmcnt(38)
	v_max3_f32 v6, |v80|, |v81|, v6
	v_max3_f32 v6, |v82|, |v83|, v6
	s_waitcnt vmcnt(37)
	v_max3_f32 v6, |v84|, |v85|, v6
	v_max3_f32 v6, |v86|, |v87|, v6
	s_waitcnt vmcnt(36)
	v_max3_f32 v6, |v88|, |v89|, v6
	v_max3_f32 v6, |v90|, |v91|, v6
	s_waitcnt vmcnt(35)
	v_max3_f32 v6, |v92|, |v93|, v6
	v_max3_f32 v6, |v94|, |v95|, v6
	s_waitcnt vmcnt(34)
	v_max3_f32 v6, |v96|, |v97|, v6
	v_max3_f32 v6, |v98|, |v99|, v6
	s_waitcnt vmcnt(33)
	v_max3_f32 v6, |v100|, |v101|, v6
	v_max3_f32 v6, |v102|, |v103|, v6
	s_nop 1
	v_max_u32_dpp v6, v6, v6 quad_perm:[1,0,3,2] row_mask:0xf bank_mask:0xf bound_ctrl:1
	s_nop 1
	v_max_u32_dpp v6, v6, v6 quad_perm:[2,3,0,1] row_mask:0xf bank_mask:0xf bound_ctrl:1
	s_nop 1
	v_max_u32_dpp v6, v6, v6 row_half_mirror row_mask:0xf bank_mask:0xf bound_ctrl:1
	s_nop 1
	v_max_u32_dpp v6, v6, v6 row_mirror row_mask:0xf bank_mask:0xf bound_ctrl:1
	s_nop 1
	v_mov_b32_e32 v7, v6
	s_nop 1
	v_permlane16_swap_b32_e32 v6, v7
	v_max_u32_e32 v6, v6, v7
	v_mov_b32_e32 v7, v6
	s_nop 1
	v_permlane32_swap_b32_e32 v6, v7
	v_max_u32_e32 v6, v6, v7
	v_div_scale_f32 v12, s[16:17], v6, v6, s14
	v_rcp_f32_e32 v13, v12
	s_nop 0
	v_fma_f32 v14, -v12, v13, 1.0
	v_fmac_f32_e32 v13, v14, v13
	v_div_scale_f32 v14, vcc, s14, v6, s14
	v_mul_f32_e32 v15, v14, v13
	v_fma_f32 v16, -v12, v15, v14
	v_fmac_f32_e32 v15, v16, v13
	v_fma_f32 v12, -v12, v15, v14
	v_div_fmas_f32 v12, v12, v13, v15
	v_div_fixup_f32 v9, v12, v6, s14
	v_cmp_lt_f32_e32 vcc, 0, v6
	s_nop 1
	v_cndmask_b32_e32 v9, 0, v9, vcc
	s_lshl_b32 s1, s4, 12
	s_add_u32 s8, s90, 0xba00000
	s_addc_u32 s9, s91, 0
	s_add_u32 s8, s8, s1
	s_addc_u32 s9, s9, 0
	s_lshl_b32 s1, s4, 2
	s_add_u32 s10, s90, 0x1ba00000
	s_addc_u32 s11, s91, 0
	s_add_u32 s10, s10, s1
	s_addc_u32 s11, s11, 0
	v_mul_f32_e32 v40, v40, v9
	v_mul_f32_e32 v41, v41, v9
	v_mul_f32_e32 v42, v42, v9
	v_mul_f32_e32 v43, v43, v9
	v_mov_b32_e32 v20, v10
	v_cvt_pk_fp8_f32 v20, v40, v41
	v_mul_f32_e32 v44, v44, v9
	v_mul_f32_e32 v45, v45, v9
	v_mul_f32_e32 v46, v46, v9
	v_mul_f32_e32 v47, v47, v9
	v_mov_b32_e32 v21, v10
	v_cvt_pk_fp8_f32 v21, v44, v45
	v_cvt_pk_fp8_f32 v20, v42, v43 op_sel:[0,0,1]
	v_mul_f32_e32 v48, v48, v9
	v_mul_f32_e32 v49, v49, v9
	v_mul_f32_e32 v50, v50, v9
	v_mul_f32_e32 v51, v51, v9
	v_mov_b32_e32 v22, v10
	v_cvt_pk_fp8_f32 v22, v48, v49
	v_cvt_pk_fp8_f32 v21, v46, v47 op_sel:[0,0,1]
	v_mul_f32_e32 v52, v52, v9
	v_mul_f32_e32 v53, v53, v9
	v_mul_f32_e32 v54, v54, v9
	v_mul_f32_e32 v55, v55, v9
	v_mov_b32_e32 v23, v10
	v_cvt_pk_fp8_f32 v23, v52, v53
	v_cvt_pk_fp8_f32 v22, v50, v51 op_sel:[0,0,1]
	v_mul_f32_e32 v56, v56, v9
	v_mul_f32_e32 v57, v57, v9
	v_mul_f32_e32 v58, v58, v9
	v_mul_f32_e32 v59, v59, v9
	v_mov_b32_e32 v24, v10
	v_cvt_pk_fp8_f32 v24, v56, v57
	v_cvt_pk_fp8_f32 v23, v54, v55 op_sel:[0,0,1]
	v_mul_f32_e32 v60, v60, v9
	v_mul_f32_e32 v61, v61, v9
	v_mul_f32_e32 v62, v62, v9
	v_mul_f32_e32 v63, v63, v9
	v_mov_b32_e32 v25, v10
	v_cvt_pk_fp8_f32 v25, v60, v61
	v_cvt_pk_fp8_f32 v24, v58, v59 op_sel:[0,0,1]
	v_mul_f32_e32 v64, v64, v9
	v_mul_f32_e32 v65, v65, v9
	v_mul_f32_e32 v66, v66, v9
	v_mul_f32_e32 v67, v67, v9
	v_mov_b32_e32 v26, v10
	v_cvt_pk_fp8_f32 v26, v64, v65
	v_cvt_pk_fp8_f32 v25, v62, v63 op_sel:[0,0,1]
	v_mul_f32_e32 v68, v68, v9
	v_mul_f32_e32 v69, v69, v9
	v_mul_f32_e32 v70, v70, v9
	v_mul_f32_e32 v71, v71, v9
	v_mov_b32_e32 v27, v10
	v_cvt_pk_fp8_f32 v27, v68, v69
	v_cvt_pk_fp8_f32 v26, v66, v67 op_sel:[0,0,1]
	v_mul_f32_e32 v72, v72, v9
	v_mul_f32_e32 v73, v73, v9
	v_mul_f32_e32 v74, v74, v9
	v_mul_f32_e32 v75, v75, v9
	v_mov_b32_e32 v28, v10
	v_cvt_pk_fp8_f32 v28, v72, v73
	v_cvt_pk_fp8_f32 v27, v70, v71 op_sel:[0,0,1]
	v_mul_f32_e32 v76, v76, v9
	v_mul_f32_e32 v77, v77, v9
	v_mul_f32_e32 v78, v78, v9
	v_mul_f32_e32 v79, v79, v9
	v_mov_b32_e32 v29, v10
	v_cvt_pk_fp8_f32 v29, v76, v77
	v_cvt_pk_fp8_f32 v28, v74, v75 op_sel:[0,0,1]
	v_mul_f32_e32 v80, v80, v9
	v_mul_f32_e32 v81, v81, v9
	v_mul_f32_e32 v82, v82, v9
	v_mul_f32_e32 v83, v83, v9
	v_mov_b32_e32 v30, v10
	v_cvt_pk_fp8_f32 v30, v80, v81
	v_cvt_pk_fp8_f32 v29, v78, v79 op_sel:[0,0,1]
	v_mul_f32_e32 v84, v84, v9
	v_mul_f32_e32 v85, v85, v9
	v_mul_f32_e32 v86, v86, v9
	v_mul_f32_e32 v87, v87, v9
	v_mov_b32_e32 v31, v10
	v_cvt_pk_fp8_f32 v31, v84, v85
	v_cvt_pk_fp8_f32 v30, v82, v83 op_sel:[0,0,1]
	v_mul_f32_e32 v88, v88, v9
	v_mul_f32_e32 v89, v89, v9
	v_mul_f32_e32 v90, v90, v9
	v_mul_f32_e32 v91, v91, v9
	v_mov_b32_e32 v32, v10
	v_cvt_pk_fp8_f32 v32, v88, v89
	v_cvt_pk_fp8_f32 v31, v86, v87 op_sel:[0,0,1]
	v_mul_f32_e32 v92, v92, v9
	v_mul_f32_e32 v93, v93, v9
	v_mul_f32_e32 v94, v94, v9
	v_mul_f32_e32 v95, v95, v9
	v_mov_b32_e32 v33, v10
	v_cvt_pk_fp8_f32 v33, v92, v93
	v_cvt_pk_fp8_f32 v32, v90, v91 op_sel:[0,0,1]
	v_mul_f32_e32 v96, v96, v9
	v_mul_f32_e32 v97, v97, v9
	v_mul_f32_e32 v98, v98, v9
	v_mul_f32_e32 v99, v99, v9
	v_mov_b32_e32 v34, v10
	v_cvt_pk_fp8_f32 v34, v96, v97
	v_cvt_pk_fp8_f32 v33, v94, v95 op_sel:[0,0,1]
	v_mul_f32_e32 v100, v100, v9
	v_mul_f32_e32 v101, v101, v9
	v_mul_f32_e32 v102, v102, v9
	v_mul_f32_e32 v103, v103, v9
	v_mov_b32_e32 v35, v10
	v_cvt_pk_fp8_f32 v35, v100, v101
	v_cvt_pk_fp8_f32 v34, v98, v99 op_sel:[0,0,1]
	v_cvt_pk_fp8_f32 v35, v102, v103 op_sel:[0,0,1]
	s_nop 0
	v_mul_f32_e32 v8, 0x3b800000, v6
	global_store_dword v2, v20, s[8:9]
	global_store_dword v2, v21, s[8:9] offset:256
	global_store_dword v2, v22, s[8:9] offset:512
	global_store_dword v2, v23, s[8:9] offset:768
	global_store_dword v2, v24, s[8:9] offset:1024
	global_store_dword v2, v25, s[8:9] offset:1280
	global_store_dword v2, v26, s[8:9] offset:1536
; __device__ __forceinline__ void peer_row_load(f32x4 (&v)[16], const float* const (&in)[34], int it, int layer, int lane) {
;     const int tbl = it >= NEXP, r = it - tbl * NEXP + layer * NEXP;
;     const f32x4* src = (const f32x4*)((tbl ? in[33] : in[32]) + (size_t)r * D) + lane;
; #pragma unroll
;     for (int j = 0; j < 16; ++j) v[j] = src[64 * j];
; __device__ __forceinline__ void peer_row_store(const f32x4 (&v)[16], unsigned char* ws, int it, int layer, int lane) {
;     ...
;     unsigned* dst = (unsigned*)(ws + (tbl ? WS_PV : WS_PU) + (size_t)r * D) + lane;
;     if (tbl) {
;         const int rl = it - NEXP;
;         unsigned char* pvl = ws + WS_PV + (size_t)layer * NEXP * D + (size_t)rl * 8 + (lane & 1) * 4;
;         unsigned char* pvg = ws + WS_PV + (size_t)layer * NEXP * D + (size_t)NEXP * 2048 + (size_t)rl * 2048 + 4 * lane;
; #pragma unroll
;         for (int j = 0; j < 16; ++j) { int w = __builtin_amdgcn_cvt_pk_bf8_f32(v[j][0] * q, v[j][1] * q, 0, false); w = __builtin_amdgcn_cvt_pk_bf8_f32(v[j][2] * q, v[j][3] * q, w, true);
;             if (j < 8) *(unsigned*)(pvl + (size_t)((lane >> 1) + 32 * j) * (NEXP * 8)) = (unsigned)w;
;             else *(unsigned*)(pvg + 256 * (j - 8)) = (unsigned)w; }
;     } else {
; #pragma unroll
;         for (int j = 0; j < 16; ++j) { int w = __builtin_amdgcn_cvt_pk_fp8_f32(v[j][0] * q, v[j][1] * q, 0, false); w = __builtin_amdgcn_cvt_pk_fp8_f32(v[j][2] * q, v[j][3] * q, w, true); dst[64 * j] = (unsigned)w; }
;     }
;     if (lane == 0) ((float*)(ws + (tbl ? WS_SV : WS_SU)))[r] = am * (1.0f / 256.0f);
	global_store_dword v2, v27, s[8:9] offset:1792
	global_store_dword v2, v28, s[8:9] offset:2048
	global_store_dword v2, v29, s[8:9] offset:2304
	global_store_dword v2, v30, s[8:9] offset:2560
	global_store_dword v2, v31, s[8:9] offset:2816
	global_store_dword v2, v32, s[8:9] offset:3072
	global_store_dword v2, v33, s[8:9] offset:3328
	global_store_dword v2, v34, s[8:9] offset:3584
	global_store_dword v2, v35, s[8:9] offset:3840
	s_mov_b64 s[18:19], exec
	s_mov_b64 exec, s[12:13]
	global_store_dword v10, v8, s[10:11]
	s_mov_b64 exec, s[18:19]
	s_mov_b32 s4, s5
	s_add_i32 s5, s4, 1024
	s_lshl_b32 s1, s5, 14
	s_add_u32 s6, s84, s1
	s_addc_u32 s7, s85, 0
	global_load_dwordx4 v[40:43], v1, s[6:7]
	global_load_dwordx4 v[44:47], v1, s[6:7] offset:1024
	global_load_dwordx4 v[48:51], v1, s[6:7] offset:2048
	global_load_dwordx4 v[52:55], v1, s[6:7] offset:3072
	global_load_dwordx4 v[56:59], v3, s[6:7]
	global_load_dwordx4 v[60:63], v3, s[6:7] offset:1024
	global_load_dwordx4 v[64:67], v3, s[6:7] offset:2048
	global_load_dwordx4 v[68:71], v3, s[6:7] offset:3072
	global_load_dwordx4 v[72:75], v4, s[6:7]
	global_load_dwordx4 v[76:79], v4, s[6:7] offset:1024
	global_load_dwordx4 v[80:83], v4, s[6:7] offset:2048
	global_load_dwordx4 v[84:87], v4, s[6:7] offset:3072
	global_load_dwordx4 v[88:91], v5, s[6:7]
	global_load_dwordx4 v[92:95], v5, s[6:7] offset:1024
	global_load_dwordx4 v[96:99], v5, s[6:7] offset:2048
	global_load_dwordx4 v[100:103], v5, s[6:7] offset:3072
	s_waitcnt vmcnt(48)
	v_max3_f32 v6, |v104|, |v105|, 0
	v_max3_f32 v6, |v106|, |v107|, v6
	s_waitcnt vmcnt(47)
	v_max3_f32 v6, |v108|, |v109|, v6
	v_max3_f32 v6, |v110|, |v111|, v6
	s_waitcnt vmcnt(46)
	v_max3_f32 v6, |v112|, |v113|, v6
	v_max3_f32 v6, |v114|, |v115|, v6
	s_waitcnt vmcnt(45)
	v_max3_f32 v6, |v116|, |v117|, v6
	v_max3_f32 v6, |v118|, |v119|, v6
	s_waitcnt vmcnt(44)
	v_max3_f32 v6, |v120|, |v121|, v6
	v_max3_f32 v6, |v122|, |v123|, v6
	s_waitcnt vmcnt(43)
	v_max3_f32 v6, |v124|, |v125|, v6
	v_max3_f32 v6, |v126|, |v127|, v6
	s_waitcnt vmcnt(42)
	v_max3_f32 v6, |v128|, |v129|, v6
	v_max3_f32 v6, |v130|, |v131|, v6
	s_waitcnt vmcnt(41)
	v_max3_f32 v6, |v132|, |v133|, v6
	v_max3_f32 v6, |v134|, |v135|, v6
	s_waitcnt vmcnt(40)
	v_max3_f32 v6, |v136|, |v137|, v6
	v_max3_f32 v6, |v138|, |v139|, v6
	s_waitcnt vmcnt(39)
	v_max3_f32 v6, |v140|, |v141|, v6
	v_max3_f32 v6, |v142|, |v143|, v6
	s_waitcnt vmcnt(38)
	v_max3_f32 v6, |v144|, |v145|, v6
	v_max3_f32 v6, |v146|, |v147|, v6
	s_waitcnt vmcnt(37)
	v_max3_f32 v6, |v148|, |v149|, v6
	v_max3_f32 v6, |v150|, |v151|, v6
	s_waitcnt vmcnt(36)
	v_max3_f32 v6, |v152|, |v153|, v6
	v_max3_f32 v6, |v154|, |v155|, v6
	s_waitcnt vmcnt(35)
	v_max3_f32 v6, |v156|, |v157|, v6
	v_max3_f32 v6, |v158|, |v159|, v6
	s_waitcnt vmcnt(34)
	v_max3_f32 v6, |v160|, |v161|, v6
	v_max3_f32 v6, |v162|, |v163|, v6
	s_waitcnt vmcnt(33)
	v_max3_f32 v6, |v164|, |v165|, v6
	v_max3_f32 v6, |v166|, |v167|, v6
	s_nop 1
	v_max_u32_dpp v6, v6, v6 quad_perm:[1,0,3,2] row_mask:0xf bank_mask:0xf bound_ctrl:1
	s_nop 1
	v_max_u32_dpp v6, v6, v6 quad_perm:[2,3,0,1] row_mask:0xf bank_mask:0xf bound_ctrl:1
	s_nop 1
	v_max_u32_dpp v6, v6, v6 row_half_mirror row_mask:0xf bank_mask:0xf bound_ctrl:1
	s_nop 1
	v_max_u32_dpp v6, v6, v6 row_mirror row_mask:0xf bank_mask:0xf bound_ctrl:1
	s_nop 1
	v_mov_b32_e32 v7, v6
	s_nop 1
	v_permlane16_swap_b32_e32 v6, v7
	v_max_u32_e32 v6, v6, v7
	v_mov_b32_e32 v7, v6
	s_nop 1
	v_permlane32_swap_b32_e32 v6, v7
	v_max_u32_e32 v6, v6, v7
	v_div_scale_f32 v12, s[16:17], v6, v6, s14
	v_rcp_f32_e32 v13, v12
	s_nop 0
	v_fma_f32 v14, -v12, v13, 1.0
	v_fmac_f32_e32 v13, v14, v13
	v_div_scale_f32 v14, vcc, s14, v6, s14
	v_mul_f32_e32 v15, v14, v13
	v_fma_f32 v16, -v12, v15, v14
	v_fmac_f32_e32 v15, v16, v13
	v_fma_f32 v12, -v12, v15, v14
	v_div_fmas_f32 v12, v12, v13, v15
	v_div_fixup_f32 v9, v12, v6, s14
	v_cmp_lt_f32_e32 vcc, 0, v6
	s_nop 1
	v_cndmask_b32_e32 v9, 0, v9, vcc
	s_lshl_b32 s1, s4, 12
	s_add_u32 s8, s90, 0xba00000
	s_addc_u32 s9, s91, 0
	s_add_u32 s8, s8, s1
	s_addc_u32 s9, s9, 0
	s_lshl_b32 s1, s4, 2
	s_add_u32 s10, s90, 0x1ba00000
	s_addc_u32 s11, s91, 0
	s_add_u32 s10, s10, s1
	s_addc_u32 s11, s11, 0
	v_mul_f32_e32 v104, v104, v9
	v_mul_f32_e32 v105, v105, v9
	v_mul_f32_e32 v106, v106, v9
	v_mul_f32_e32 v107, v107, v9
	v_mov_b32_e32 v20, v10
	v_cvt_pk_fp8_f32 v20, v104, v105
	v_mul_f32_e32 v108, v108, v9
	v_mul_f32_e32 v109, v109, v9
	v_mul_f32_e32 v110, v110, v9
	v_mul_f32_e32 v111, v111, v9
	v_mov_b32_e32 v21, v10
	v_cvt_pk_fp8_f32 v21, v108, v109
	v_cvt_pk_fp8_f32 v20, v106, v107 op_sel:[0,0,1]
	v_mul_f32_e32 v112, v112, v9
	v_mul_f32_e32 v113, v113, v9
	v_mul_f32_e32 v114, v114, v9
	v_mul_f32_e32 v115, v115, v9
	v_mov_b32_e32 v22, v10
	v_cvt_pk_fp8_f32 v22, v112, v113
	v_cvt_pk_fp8_f32 v21, v110, v111 op_sel:[0,0,1]
	v_mul_f32_e32 v116, v116, v9
	v_mul_f32_e32 v117, v117, v9
	v_mul_f32_e32 v118, v118, v9
	v_mul_f32_e32 v119, v119, v9
	v_mov_b32_e32 v23, v10
	v_cvt_pk_fp8_f32 v23, v116, v117
	v_cvt_pk_fp8_f32 v22, v114, v115 op_sel:[0,0,1]
	v_mul_f32_e32 v120, v120, v9
	v_mul_f32_e32 v121, v121, v9
	v_mul_f32_e32 v122, v122, v9
	v_mul_f32_e32 v123, v123, v9
	v_mov_b32_e32 v24, v10
	v_cvt_pk_fp8_f32 v24, v120, v121
	v_cvt_pk_fp8_f32 v23, v118, v119 op_sel:[0,0,1]
	v_mul_f32_e32 v124, v124, v9
	v_mul_f32_e32 v125, v125, v9
	v_mul_f32_e32 v126, v126, v9
	v_mul_f32_e32 v127, v127, v9
	v_mov_b32_e32 v25, v10
	v_cvt_pk_fp8_f32 v25, v124, v125
	v_cvt_pk_fp8_f32 v24, v122, v123 op_sel:[0,0,1]
	v_mul_f32_e32 v128, v128, v9
	v_mul_f32_e32 v129, v129, v9
	v_mul_f32_e32 v130, v130, v9
	v_mul_f32_e32 v131, v131, v9
	v_mov_b32_e32 v26, v10
; __device__ __forceinline__ void peer_row_load(f32x4 (&v)[16], const float* const (&in)[34], int it, int layer, int lane) {
;     const int tbl = it >= NEXP, r = it - tbl * NEXP + layer * NEXP;
;     const f32x4* src = (const f32x4*)((tbl ? in[33] : in[32]) + (size_t)r * D) + lane;
; #pragma unroll
;     for (int j = 0; j < 16; ++j) v[j] = src[64 * j];
; __device__ __forceinline__ void peer_row_store(const f32x4 (&v)[16], unsigned char* ws, int it, int layer, int lane) {
;     ...
;     unsigned* dst = (unsigned*)(ws + (tbl ? WS_PV : WS_PU) + (size_t)r * D) + lane;
;     if (tbl) {
;         const int rl = it - NEXP;
;         unsigned char* pvl = ws + WS_PV + (size_t)layer * NEXP * D + (size_t)rl * 8 + (lane & 1) * 4;
;         unsigned char* pvg = ws + WS_PV + (size_t)layer * NEXP * D + (size_t)NEXP * 2048 + (size_t)rl * 2048 + 4 * lane;
; #pragma unroll
;         for (int j = 0; j < 16; ++j) { int w = __builtin_amdgcn_cvt_pk_bf8_f32(v[j][0] * q, v[j][1] * q, 0, false); w = __builtin_amdgcn_cvt_pk_bf8_f32(v[j][2] * q, v[j][3] * q, w, true);
;             if (j < 8) *(unsigned*)(pvl + (size_t)((lane >> 1) + 32 * j) * (NEXP * 8)) = (unsigned)w;
;             else *(unsigned*)(pvg + 256 * (j - 8)) = (unsigned)w; }
;     } else {
; #pragma unroll
;         for (int j = 0; j < 16; ++j) { int w = __builtin_amdgcn_cvt_pk_fp8_f32(v[j][0] * q, v[j][1] * q, 0, false); w = __builtin_amdgcn_cvt_pk_fp8_f32(v[j][2] * q, v[j][3] * q, w, true); dst[64 * j] = (unsigned)w; }
;     }
;     if (lane == 0) ((float*)(ws + (tbl ? WS_SV : WS_SU)))[r] = am * (1.0f / 256.0f);
	v_cvt_pk_fp8_f32 v26, v128, v129
	v_cvt_pk_fp8_f32 v25, v126, v127 op_sel:[0,0,1]
	v_mul_f32_e32 v132, v132, v9
	v_mul_f32_e32 v133, v133, v9
	v_mul_f32_e32 v134, v134, v9
	v_mul_f32_e32 v135, v135, v9
	v_mov_b32_e32 v27, v10
	v_cvt_pk_fp8_f32 v27, v132, v133
	v_cvt_pk_fp8_f32 v26, v130, v131 op_sel:[0,0,1]
	v_mul_f32_e32 v136, v136, v9
	v_mul_f32_e32 v137, v137, v9
	v_mul_f32_e32 v138, v138, v9
	v_mul_f32_e32 v139, v139, v9
	v_mov_b32_e32 v28, v10
	v_cvt_pk_fp8_f32 v28, v136, v137
	v_cvt_pk_fp8_f32 v27, v134, v135 op_sel:[0,0,1]
	v_mul_f32_e32 v140, v140, v9
	v_mul_f32_e32 v141, v141, v9
	v_mul_f32_e32 v142, v142, v9
	v_mul_f32_e32 v143, v143, v9
	v_mov_b32_e32 v29, v10
	v_cvt_pk_fp8_f32 v29, v140, v141
	v_cvt_pk_fp8_f32 v28, v138, v139 op_sel:[0,0,1]
	v_mul_f32_e32 v144, v144, v9
	v_mul_f32_e32 v145, v145, v9
	v_mul_f32_e32 v146, v146, v9
	v_mul_f32_e32 v147, v147, v9
	v_mov_b32_e32 v30, v10
	v_cvt_pk_fp8_f32 v30, v144, v145
	v_cvt_pk_fp8_f32 v29, v142, v143 op_sel:[0,0,1]
	v_mul_f32_e32 v148, v148, v9
	v_mul_f32_e32 v149, v149, v9
	v_mul_f32_e32 v150, v150, v9
	v_mul_f32_e32 v151, v151, v9
	v_mov_b32_e32 v31, v10
	v_cvt_pk_fp8_f32 v31, v148, v149
	v_cvt_pk_fp8_f32 v30, v146, v147 op_sel:[0,0,1]
	v_mul_f32_e32 v152, v152, v9
	v_mul_f32_e32 v153, v153, v9
	v_mul_f32_e32 v154, v154, v9
	v_mul_f32_e32 v155, v155, v9
	v_mov_b32_e32 v32, v10
	v_cvt_pk_fp8_f32 v32, v152, v153
	v_cvt_pk_fp8_f32 v31, v150, v151 op_sel:[0,0,1]
	v_mul_f32_e32 v156, v156, v9
	v_mul_f32_e32 v157, v157, v9
	v_mul_f32_e32 v158, v158, v9
	v_mul_f32_e32 v159, v159, v9
	v_mov_b32_e32 v33, v10
	v_cvt_pk_fp8_f32 v33, v156, v157
	v_cvt_pk_fp8_f32 v32, v154, v155 op_sel:[0,0,1]
	v_mul_f32_e32 v160, v160, v9
	v_mul_f32_e32 v161, v161, v9
	v_mul_f32_e32 v162, v162, v9
	v_mul_f32_e32 v163, v163, v9
	v_mov_b32_e32 v34, v10
	v_cvt_pk_fp8_f32 v34, v160, v161
	v_cvt_pk_fp8_f32 v33, v158, v159 op_sel:[0,0,1]
	v_mul_f32_e32 v164, v164, v9
	v_mul_f32_e32 v165, v165, v9
	v_mul_f32_e32 v166, v166, v9
	v_mul_f32_e32 v167, v167, v9
	v_mov_b32_e32 v35, v10
	v_cvt_pk_fp8_f32 v35, v164, v165
	v_cvt_pk_fp8_f32 v34, v162, v163 op_sel:[0,0,1]
	v_cvt_pk_fp8_f32 v35, v166, v167 op_sel:[0,0,1]
	s_nop 0
	v_mul_f32_e32 v8, 0x3b800000, v6
	global_store_dword v2, v20, s[8:9]
	global_store_dword v2, v21, s[8:9] offset:256
	global_store_dword v2, v22, s[8:9] offset:512
	global_store_dword v2, v23, s[8:9] offset:768
	global_store_dword v2, v24, s[8:9] offset:1024
	global_store_dword v2, v25, s[8:9] offset:1280
	global_store_dword v2, v26, s[8:9] offset:1536
	global_store_dword v2, v27, s[8:9] offset:1792
	global_store_dword v2, v28, s[8:9] offset:2048
	global_store_dword v2, v29, s[8:9] offset:2304
	global_store_dword v2, v30, s[8:9] offset:2560
	global_store_dword v2, v31, s[8:9] offset:2816
	global_store_dword v2, v32, s[8:9] offset:3072
	global_store_dword v2, v33, s[8:9] offset:3328
	global_store_dword v2, v34, s[8:9] offset:3584
	global_store_dword v2, v35, s[8:9] offset:3840
	s_mov_b64 s[18:19], exec
	s_mov_b64 exec, s[12:13]
	global_store_dword v10, v8, s[10:11]
	s_mov_b64 exec, s[18:19]
	s_mov_b32 s4, s5
	s_add_i32 s5, s4, 1024
	s_lshl_b32 s1, s5, 14
	s_add_u32 s6, s84, s1
	s_addc_u32 s7, s85, 0
	global_load_dwordx4 v[104:107], v1, s[6:7]
	global_load_dwordx4 v[108:111], v1, s[6:7] offset:1024
	global_load_dwordx4 v[112:115], v1, s[6:7] offset:2048
	global_load_dwordx4 v[116:119], v1, s[6:7] offset:3072
	global_load_dwordx4 v[120:123], v3, s[6:7]
	global_load_dwordx4 v[124:127], v3, s[6:7] offset:1024
	global_load_dwordx4 v[128:131], v3, s[6:7] offset:2048
	global_load_dwordx4 v[132:135], v3, s[6:7] offset:3072
	global_load_dwordx4 v[136:139], v4, s[6:7]
	global_load_dwordx4 v[140:143], v4, s[6:7] offset:1024
	global_load_dwordx4 v[144:147], v4, s[6:7] offset:2048
	global_load_dwordx4 v[148:151], v4, s[6:7] offset:3072
	global_load_dwordx4 v[152:155], v5, s[6:7]
	global_load_dwordx4 v[156:159], v5, s[6:7] offset:1024
	global_load_dwordx4 v[160:163], v5, s[6:7] offset:2048
	global_load_dwordx4 v[164:167], v5, s[6:7] offset:3072
	s_waitcnt vmcnt(48)
	v_max3_f32 v6, |v40|, |v41|, 0
	v_max3_f32 v6, |v42|, |v43|, v6
	s_waitcnt vmcnt(47)
	v_max3_f32 v6, |v44|, |v45|, v6
	v_max3_f32 v6, |v46|, |v47|, v6
	s_waitcnt vmcnt(46)
	v_max3_f32 v6, |v48|, |v49|, v6
	v_max3_f32 v6, |v50|, |v51|, v6
	s_waitcnt vmcnt(45)
	v_max3_f32 v6, |v52|, |v53|, v6
	v_max3_f32 v6, |v54|, |v55|, v6
	s_waitcnt vmcnt(44)
	v_max3_f32 v6, |v56|, |v57|, v6
	v_max3_f32 v6, |v58|, |v59|, v6
	s_waitcnt vmcnt(43)
	v_max3_f32 v6, |v60|, |v61|, v6
	v_max3_f32 v6, |v62|, |v63|, v6
	s_waitcnt vmcnt(42)
	v_max3_f32 v6, |v64|, |v65|, v6
	v_max3_f32 v6, |v66|, |v67|, v6
	s_waitcnt vmcnt(41)
	v_max3_f32 v6, |v68|, |v69|, v6
	v_max3_f32 v6, |v70|, |v71|, v6
	s_waitcnt vmcnt(40)
	v_max3_f32 v6, |v72|, |v73|, v6
	v_max3_f32 v6, |v74|, |v75|, v6
	s_waitcnt vmcnt(39)
	v_max3_f32 v6, |v76|, |v77|, v6
	v_max3_f32 v6, |v78|, |v79|, v6
	s_waitcnt vmcnt(38)
	v_max3_f32 v6, |v80|, |v81|, v6
	v_max3_f32 v6, |v82|, |v83|, v6
	s_waitcnt vmcnt(37)
	v_max3_f32 v6, |v84|, |v85|, v6
	v_max3_f32 v6, |v86|, |v87|, v6
	s_waitcnt vmcnt(36)
	v_max3_f32 v6, |v88|, |v89|, v6
	v_max3_f32 v6, |v90|, |v91|, v6
	s_waitcnt vmcnt(35)
	v_max3_f32 v6, |v92|, |v93|, v6
	v_max3_f32 v6, |v94|, |v95|, v6
	s_waitcnt vmcnt(34)
	v_max3_f32 v6, |v96|, |v97|, v6
	v_max3_f32 v6, |v98|, |v99|, v6
	s_waitcnt vmcnt(33)
; __device__ __forceinline__ void peer_row_store(const f32x4 (&v)[16], unsigned char* ws, int it, int layer, int lane) {
;     ...
;     for (int j = 0; j < 16; ++j) am = fmaxf(fmaxf(am, fmaxf(fabsf(v[j][0]), fabsf(v[j][1]))), fmaxf(fabsf(v[j][2]), fabsf(v[j][3])));
;     am = __uint_as_float(max64u(__float_as_uint(am)));
;     const float q = am > 0.f ? 256.0f / am : 0.f;
;     unsigned* dst = (unsigned*)(ws + (tbl ? WS_PV : WS_PU) + (size_t)r * D) + lane;
;     if (tbl) {
;         const int rl = it - NEXP;
;         unsigned char* pvl = ws + WS_PV + (size_t)layer * NEXP * D + (size_t)rl * 8 + (lane & 1) * 4;
;         unsigned char* pvg = ws + WS_PV + (size_t)layer * NEXP * D + (size_t)NEXP * 2048 + (size_t)rl * 2048 + 4 * lane;
; #pragma unroll
;         for (int j = 0; j < 16; ++j) { int w = __builtin_amdgcn_cvt_pk_bf8_f32(v[j][0] * q, v[j][1] * q, 0, false); w = __builtin_amdgcn_cvt_pk_bf8_f32(v[j][2] * q, v[j][3] * q, w, true);
;             if (j < 8) *(unsigned*)(pvl + (size_t)((lane >> 1) + 32 * j) * (NEXP * 8)) = (unsigned)w;
;             else *(unsigned*)(pvg + 256 * (j - 8)) = (unsigned)w; }
;     } else {
; #pragma unroll
;         for (int j = 0; j < 16; ++j) { int w = __builtin_amdgcn_cvt_pk_fp8_f32(v[j][0] * q, v[j][1] * q, 0, false); w = __builtin_amdgcn_cvt_pk_fp8_f32(v[j][2] * q, v[j][3] * q, w, true); dst[64 * j] = (unsigned)w; }
;     }
;     if (lane == 0) ((float*)(ws + (tbl ? WS_SV : WS_SU)))[r] = am * (1.0f / 256.0f);
	v_max3_f32 v6, |v100|, |v101|, v6
	v_max3_f32 v6, |v102|, |v103|, v6
	s_nop 1
	v_max_u32_dpp v6, v6, v6 quad_perm:[1,0,3,2] row_mask:0xf bank_mask:0xf bound_ctrl:1
	s_nop 1
	v_max_u32_dpp v6, v6, v6 quad_perm:[2,3,0,1] row_mask:0xf bank_mask:0xf bound_ctrl:1
	s_nop 1
	v_max_u32_dpp v6, v6, v6 row_half_mirror row_mask:0xf bank_mask:0xf bound_ctrl:1
	s_nop 1
	v_max_u32_dpp v6, v6, v6 row_mirror row_mask:0xf bank_mask:0xf bound_ctrl:1
	s_nop 1
	v_mov_b32_e32 v7, v6
	s_nop 1
	v_permlane16_swap_b32_e32 v6, v7
	v_max_u32_e32 v6, v6, v7
	v_mov_b32_e32 v7, v6
	s_nop 1
	v_permlane32_swap_b32_e32 v6, v7
	v_max_u32_e32 v6, v6, v7
	v_div_scale_f32 v12, s[16:17], v6, v6, s14
	v_rcp_f32_e32 v13, v12
	s_nop 0
	v_fma_f32 v14, -v12, v13, 1.0
	v_fmac_f32_e32 v13, v14, v13
	v_div_scale_f32 v14, vcc, s14, v6, s14
	v_mul_f32_e32 v15, v14, v13
	v_fma_f32 v16, -v12, v15, v14
	v_fmac_f32_e32 v15, v16, v13
	v_fma_f32 v12, -v12, v15, v14
	v_div_fmas_f32 v12, v12, v13, v15
	v_div_fixup_f32 v9, v12, v6, s14
	v_cmp_lt_f32_e32 vcc, 0, v6
	s_nop 1
	v_cndmask_b32_e32 v9, 0, v9, vcc
	s_lshl_b32 s1, s4, 12
	s_add_u32 s8, s90, 0xba00000
	s_addc_u32 s9, s91, 0
	s_add_u32 s8, s8, s1
	s_addc_u32 s9, s9, 0
	s_lshl_b32 s1, s4, 2
	s_add_u32 s10, s90, 0x1ba00000
	s_addc_u32 s11, s91, 0
	s_add_u32 s10, s10, s1
	s_addc_u32 s11, s11, 0
	v_mul_f32_e32 v40, v40, v9
	v_mul_f32_e32 v41, v41, v9
	v_mul_f32_e32 v42, v42, v9
	v_mul_f32_e32 v43, v43, v9
	v_mov_b32_e32 v20, v10
	v_cvt_pk_fp8_f32 v20, v40, v41
	v_mul_f32_e32 v44, v44, v9
	v_mul_f32_e32 v45, v45, v9
	v_mul_f32_e32 v46, v46, v9
	v_mul_f32_e32 v47, v47, v9
	v_mov_b32_e32 v21, v10
	v_cvt_pk_fp8_f32 v21, v44, v45
	v_cvt_pk_fp8_f32 v20, v42, v43 op_sel:[0,0,1]
	v_mul_f32_e32 v48, v48, v9
	v_mul_f32_e32 v49, v49, v9
	v_mul_f32_e32 v50, v50, v9
	v_mul_f32_e32 v51, v51, v9
	v_mov_b32_e32 v22, v10
	v_cvt_pk_fp8_f32 v22, v48, v49
	v_cvt_pk_fp8_f32 v21, v46, v47 op_sel:[0,0,1]
	v_mul_f32_e32 v52, v52, v9
	v_mul_f32_e32 v53, v53, v9
	v_mul_f32_e32 v54, v54, v9
	v_mul_f32_e32 v55, v55, v9
	v_mov_b32_e32 v23, v10
	v_cvt_pk_fp8_f32 v23, v52, v53
	v_cvt_pk_fp8_f32 v22, v50, v51 op_sel:[0,0,1]
	v_mul_f32_e32 v56, v56, v9
	v_mul_f32_e32 v57, v57, v9
	v_mul_f32_e32 v58, v58, v9
	v_mul_f32_e32 v59, v59, v9
	v_mov_b32_e32 v24, v10
	v_cvt_pk_fp8_f32 v24, v56, v57
	v_cvt_pk_fp8_f32 v23, v54, v55 op_sel:[0,0,1]
	v_mul_f32_e32 v60, v60, v9
	v_mul_f32_e32 v61, v61, v9
	v_mul_f32_e32 v62, v62, v9
	v_mul_f32_e32 v63, v63, v9
	v_mov_b32_e32 v25, v10
	v_cvt_pk_fp8_f32 v25, v60, v61
	v_cvt_pk_fp8_f32 v24, v58, v59 op_sel:[0,0,1]
	v_mul_f32_e32 v64, v64, v9
	v_mul_f32_e32 v65, v65, v9
	v_mul_f32_e32 v66, v66, v9
	v_mul_f32_e32 v67, v67, v9
	v_mov_b32_e32 v26, v10
	v_cvt_pk_fp8_f32 v26, v64, v65
	v_cvt_pk_fp8_f32 v25, v62, v63 op_sel:[0,0,1]
	v_mul_f32_e32 v68, v68, v9
	v_mul_f32_e32 v69, v69, v9
	v_mul_f32_e32 v70, v70, v9
	v_mul_f32_e32 v71, v71, v9
	v_mov_b32_e32 v27, v10
	v_cvt_pk_fp8_f32 v27, v68, v69
	v_cvt_pk_fp8_f32 v26, v66, v67 op_sel:[0,0,1]
	v_mul_f32_e32 v72, v72, v9
	v_mul_f32_e32 v73, v73, v9
	v_mul_f32_e32 v74, v74, v9
	v_mul_f32_e32 v75, v75, v9
	v_mov_b32_e32 v28, v10
	v_cvt_pk_fp8_f32 v28, v72, v73
	v_cvt_pk_fp8_f32 v27, v70, v71 op_sel:[0,0,1]
	v_mul_f32_e32 v76, v76, v9
	v_mul_f32_e32 v77, v77, v9
	v_mul_f32_e32 v78, v78, v9
	v_mul_f32_e32 v79, v79, v9
	v_mov_b32_e32 v29, v10
	v_cvt_pk_fp8_f32 v29, v76, v77
	v_cvt_pk_fp8_f32 v28, v74, v75 op_sel:[0,0,1]
	v_mul_f32_e32 v80, v80, v9
	v_mul_f32_e32 v81, v81, v9
	v_mul_f32_e32 v82, v82, v9
	v_mul_f32_e32 v83, v83, v9
	v_mov_b32_e32 v30, v10
	v_cvt_pk_fp8_f32 v30, v80, v81
	v_cvt_pk_fp8_f32 v29, v78, v79 op_sel:[0,0,1]
	v_mul_f32_e32 v84, v84, v9
	v_mul_f32_e32 v85, v85, v9
	v_mul_f32_e32 v86, v86, v9
	v_mul_f32_e32 v87, v87, v9
	v_mov_b32_e32 v31, v10
	v_cvt_pk_fp8_f32 v31, v84, v85
	v_cvt_pk_fp8_f32 v30, v82, v83 op_sel:[0,0,1]
	v_mul_f32_e32 v88, v88, v9
	v_mul_f32_e32 v89, v89, v9
	v_mul_f32_e32 v90, v90, v9
	v_mul_f32_e32 v91, v91, v9
	v_mov_b32_e32 v32, v10
	v_cvt_pk_fp8_f32 v32, v88, v89
	v_cvt_pk_fp8_f32 v31, v86, v87 op_sel:[0,0,1]
	v_mul_f32_e32 v92, v92, v9
	v_mul_f32_e32 v93, v93, v9
	v_mul_f32_e32 v94, v94, v9
	v_mul_f32_e32 v95, v95, v9
	v_mov_b32_e32 v33, v10
	v_cvt_pk_fp8_f32 v33, v92, v93
	v_cvt_pk_fp8_f32 v32, v90, v91 op_sel:[0,0,1]
	v_mul_f32_e32 v96, v96, v9
	v_mul_f32_e32 v97, v97, v9
	v_mul_f32_e32 v98, v98, v9
	v_mul_f32_e32 v99, v99, v9
	v_mov_b32_e32 v34, v10
	v_cvt_pk_fp8_f32 v34, v96, v97
	v_cvt_pk_fp8_f32 v33, v94, v95 op_sel:[0,0,1]
	v_mul_f32_e32 v100, v100, v9
	v_mul_f32_e32 v101, v101, v9
	v_mul_f32_e32 v102, v102, v9
	v_mul_f32_e32 v103, v103, v9
	v_mov_b32_e32 v35, v10
	v_cvt_pk_fp8_f32 v35, v100, v101
	v_cvt_pk_fp8_f32 v34, v98, v99 op_sel:[0,0,1]
	v_cvt_pk_fp8_f32 v35, v102, v103 op_sel:[0,0,1]
	s_nop 0
	v_mul_f32_e32 v8, 0x3b800000, v6
	global_store_dword v2, v20, s[8:9]
	global_store_dword v2, v21, s[8:9] offset:256
	global_store_dword v2, v22, s[8:9] offset:512
	global_store_dword v2, v23, s[8:9] offset:768
	global_store_dword v2, v24, s[8:9] offset:1024
	global_store_dword v2, v25, s[8:9] offset:1280
	global_store_dword v2, v26, s[8:9] offset:1536
	global_store_dword v2, v27, s[8:9] offset:1792
	global_store_dword v2, v28, s[8:9] offset:2048
	global_store_dword v2, v29, s[8:9] offset:2304
	global_store_dword v2, v30, s[8:9] offset:2560
	global_store_dword v2, v31, s[8:9] offset:2816
	global_store_dword v2, v32, s[8:9] offset:3072
	global_store_dword v2, v33, s[8:9] offset:3328
	global_store_dword v2, v34, s[8:9] offset:3584
	global_store_dword v2, v35, s[8:9] offset:3840
	s_mov_b64 s[18:19], exec
	s_mov_b64 exec, s[12:13]
	global_store_dword v10, v8, s[10:11]
	s_mov_b64 exec, s[18:19]
	s_mov_b32 s4, s5
	s_waitcnt vmcnt(32)
; __device__ __forceinline__ void peer_row_store(const f32x4 (&v)[16], unsigned char* ws, int it, int layer, int lane) {
;     ...
;     for (int j = 0; j < 16; ++j) am = fmaxf(fmaxf(am, fmaxf(fabsf(v[j][0]), fabsf(v[j][1]))), fmaxf(fabsf(v[j][2]), fabsf(v[j][3])));
	v_max3_f32 v6, |v104|, |v105|, 0
	v_max3_f32 v6, |v106|, |v107|, v6
	s_waitcnt vmcnt(31)
	v_max3_f32 v6, |v108|, |v109|, v6
	v_max3_f32 v6, |v110|, |v111|, v6
	s_waitcnt vmcnt(30)
	v_max3_f32 v6, |v112|, |v113|, v6
	v_max3_f32 v6, |v114|, |v115|, v6
	s_waitcnt vmcnt(29)
	v_max3_f32 v6, |v116|, |v117|, v6
	v_max3_f32 v6, |v118|, |v119|, v6
	s_waitcnt vmcnt(28)
	v_max3_f32 v6, |v120|, |v121|, v6
	v_max3_f32 v6, |v122|, |v123|, v6
	s_waitcnt vmcnt(27)
	v_max3_f32 v6, |v124|, |v125|, v6
	v_max3_f32 v6, |v126|, |v127|, v6
	s_waitcnt vmcnt(26)
	v_max3_f32 v6, |v128|, |v129|, v6
	v_max3_f32 v6, |v130|, |v131|, v6
	s_waitcnt vmcnt(25)
	v_max3_f32 v6, |v132|, |v133|, v6
	v_max3_f32 v6, |v134|, |v135|, v6
	s_waitcnt vmcnt(24)
	v_max3_f32 v6, |v136|, |v137|, v6
	v_max3_f32 v6, |v138|, |v139|, v6
	s_waitcnt vmcnt(23)
	v_max3_f32 v6, |v140|, |v141|, v6
	v_max3_f32 v6, |v142|, |v143|, v6
	s_waitcnt vmcnt(22)
	v_max3_f32 v6, |v144|, |v145|, v6
	v_max3_f32 v6, |v146|, |v147|, v6
	s_waitcnt vmcnt(21)
	v_max3_f32 v6, |v148|, |v149|, v6
	v_max3_f32 v6, |v150|, |v151|, v6
	s_waitcnt vmcnt(20)
	v_max3_f32 v6, |v152|, |v153|, v6
	v_max3_f32 v6, |v154|, |v155|, v6
	s_waitcnt vmcnt(19)
	v_max3_f32 v6, |v156|, |v157|, v6
	v_max3_f32 v6, |v158|, |v159|, v6
	s_waitcnt vmcnt(18)
	v_max3_f32 v6, |v160|, |v161|, v6
	v_max3_f32 v6, |v162|, |v163|, v6
	s_waitcnt vmcnt(17)
; __device__ __forceinline__ void peer_row_store(const f32x4 (&v)[16], unsigned char* ws, int it, int layer, int lane) {
;     ...
;     am = __uint_as_float(max64u(__float_as_uint(am)));
;     const float q = am > 0.f ? 256.0f / am : 0.f;
;     unsigned* dst = (unsigned*)(ws + (tbl ? WS_PV : WS_PU) + (size_t)r * D) + lane;
;     if (tbl) {
;         const int rl = it - NEXP;
;         unsigned char* pvl = ws + WS_PV + (size_t)layer * NEXP * D + (size_t)rl * 8 + (lane & 1) * 4;
;         unsigned char* pvg = ws + WS_PV + (size_t)layer * NEXP * D + (size_t)NEXP * 2048 + (size_t)rl * 2048 + 4 * lane;
; #pragma unroll
;         for (int j = 0; j < 16; ++j) { int w = __builtin_amdgcn_cvt_pk_bf8_f32(v[j][0] * q, v[j][1] * q, 0, false); w = __builtin_amdgcn_cvt_pk_bf8_f32(v[j][2] * q, v[j][3] * q, w, true);
;             if (j < 8) *(unsigned*)(pvl + (size_t)((lane >> 1) + 32 * j) * (NEXP * 8)) = (unsigned)w;
;             else *(unsigned*)(pvg + 256 * (j - 8)) = (unsigned)w; }
;     } else {
; #pragma unroll
;         for (int j = 0; j < 16; ++j) { int w = __builtin_amdgcn_cvt_pk_fp8_f32(v[j][0] * q, v[j][1] * q, 0, false); w = __builtin_amdgcn_cvt_pk_fp8_f32(v[j][2] * q, v[j][3] * q, w, true); dst[64 * j] = (unsigned)w; }
;     }
;     if (lane == 0) ((float*)(ws + (tbl ? WS_SV : WS_SU)))[r] = am * (1.0f / 256.0f);
	v_max3_f32 v6, |v164|, |v165|, v6
	v_max3_f32 v6, |v166|, |v167|, v6
	s_nop 1
	v_max_u32_dpp v6, v6, v6 quad_perm:[1,0,3,2] row_mask:0xf bank_mask:0xf bound_ctrl:1
	s_nop 1
	v_max_u32_dpp v6, v6, v6 quad_perm:[2,3,0,1] row_mask:0xf bank_mask:0xf bound_ctrl:1
	s_nop 1
	v_max_u32_dpp v6, v6, v6 row_half_mirror row_mask:0xf bank_mask:0xf bound_ctrl:1
	s_nop 1
	v_max_u32_dpp v6, v6, v6 row_mirror row_mask:0xf bank_mask:0xf bound_ctrl:1
	s_nop 1
	v_mov_b32_e32 v7, v6
	s_nop 1
	v_permlane16_swap_b32_e32 v6, v7
	v_max_u32_e32 v6, v6, v7
	v_mov_b32_e32 v7, v6
	s_nop 1
	v_permlane32_swap_b32_e32 v6, v7
	v_max_u32_e32 v6, v6, v7
	v_div_scale_f32 v12, s[16:17], v6, v6, s14
	v_rcp_f32_e32 v13, v12
	s_nop 0
	v_fma_f32 v14, -v12, v13, 1.0
	v_fmac_f32_e32 v13, v14, v13
	v_div_scale_f32 v14, vcc, s14, v6, s14
	v_mul_f32_e32 v15, v14, v13
	v_fma_f32 v16, -v12, v15, v14
	v_fmac_f32_e32 v15, v16, v13
	v_fma_f32 v12, -v12, v15, v14
	v_div_fmas_f32 v12, v12, v13, v15
	v_div_fixup_f32 v9, v12, v6, s14
	v_cmp_lt_f32_e32 vcc, 0, v6
	s_nop 1
	v_cndmask_b32_e32 v9, 0, v9, vcc
	s_lshl_b32 s1, s4, 12
	s_add_u32 s8, s90, 0xba00000
	s_addc_u32 s9, s91, 0
	s_add_u32 s8, s8, s1
	s_addc_u32 s9, s9, 0
	s_lshl_b32 s1, s4, 2
	s_add_u32 s10, s90, 0x1ba00000
	s_addc_u32 s11, s91, 0
	s_add_u32 s10, s10, s1
	s_addc_u32 s11, s11, 0
	v_mul_f32_e32 v104, v104, v9
	v_mul_f32_e32 v105, v105, v9
	v_mul_f32_e32 v106, v106, v9
	v_mul_f32_e32 v107, v107, v9
	v_mov_b32_e32 v20, v10
	v_cvt_pk_fp8_f32 v20, v104, v105
	v_mul_f32_e32 v108, v108, v9
	v_mul_f32_e32 v109, v109, v9
	v_mul_f32_e32 v110, v110, v9
	v_mul_f32_e32 v111, v111, v9
	v_mov_b32_e32 v21, v10
	v_cvt_pk_fp8_f32 v21, v108, v109
	v_cvt_pk_fp8_f32 v20, v106, v107 op_sel:[0,0,1]
	v_mul_f32_e32 v112, v112, v9
	v_mul_f32_e32 v113, v113, v9
	v_mul_f32_e32 v114, v114, v9
	v_mul_f32_e32 v115, v115, v9
	v_mov_b32_e32 v22, v10
	v_cvt_pk_fp8_f32 v22, v112, v113
	v_cvt_pk_fp8_f32 v21, v110, v111 op_sel:[0,0,1]
	v_mul_f32_e32 v116, v116, v9
	v_mul_f32_e32 v117, v117, v9
	v_mul_f32_e32 v118, v118, v9
	v_mul_f32_e32 v119, v119, v9
	v_mov_b32_e32 v23, v10
	v_cvt_pk_fp8_f32 v23, v116, v117
	v_cvt_pk_fp8_f32 v22, v114, v115 op_sel:[0,0,1]
	v_mul_f32_e32 v120, v120, v9
	v_mul_f32_e32 v121, v121, v9
	v_mul_f32_e32 v122, v122, v9
	v_mul_f32_e32 v123, v123, v9
	v_mov_b32_e32 v24, v10
	v_cvt_pk_fp8_f32 v24, v120, v121
	v_cvt_pk_fp8_f32 v23, v118, v119 op_sel:[0,0,1]
	v_mul_f32_e32 v124, v124, v9
	v_mul_f32_e32 v125, v125, v9
	v_mul_f32_e32 v126, v126, v9
	v_mul_f32_e32 v127, v127, v9
	v_mov_b32_e32 v25, v10
	v_cvt_pk_fp8_f32 v25, v124, v125
	v_cvt_pk_fp8_f32 v24, v122, v123 op_sel:[0,0,1]
	v_mul_f32_e32 v128, v128, v9
	v_mul_f32_e32 v129, v129, v9
	v_mul_f32_e32 v130, v130, v9
	v_mul_f32_e32 v131, v131, v9
	v_mov_b32_e32 v26, v10
	v_cvt_pk_fp8_f32 v26, v128, v129
	v_cvt_pk_fp8_f32 v25, v126, v127 op_sel:[0,0,1]
	v_mul_f32_e32 v132, v132, v9
	v_mul_f32_e32 v133, v133, v9
	v_mul_f32_e32 v134, v134, v9
	v_mul_f32_e32 v135, v135, v9
	v_mov_b32_e32 v27, v10
	v_cvt_pk_fp8_f32 v27, v132, v133
	v_cvt_pk_fp8_f32 v26, v130, v131 op_sel:[0,0,1]
	v_mul_f32_e32 v136, v136, v9
	v_mul_f32_e32 v137, v137, v9
	v_mul_f32_e32 v138, v138, v9
	v_mul_f32_e32 v139, v139, v9
	v_mov_b32_e32 v28, v10
	v_cvt_pk_fp8_f32 v28, v136, v137
	v_cvt_pk_fp8_f32 v27, v134, v135 op_sel:[0,0,1]
	v_mul_f32_e32 v140, v140, v9
	v_mul_f32_e32 v141, v141, v9
	v_mul_f32_e32 v142, v142, v9
	v_mul_f32_e32 v143, v143, v9
	v_mov_b32_e32 v29, v10
	v_cvt_pk_fp8_f32 v29, v140, v141
	v_cvt_pk_fp8_f32 v28, v138, v139 op_sel:[0,0,1]
	v_mul_f32_e32 v144, v144, v9
	v_mul_f32_e32 v145, v145, v9
	v_mul_f32_e32 v146, v146, v9
	v_mul_f32_e32 v147, v147, v9
	v_mov_b32_e32 v30, v10
	v_cvt_pk_fp8_f32 v30, v144, v145
	v_cvt_pk_fp8_f32 v29, v142, v143 op_sel:[0,0,1]
	v_mul_f32_e32 v148, v148, v9
	v_mul_f32_e32 v149, v149, v9
	v_mul_f32_e32 v150, v150, v9
	v_mul_f32_e32 v151, v151, v9
	v_mov_b32_e32 v31, v10
	v_cvt_pk_fp8_f32 v31, v148, v149
	v_cvt_pk_fp8_f32 v30, v146, v147 op_sel:[0,0,1]
	v_mul_f32_e32 v152, v152, v9
	v_mul_f32_e32 v153, v153, v9
	v_mul_f32_e32 v154, v154, v9
	v_mul_f32_e32 v155, v155, v9
	v_mov_b32_e32 v32, v10
	v_cvt_pk_fp8_f32 v32, v152, v153
	v_cvt_pk_fp8_f32 v31, v150, v151 op_sel:[0,0,1]
	v_mul_f32_e32 v156, v156, v9
	v_mul_f32_e32 v157, v157, v9
	v_mul_f32_e32 v158, v158, v9
	v_mul_f32_e32 v159, v159, v9
	v_mov_b32_e32 v33, v10
	v_cvt_pk_fp8_f32 v33, v156, v157
	v_cvt_pk_fp8_f32 v32, v154, v155 op_sel:[0,0,1]
	v_mul_f32_e32 v160, v160, v9
	v_mul_f32_e32 v161, v161, v9
	v_mul_f32_e32 v162, v162, v9
	v_mul_f32_e32 v163, v163, v9
	v_mov_b32_e32 v34, v10
	v_cvt_pk_fp8_f32 v34, v160, v161
	v_cvt_pk_fp8_f32 v33, v158, v159 op_sel:[0,0,1]
	v_mul_f32_e32 v164, v164, v9
	v_mul_f32_e32 v165, v165, v9
	v_mul_f32_e32 v166, v166, v9
	v_mul_f32_e32 v167, v167, v9
	v_mov_b32_e32 v35, v10
	v_cvt_pk_fp8_f32 v35, v164, v165
	v_cvt_pk_fp8_f32 v34, v162, v163 op_sel:[0,0,1]
	v_cvt_pk_fp8_f32 v35, v166, v167 op_sel:[0,0,1]
	s_nop 0
	v_mul_f32_e32 v8, 0x3b800000, v6
	global_store_dword v2, v20, s[8:9]
	global_store_dword v2, v21, s[8:9] offset:256
	global_store_dword v2, v22, s[8:9] offset:512
	global_store_dword v2, v23, s[8:9] offset:768
	global_store_dword v2, v24, s[8:9] offset:1024
	global_store_dword v2, v25, s[8:9] offset:1280
	global_store_dword v2, v26, s[8:9] offset:1536
	global_store_dword v2, v27, s[8:9] offset:1792
	global_store_dword v2, v28, s[8:9] offset:2048
	global_store_dword v2, v29, s[8:9] offset:2304
	global_store_dword v2, v30, s[8:9] offset:2560
	global_store_dword v2, v31, s[8:9] offset:2816
	global_store_dword v2, v32, s[8:9] offset:3072
	global_store_dword v2, v33, s[8:9] offset:3328
	global_store_dword v2, v34, s[8:9] offset:3584
	global_store_dword v2, v35, s[8:9] offset:3840
	s_mov_b64 s[18:19], exec
	s_mov_b64 exec, s[12:13]
	global_store_dword v10, v8, s[10:11]
	s_mov_b64 exec, s[18:19]
	s_waitcnt vmcnt(0)
